# all individually-neutral edits together: branch-free rider block, scalar K base in GQA loops, conv + Fourier-stage-2 load balance, DMA-first GEMM segments, no per-segment setprio
# baseline (speedup 1.0000x reference)
; #define PG8_STAGE(bufoff, gbase, voff) do { _Pragma("unroll") for (int _i = 0; _i < 2; ++_i) \
;         __builtin_amdgcn_global_load_lds((const unsigned*)(wsb + (size_t)(gbase) + (voff)[_i]), (LAS unsigned*)(lds + (bufoff) + ldsw + _i * 8192), 16, 0, 0); } while (0)
; #define PG8_LDA(dst, b, h) do { _Pragma("unroll") for (int m = 0; m < 4; ++m) { if constexpr (FP8) dst##8[m] = PG8_LD8(pa, PG8_SA(b, h) + m * 2048); \
;         else { _Pragma("unroll") for (int k = 0; k < 2; ++k) dst[m][k] = *(const LAS bf16x8*)(pa + PG8_SA(b, h) + m * 2048 + k * 1024); } } } while (0)
; #define PG8_LDB(dst, b, h) do { _Pragma("unroll") for (int n = 0; n < 2; ++n) { if constexpr (FP8) dst##8[n] = PG8_LD8(pb, PG8_SA(b, h) + n * 2048); \
;         else { _Pragma("unroll") for (int k = 0; k < 2; ++k) dst[n][k] = *(const LAS bf16x8*)(pb + PG8_SA(b, h) + n * 2048 + k * 1024); } } } while (0)
; #define PG8_WAIT_V(n) asm volatile("s_waitcnt vmcnt(" #n ")" ::: "memory")
; #define PG8_WAIT_L(n) asm volatile("s_waitcnt lgkmcnt(" #n ")" ::: "memory")
; #define PG8_BAR __builtin_amdgcn_s_barrier()
; #define PG8_SCHED __builtin_amdgcn_sched_barrier(0)
; template <class Epi, class Sched, bool PERM, bool FP8 = false, bool GATHER = false>
; DI void gemm_phase(LAS unsigned char* lds, const unsigned char* wsb, const unsigned lda, const unsigned ldb, const int nt, const Sched& S, const Epi& E) {
;     ...
;             PG8_LDB(B0, 0, 0); PG8_LDB(B1, 0, 1); PG8_SCHED; PG8_LDA(At, 0, 0); PG8_STAGEA(PG8_SA(1, 1), t + 1, 1, false);
;             if constexpr (GATHER) { if (last) {
;                 int tz = tid; asm volatile("" : "+v"(tz));
; #pragma unroll
;                 for (int i = 0; i < 2; ++i) { int R, C; stage_rc(tz * 16 + i * 8192, R, C);
; #pragma unroll
;                     for (int h = 0; h < 2; ++h) { const unsigned tk = (unsigned)tokt[h * HALF + R]; offC[h][i] = (tk < (unsigned)NTOK ? tk : (unsigned)(NTOK - 1)) * lda + (unsigned)C * 2u; } } } }
;             PG8_WAIT_V(8); PG8_WAIT_L(0); PG8_BAR; PG8_MMA(0, 0, At, B0); PG8_MMA(0, 1, At, B1); PG8_BAR; PG8_SCHED;
;             PG8_LDA(At, 0, 1); PG8_STAGE(PG8_SB(0, 0), b2, voffB); PG8_STAGE(PG8_SB(0, 1), b2 + hstepB, voffB); PG8_STAGEA(PG8_SA(0, 0), k2, 0, last);
;             PG8_WAIT_V(8); PG8_WAIT_L(0); PG8_BAR; PG8_MMA(1, 0, At, B0); PG8_MMA(1, 1, At, B1); PG8_BAR; PG8_SCHED;
.LBB0_405:
	s_add_i32 s41, s5, 0xfffe0080
	s_cmp_eq_u32 s7, 4
	s_cselect_b32 s40, s38, s4
	s_cselect_b32 s41, s37, s41
	s_add_i32 s52, s40, 0x80
	s_add_u32 s54, s10, s5
	s_addc_u32 s55, s11, 0
	s_mov_b32 m0, s29
	v_lshl_add_u64 v[206:207], s[54:55], 0, v[154:155]
	global_load_lds_dwordx4 v[206:207], off
	v_lshl_add_u64 v[206:207], s[54:55], 0, v[156:157]
	s_mov_b32 m0, s82
	s_nop 0
	global_load_lds_dwordx4 v[206:207], off
	ds_read_b128 v[130:133], v186
	ds_read_b128 v[134:137], v186 offset:1024
	ds_read_b128 v[138:141], v186 offset:2048
	ds_read_b128 v[142:145], v186 offset:3072
	ds_read_b128 v[146:149], v186 offset:16384
	ds_read_b128 v[150:153], v186 offset:17408
	ds_read_b128 v[160:163], v186 offset:18432
	ds_read_b128 v[164:167], v186 offset:19456
	ds_read_b128 v[168:171], v185
	ds_read_b128 v[172:175], v185 offset:1024
	ds_read_b128 v[176:179], v185 offset:2048
	ds_read_b128 v[180:183], v185 offset:3072
	ds_read_b128 v[190:193], v185 offset:4096
	ds_read_b128 v[194:197], v185 offset:5120
	ds_read_b128 v[198:201], v185 offset:6144
	ds_read_b128 v[202:205], v185 offset:7168
	s_waitcnt vmcnt(8)
	s_waitcnt lgkmcnt(0)
	s_barrier
	s_waitcnt lgkmcnt(0)
	v_mfma_f32_16x16x128_f8f6f4 v[126:129], v[130:137], v[168:175], v[126:129]
	v_mfma_f32_16x16x128_f8f6f4 v[122:125], v[138:145], v[168:175], v[122:125]
	v_mfma_f32_16x16x128_f8f6f4 v[110:113], v[130:137], v[176:183], v[110:113]
	v_mfma_f32_16x16x128_f8f6f4 v[106:109], v[138:145], v[176:183], v[106:109]
	v_mfma_f32_16x16x128_f8f6f4 v[206:209], v[130:137], v[190:197], v[94:97]
	v_mfma_f32_16x16x128_f8f6f4 v[210:213], v[138:145], v[190:197], v[90:93]
	v_mfma_f32_16x16x128_f8f6f4 v[214:217], v[130:137], v[198:205], v[78:81]
	v_mfma_f32_16x16x128_f8f6f4 v[218:221], v[138:145], v[198:205], v[74:77]
	v_mfma_f32_16x16x128_f8f6f4 v[118:121], v[146:153], v[168:175], v[118:121]
	v_mfma_f32_16x16x128_f8f6f4 v[114:117], v[160:167], v[168:175], v[114:117]
	v_mfma_f32_16x16x128_f8f6f4 v[102:105], v[146:153], v[176:183], v[102:105]
	v_mfma_f32_16x16x128_f8f6f4 v[98:101], v[160:167], v[176:183], v[98:101]
	v_mfma_f32_16x16x128_f8f6f4 v[168:171], v[146:153], v[190:197], v[86:89]
	v_mfma_f32_16x16x128_f8f6f4 v[172:175], v[160:167], v[190:197], v[82:85]
	v_mfma_f32_16x16x128_f8f6f4 v[176:179], v[146:153], v[198:205], v[70:73]
	v_mfma_f32_16x16x128_f8f6f4 v[180:183], v[160:167], v[198:205], v[66:69]
	s_barrier
	s_add_u32 s54, s10, s40
	s_addc_u32 s55, s11, 0
	s_mov_b32 m0, s58
	v_lshl_add_u64 v[190:191], s[54:55], 0, v[154:155]
	s_add_i32 s53, s40, 0x20000
	global_load_lds_dwordx4 v[190:191], off
	v_lshl_add_u64 v[190:191], s[54:55], 0, v[156:157]
	s_add_u32 s54, s10, s53
	s_mov_b32 m0, s59
	s_addc_u32 s55, s11, 0
	global_load_lds_dwordx4 v[190:191], off
	v_lshl_add_u64 v[190:191], s[54:55], 0, v[154:155]
	s_mov_b32 m0, s60
	s_nop 0
	global_load_lds_dwordx4 v[190:191], off
	v_lshl_add_u64 v[190:191], s[54:55], 0, v[156:157]
	s_add_u32 s54, s10, s41
	s_mov_b32 m0, s61
	s_addc_u32 s55, s11, 0
	global_load_lds_dwordx4 v[190:191], off
	v_lshl_add_u64 v[190:191], s[54:55], 0, v[154:155]
	s_mov_b32 m0, s57
	s_nop 0
	global_load_lds_dwordx4 v[190:191], off
	v_lshl_add_u64 v[190:191], s[54:55], 0, v[156:157]
	s_mov_b32 m0, s62
	s_nop 0
	global_load_lds_dwordx4 v[190:191], off
	ds_read_b128 v[66:69], v185 offset:16384
	ds_read_b128 v[70:73], v185 offset:17408
	ds_read_b128 v[74:77], v185 offset:18432
	ds_read_b128 v[78:81], v185 offset:19456
	ds_read_b128 v[82:85], v185 offset:20480
	ds_read_b128 v[86:89], v185 offset:21504
	ds_read_b128 v[90:93], v185 offset:22528
	ds_read_b128 v[94:97], v185 offset:23552
	s_waitcnt vmcnt(8)
	s_waitcnt lgkmcnt(0)
	s_barrier
	s_waitcnt lgkmcnt(0)
	v_mfma_f32_16x16x128_f8f6f4 v[62:65], v[130:137], v[66:73], v[62:65]
	v_mfma_f32_16x16x128_f8f6f4 v[58:61], v[138:145], v[66:73], v[58:61]
	v_mfma_f32_16x16x128_f8f6f4 v[190:193], v[130:137], v[74:81], v[46:49]
	v_mfma_f32_16x16x128_f8f6f4 v[194:197], v[138:145], v[74:81], v[42:45]
	v_mfma_f32_16x16x128_f8f6f4 v[198:201], v[130:137], v[82:89], v[30:33]
	v_mfma_f32_16x16x128_f8f6f4 v[202:205], v[138:145], v[82:89], v[26:29]
	v_mfma_f32_16x16x128_f8f6f4 v[222:225], v[130:137], v[90:97], v[14:17]
	v_mfma_f32_16x16x128_f8f6f4 v[226:229], v[138:145], v[90:97], v[10:13]
	v_mfma_f32_16x16x128_f8f6f4 v[54:57], v[146:153], v[66:73], v[54:57]
	v_mfma_f32_16x16x128_f8f6f4 v[50:53], v[160:167], v[66:73], v[50:53]
	v_mfma_f32_16x16x128_f8f6f4 v[230:233], v[146:153], v[74:81], v[38:41]
	v_mfma_f32_16x16x128_f8f6f4 v[234:237], v[160:167], v[74:81], v[34:37]
	v_mfma_f32_16x16x128_f8f6f4 v[238:241], v[146:153], v[82:89], v[22:25]
	v_mfma_f32_16x16x128_f8f6f4 v[242:245], v[160:167], v[82:89], v[18:21]
	v_mfma_f32_16x16x128_f8f6f4 v[246:249], v[146:153], v[90:97], v[6:9]
	v_mfma_f32_16x16x128_f8f6f4 v[250:253], v[160:167], v[90:97], v[2:5]
	s_barrier
; #define PG8_STAGE(bufoff, gbase, voff) do { _Pragma("unroll") for (int _i = 0; _i < 2; ++_i) \
;         __builtin_amdgcn_global_load_lds((const unsigned*)(wsb + (size_t)(gbase) + (voff)[_i]), (LAS unsigned*)(lds + (bufoff) + ldsw + _i * 8192), 16, 0, 0); } while (0)
; #define PG8_LDA(dst, b, h) do { _Pragma("unroll") for (int m = 0; m < 4; ++m) { if constexpr (FP8) dst##8[m] = PG8_LD8(pa, PG8_SA(b, h) + m * 2048); \
;         else { _Pragma("unroll") for (int k = 0; k < 2; ++k) dst[m][k] = *(const LAS bf16x8*)(pa + PG8_SA(b, h) + m * 2048 + k * 1024); } } } while (0)
; #define PG8_LDB(dst, b, h) do { _Pragma("unroll") for (int n = 0; n < 2; ++n) { if constexpr (FP8) dst##8[n] = PG8_LD8(pb, PG8_SA(b, h) + n * 2048); \
;         else { _Pragma("unroll") for (int k = 0; k < 2; ++k) dst[n][k] = *(const LAS bf16x8*)(pb + PG8_SA(b, h) + n * 2048 + k * 1024); } } } while (0)
; #define PG8_WAIT_V(n) asm volatile("s_waitcnt vmcnt(" #n ")" ::: "memory")
; #define PG8_WAIT_L(n) asm volatile("s_waitcnt lgkmcnt(" #n ")" ::: "memory")
; #define PG8_BAR __builtin_amdgcn_s_barrier()
; #define PG8_SCHED __builtin_amdgcn_sched_barrier(0)
; template <class Epi, class Sched, bool PERM, bool FP8 = false, bool GATHER = false>
; DI void gemm_phase(LAS unsigned char* lds, const unsigned char* wsb, const unsigned lda, const unsigned ldb, const int nt, const Sched& S, const Epi& E) {
;     ...
;             PG8_LDB(B0, 1, 0); PG8_LDB(B1, 1, 1); PG8_SCHED; PG8_LDA(At, 1, 0); PG8_STAGEA(PG8_SA(0, 1), k2, 1, last);
;             PG8_WAIT_V(8); PG8_WAIT_L(0); PG8_BAR; PG8_MMA(0, 0, At, B0); PG8_MMA(0, 1, At, B1); PG8_BAR; PG8_SCHED;
;             PG8_LDA(At, 1, 1); PG8_STAGE(PG8_SB(1, 0), b3, voffB); PG8_STAGE(PG8_SB(1, 1), b3 + hstepB, voffB); PG8_STAGEA(PG8_SA(1, 0), k3, 0, last);
;             PG8_WAIT_V(8); PG8_WAIT_L(0); PG8_BAR; PG8_MMA(1, 0, At, B0); PG8_MMA(1, 1, At, B1); PG8_BAR; PG8_SCHED;
;         }
;         if (wr == 0) PG8_BAR;
	s_nop 4
	s_add_i32 s53, s41, 0x20000
	s_add_u32 s54, s10, s53
	s_addc_u32 s55, s11, 0
	s_mov_b32 m0, s63
	v_lshl_add_u64 v[66:67], s[54:55], 0, v[154:155]
	global_load_lds_dwordx4 v[66:67], off
	v_lshl_add_u64 v[66:67], s[54:55], 0, v[156:157]
	s_mov_b32 m0, s64
	s_nop 0
	global_load_lds_dwordx4 v[66:67], off
	ds_read_b128 v[2:5], v186 offset:32768
	ds_read_b128 v[6:9], v186 offset:33792
	ds_read_b128 v[18:21], v186 offset:34816
	ds_read_b128 v[22:25], v186 offset:35840
	ds_read_b128 v[130:133], v186 offset:49152
	ds_read_b128 v[134:137], v186 offset:50176
	ds_read_b128 v[138:141], v186 offset:51200
	ds_read_b128 v[142:145], v186 offset:52224
	ds_read_b128 v[10:13], v185 offset:32768
	ds_read_b128 v[14:17], v185 offset:33792
	ds_read_b128 v[26:29], v185 offset:34816
	ds_read_b128 v[30:33], v185 offset:35840
	ds_read_b128 v[34:37], v185 offset:36864
	ds_read_b128 v[38:41], v185 offset:37888
	ds_read_b128 v[42:45], v185 offset:38912
	ds_read_b128 v[46:49], v185 offset:39936
	s_waitcnt vmcnt(8)
	s_waitcnt lgkmcnt(0)
	s_barrier
	s_waitcnt lgkmcnt(0)
	v_mfma_f32_16x16x128_f8f6f4 v[126:129], v[2:9], v[10:17], v[126:129]
	v_mfma_f32_16x16x128_f8f6f4 v[122:125], v[18:25], v[10:17], v[122:125]
	v_mfma_f32_16x16x128_f8f6f4 v[110:113], v[2:9], v[26:33], v[110:113]
	v_mfma_f32_16x16x128_f8f6f4 v[106:109], v[18:25], v[26:33], v[106:109]
	v_mfma_f32_16x16x128_f8f6f4 v[94:97], v[2:9], v[34:41], v[206:209]
	v_mfma_f32_16x16x128_f8f6f4 v[90:93], v[18:25], v[34:41], v[210:213]
	v_mfma_f32_16x16x128_f8f6f4 v[78:81], v[2:9], v[42:49], v[214:217]
	v_mfma_f32_16x16x128_f8f6f4 v[74:77], v[18:25], v[42:49], v[218:221]
	v_mfma_f32_16x16x128_f8f6f4 v[118:121], v[130:137], v[10:17], v[118:121]
	v_mfma_f32_16x16x128_f8f6f4 v[114:117], v[138:145], v[10:17], v[114:117]
	v_mfma_f32_16x16x128_f8f6f4 v[102:105], v[130:137], v[26:33], v[102:105]
	v_mfma_f32_16x16x128_f8f6f4 v[98:101], v[138:145], v[26:33], v[98:101]
	v_mfma_f32_16x16x128_f8f6f4 v[86:89], v[130:137], v[34:41], v[168:171]
	v_mfma_f32_16x16x128_f8f6f4 v[82:85], v[138:145], v[34:41], v[172:175]
	v_mfma_f32_16x16x128_f8f6f4 v[70:73], v[130:137], v[42:49], v[176:179]
	v_mfma_f32_16x16x128_f8f6f4 v[66:69], v[138:145], v[42:49], v[180:183]
	s_barrier
	s_add_u32 s52, s10, s52
	s_addc_u32 s53, s11, 0
	s_mov_b32 m0, s74
	v_lshl_add_u64 v[10:11], s[52:53], 0, v[154:155]
	s_add_i32 s40, s40, 0x20080
	global_load_lds_dwordx4 v[10:11], off
	v_lshl_add_u64 v[10:11], s[52:53], 0, v[156:157]
	s_add_u32 s52, s10, s40
	s_mov_b32 m0, s75
	s_addc_u32 s53, s11, 0
	s_addk_i32 s41, 0x80
	global_load_lds_dwordx4 v[10:11], off
	v_lshl_add_u64 v[10:11], s[52:53], 0, v[154:155]
	s_mov_b32 m0, s78
	s_add_u32 s40, s10, s41
	global_load_lds_dwordx4 v[10:11], off
	v_lshl_add_u64 v[10:11], s[52:53], 0, v[156:157]
	s_mov_b32 m0, s79
	s_addc_u32 s41, s11, 0
	global_load_lds_dwordx4 v[10:11], off
	v_lshl_add_u64 v[10:11], s[40:41], 0, v[154:155]
	s_mov_b32 m0, s76
	s_nop 0
	global_load_lds_dwordx4 v[10:11], off
	v_lshl_add_u64 v[10:11], s[40:41], 0, v[156:157]
	s_mov_b32 m0, s77
	s_nop 0
	global_load_lds_dwordx4 v[10:11], off
	ds_read_b128 v[34:37], v185 offset:49152
	ds_read_b128 v[38:41], v185 offset:50176
	ds_read_b128 v[146:149], v185 offset:51200
	ds_read_b128 v[150:153], v185 offset:52224
	ds_read_b128 v[160:163], v185 offset:53248
	ds_read_b128 v[164:167], v185 offset:54272
	ds_read_b128 v[168:171], v185 offset:55296
	ds_read_b128 v[172:175], v185 offset:56320
	s_waitcnt vmcnt(8)
	s_waitcnt lgkmcnt(0)
	s_barrier
	s_waitcnt lgkmcnt(0)
	v_mfma_f32_16x16x128_f8f6f4 v[62:65], v[2:9], v[34:41], v[62:65]
	v_mfma_f32_16x16x128_f8f6f4 v[58:61], v[18:25], v[34:41], v[58:61]
	v_mfma_f32_16x16x128_f8f6f4 v[46:49], v[2:9], v[146:153], v[190:193]
	v_mfma_f32_16x16x128_f8f6f4 v[42:45], v[18:25], v[146:153], v[194:197]
	v_mfma_f32_16x16x128_f8f6f4 v[30:33], v[2:9], v[160:167], v[198:201]
	v_mfma_f32_16x16x128_f8f6f4 v[26:29], v[18:25], v[160:167], v[202:205]
	v_mfma_f32_16x16x128_f8f6f4 v[14:17], v[2:9], v[168:175], v[222:225]
	v_mfma_f32_16x16x128_f8f6f4 v[10:13], v[18:25], v[168:175], v[226:229]
	v_mfma_f32_16x16x128_f8f6f4 v[54:57], v[130:137], v[34:41], v[54:57]
	v_mfma_f32_16x16x128_f8f6f4 v[50:53], v[138:145], v[34:41], v[50:53]
	v_mfma_f32_16x16x128_f8f6f4 v[38:41], v[130:137], v[146:153], v[230:233]
	v_mfma_f32_16x16x128_f8f6f4 v[34:37], v[138:145], v[146:153], v[234:237]
	v_mfma_f32_16x16x128_f8f6f4 v[22:25], v[130:137], v[160:167], v[238:241]
	v_mfma_f32_16x16x128_f8f6f4 v[18:21], v[138:145], v[160:167], v[242:245]
	v_mfma_f32_16x16x128_f8f6f4 v[6:9], v[130:137], v[168:175], v[246:249]
	v_mfma_f32_16x16x128_f8f6f4 v[2:5], v[138:145], v[168:175], v[250:253]
	s_barrier
	s_add_i32 s7, s7, 2
	s_addk_i32 s5, 0x100
	s_addk_i32 s4, 0x100
	s_cmp_gt_u32 s7, 5
	s_cbranch_scc0 .LBB0_405
	s_and_b64 vcc, exec, s[14:15]
	s_cbranch_vccz .LBB0_408
	s_barrier

; #define PG8_STAGE(bufoff, gbase, voff) do { _Pragma("unroll") for (int _i = 0; _i < 2; ++_i) \
;         __builtin_amdgcn_global_load_lds((const unsigned*)(wsb + (size_t)(gbase) + (voff)[_i]), (LAS unsigned*)(lds + (bufoff) + ldsw + _i * 8192), 16, 0, 0); } while (0)
; #define PG8_LDA(dst, b, h) do { _Pragma("unroll") for (int m = 0; m < 4; ++m) { if constexpr (FP8) dst##8[m] = PG8_LD8(pa, PG8_SA(b, h) + m * 2048); \
;         else { _Pragma("unroll") for (int k = 0; k < 2; ++k) dst[m][k] = *(const LAS bf16x8*)(pa + PG8_SA(b, h) + m * 2048 + k * 1024); } } } while (0)
; #define PG8_LDB(dst, b, h) do { _Pragma("unroll") for (int n = 0; n < 2; ++n) { if constexpr (FP8) dst##8[n] = PG8_LD8(pb, PG8_SA(b, h) + n * 2048); \
;         else { _Pragma("unroll") for (int k = 0; k < 2; ++k) dst[n][k] = *(const LAS bf16x8*)(pb + PG8_SA(b, h) + n * 2048 + k * 1024); } } } while (0)
; #define PG8_WAIT_V(n) asm volatile("s_waitcnt vmcnt(" #n ")" ::: "memory")
; #define PG8_WAIT_L(n) asm volatile("s_waitcnt lgkmcnt(" #n ")" ::: "memory")
; #define PG8_BAR __builtin_amdgcn_s_barrier()
; #define PG8_SCHED __builtin_amdgcn_sched_barrier(0)
; template <class Epi, class Sched, bool PERM, bool FP8 = false, bool GATHER = false>
; DI void gemm_phase(LAS unsigned char* lds, const unsigned char* wsb, const unsigned lda, const unsigned ldb, const int nt, const Sched& S, const Epi& E) {
;     ...
;             PG8_LDB(B0, 0, 0); PG8_LDB(B1, 0, 1); PG8_SCHED; PG8_LDA(At, 0, 0); PG8_STAGEA(PG8_SA(1, 1), t + 1, 1, false);
;             if constexpr (GATHER) { if (last) {
;                 int tz = tid; asm volatile("" : "+v"(tz));
; #pragma unroll
;                 for (int i = 0; i < 2; ++i) { int R, C; stage_rc(tz * 16 + i * 8192, R, C);
; #pragma unroll
;                     for (int h = 0; h < 2; ++h) { const unsigned tk = (unsigned)tokt[h * HALF + R]; offC[h][i] = (tk < (unsigned)NTOK ? tk : (unsigned)(NTOK - 1)) * lda + (unsigned)C * 2u; } } } }
;             PG8_WAIT_V(8); PG8_WAIT_L(0); PG8_BAR; PG8_MMA(0, 0, At, B0); PG8_MMA(0, 1, At, B1); PG8_BAR; PG8_SCHED;
;             PG8_LDA(At, 0, 1); PG8_STAGE(PG8_SB(0, 0), b2, voffB); PG8_STAGE(PG8_SB(0, 1), b2 + hstepB, voffB); PG8_STAGEA(PG8_SA(0, 0), k2, 0, last);
;             PG8_WAIT_V(8); PG8_WAIT_L(0); PG8_BAR; PG8_MMA(1, 0, At, B0); PG8_MMA(1, 1, At, B1); PG8_BAR; PG8_SCHED;
.LBB0_573:
	s_add_i32 s23, s19, 0xfffe0080
	s_cmp_eq_u32 s20, 4
	s_cselect_b32 s22, s66, s18
	s_cselect_b32 s23, s65, s23
	s_add_i32 s24, s22, 0x80
	s_add_u32 s26, s4, s19
	s_addc_u32 s27, s5, 0
	s_mov_b32 m0, s59
	v_lshl_add_u64 v[130:131], s[26:27], 0, v[136:137]
	global_load_lds_dwordx4 v[130:131], off
	v_lshl_add_u64 v[130:131], s[26:27], 0, v[138:139]
	s_mov_b32 m0, s60
	s_nop 0
	global_load_lds_dwordx4 v[130:131], off
	ds_read_b128 v[144:147], v142
	ds_read_b128 v[148:151], v142 offset:1024
	ds_read_b128 v[152:155], v142 offset:2048
	ds_read_b128 v[156:159], v142 offset:3072
	ds_read_b128 v[160:163], v142 offset:16384
	ds_read_b128 v[164:167], v142 offset:17408
	ds_read_b128 v[168:171], v142 offset:18432
	ds_read_b128 v[172:175], v142 offset:19456
	ds_read_b128 v[176:179], v141
	ds_read_b128 v[180:183], v141 offset:1024
	ds_read_b128 v[184:187], v141 offset:2048
	ds_read_b128 v[188:191], v141 offset:3072
	ds_read_b128 v[192:195], v141 offset:4096
	ds_read_b128 v[196:199], v141 offset:5120
	ds_read_b128 v[200:203], v141 offset:6144
	ds_read_b128 v[204:207], v141 offset:7168
	s_waitcnt vmcnt(8)
	s_waitcnt lgkmcnt(0)
	s_barrier
	s_waitcnt lgkmcnt(0)
	v_mfma_f32_16x16x128_f8f6f4 v[126:129], v[144:151], v[176:183], v[126:129]
	v_mfma_f32_16x16x128_f8f6f4 v[122:125], v[152:159], v[176:183], v[122:125]
	v_mfma_f32_16x16x128_f8f6f4 v[114:117], v[144:151], v[184:191], v[114:117]
	v_mfma_f32_16x16x128_f8f6f4 v[106:109], v[152:159], v[184:191], v[106:109]
	v_mfma_f32_16x16x128_f8f6f4 v[98:101], v[144:151], v[192:199], v[98:101]
	v_mfma_f32_16x16x128_f8f6f4 v[208:211], v[152:159], v[192:199], v[90:93]
	v_mfma_f32_16x16x128_f8f6f4 v[212:215], v[144:151], v[200:207], v[82:85]
	v_mfma_f32_16x16x128_f8f6f4 v[216:219], v[152:159], v[200:207], v[74:77]
	v_mfma_f32_16x16x128_f8f6f4 v[118:121], v[160:167], v[176:183], v[118:121]
	v_mfma_f32_16x16x128_f8f6f4 v[110:113], v[168:175], v[176:183], v[110:113]
	v_mfma_f32_16x16x128_f8f6f4 v[102:105], v[160:167], v[184:191], v[102:105]
	v_mfma_f32_16x16x128_f8f6f4 v[176:179], v[168:175], v[184:191], v[94:97]
	v_mfma_f32_16x16x128_f8f6f4 v[180:183], v[160:167], v[192:199], v[86:89]
	v_mfma_f32_16x16x128_f8f6f4 v[184:187], v[168:175], v[192:199], v[78:81]
	v_mfma_f32_16x16x128_f8f6f4 v[188:191], v[160:167], v[200:207], v[70:73]
	v_mfma_f32_16x16x128_f8f6f4 v[192:195], v[168:175], v[200:207], v[66:69]
	s_barrier
	s_add_u32 s26, s4, s22
	s_addc_u32 s27, s5, 0
	s_mov_b32 m0, s38
	v_lshl_add_u64 v[130:131], s[26:27], 0, v[134:135]
	s_add_i32 s25, s22, 0x20000
	global_load_lds_dwordx4 v[130:131], off
	v_lshl_add_u64 v[130:131], s[26:27], 0, v[252:253]
	s_add_u32 s26, s4, s25
	s_mov_b32 m0, s39
	s_addc_u32 s27, s5, 0
	global_load_lds_dwordx4 v[130:131], off
	v_lshl_add_u64 v[130:131], s[26:27], 0, v[134:135]
	s_mov_b32 m0, s40
	s_nop 0
	global_load_lds_dwordx4 v[130:131], off
	v_lshl_add_u64 v[130:131], s[26:27], 0, v[252:253]
	s_add_u32 s26, s4, s23
	s_mov_b32 m0, s41
	s_addc_u32 s27, s5, 0
	global_load_lds_dwordx4 v[130:131], off
	v_lshl_add_u64 v[130:131], s[26:27], 0, v[136:137]
	s_mov_b32 m0, s29
	s_nop 0
	global_load_lds_dwordx4 v[130:131], off
	v_lshl_add_u64 v[130:131], s[26:27], 0, v[138:139]
	s_mov_b32 m0, s42
	s_nop 0
	global_load_lds_dwordx4 v[130:131], off
	ds_read_b128 v[66:69], v141 offset:16384
	ds_read_b128 v[70:73], v141 offset:17408
	ds_read_b128 v[74:77], v141 offset:18432
	ds_read_b128 v[78:81], v141 offset:19456
	ds_read_b128 v[82:85], v141 offset:20480
	ds_read_b128 v[86:89], v141 offset:21504
	ds_read_b128 v[90:93], v141 offset:22528
	ds_read_b128 v[94:97], v141 offset:23552
	s_waitcnt vmcnt(8)
	s_waitcnt lgkmcnt(0)
	s_barrier
	s_waitcnt lgkmcnt(0)
	v_mfma_f32_16x16x128_f8f6f4 v[62:65], v[144:151], v[66:73], v[62:65]
	v_mfma_f32_16x16x128_f8f6f4 v[58:61], v[152:159], v[66:73], v[58:61]
	v_mfma_f32_16x16x128_f8f6f4 v[50:53], v[144:151], v[74:81], v[50:53]
	v_mfma_f32_16x16x128_f8f6f4 v[196:199], v[152:159], v[74:81], v[42:45]
	v_mfma_f32_16x16x128_f8f6f4 v[200:203], v[144:151], v[82:89], v[34:37]
	v_mfma_f32_16x16x128_f8f6f4 v[204:207], v[152:159], v[82:89], v[26:29]
	v_mfma_f32_16x16x128_f8f6f4 v[220:223], v[144:151], v[90:97], v[18:21]
	v_mfma_f32_16x16x128_f8f6f4 v[224:227], v[152:159], v[90:97], v[10:13]
	v_mfma_f32_16x16x128_f8f6f4 v[54:57], v[160:167], v[66:73], v[54:57]
	v_mfma_f32_16x16x128_f8f6f4 v[228:231], v[168:175], v[66:73], v[46:49]
	v_mfma_f32_16x16x128_f8f6f4 v[232:235], v[160:167], v[74:81], v[38:41]
	v_mfma_f32_16x16x128_f8f6f4 v[236:239], v[168:175], v[74:81], v[30:33]
	v_mfma_f32_16x16x128_f8f6f4 v[240:243], v[160:167], v[82:89], v[22:25]
	v_mfma_f32_16x16x128_f8f6f4 v[244:247], v[168:175], v[82:89], v[14:17]
	v_mfma_f32_16x16x128_f8f6f4 v[248:251], v[160:167], v[90:97], v[6:9]
	v_mfma_f32_16x16x128_f8f6f4 v[130:133], v[168:175], v[90:97], v[2:5]
	s_barrier
; #define PG8_STAGE(bufoff, gbase, voff) do { _Pragma("unroll") for (int _i = 0; _i < 2; ++_i) \
;         __builtin_amdgcn_global_load_lds((const unsigned*)(wsb + (size_t)(gbase) + (voff)[_i]), (LAS unsigned*)(lds + (bufoff) + ldsw + _i * 8192), 16, 0, 0); } while (0)
; #define PG8_LDA(dst, b, h) do { _Pragma("unroll") for (int m = 0; m < 4; ++m) { if constexpr (FP8) dst##8[m] = PG8_LD8(pa, PG8_SA(b, h) + m * 2048); \
;         else { _Pragma("unroll") for (int k = 0; k < 2; ++k) dst[m][k] = *(const LAS bf16x8*)(pa + PG8_SA(b, h) + m * 2048 + k * 1024); } } } while (0)
; #define PG8_LDB(dst, b, h) do { _Pragma("unroll") for (int n = 0; n < 2; ++n) { if constexpr (FP8) dst##8[n] = PG8_LD8(pb, PG8_SA(b, h) + n * 2048); \
;         else { _Pragma("unroll") for (int k = 0; k < 2; ++k) dst[n][k] = *(const LAS bf16x8*)(pb + PG8_SA(b, h) + n * 2048 + k * 1024); } } } while (0)
; #define PG8_WAIT_V(n) asm volatile("s_waitcnt vmcnt(" #n ")" ::: "memory")
; #define PG8_WAIT_L(n) asm volatile("s_waitcnt lgkmcnt(" #n ")" ::: "memory")
; #define PG8_BAR __builtin_amdgcn_s_barrier()
; #define PG8_SCHED __builtin_amdgcn_sched_barrier(0)
; template <class Epi, class Sched, bool PERM, bool FP8 = false, bool GATHER = false>
; DI void gemm_phase(LAS unsigned char* lds, const unsigned char* wsb, const unsigned lda, const unsigned ldb, const int nt, const Sched& S, const Epi& E) {
;     ...
;             PG8_LDB(B0, 1, 0); PG8_LDB(B1, 1, 1); PG8_SCHED; PG8_LDA(At, 1, 0); PG8_STAGEA(PG8_SA(0, 1), k2, 1, last);
;             PG8_WAIT_V(8); PG8_WAIT_L(0); PG8_BAR; PG8_MMA(0, 0, At, B0); PG8_MMA(0, 1, At, B1); PG8_BAR; PG8_SCHED;
;             PG8_LDA(At, 1, 1); PG8_STAGE(PG8_SB(1, 0), b3, voffB); PG8_STAGE(PG8_SB(1, 1), b3 + hstepB, voffB); PG8_STAGEA(PG8_SA(1, 0), k3, 0, last);
;             PG8_WAIT_V(8); PG8_WAIT_L(0); PG8_BAR; PG8_MMA(1, 0, At, B0); PG8_MMA(1, 1, At, B1); PG8_BAR; PG8_SCHED;
;         }
;         if (wr == 0) PG8_BAR;
	s_nop 4
	s_add_i32 s25, s23, 0x20000
	s_add_u32 s26, s4, s25
	s_addc_u32 s27, s5, 0
	s_mov_b32 m0, s43
	v_lshl_add_u64 v[66:67], s[26:27], 0, v[136:137]
	global_load_lds_dwordx4 v[66:67], off
	v_lshl_add_u64 v[66:67], s[26:27], 0, v[138:139]
	s_mov_b32 m0, s44
	s_nop 0
	global_load_lds_dwordx4 v[66:67], off
	ds_read_b128 v[2:5], v142 offset:32768
	ds_read_b128 v[6:9], v142 offset:33792
	ds_read_b128 v[10:13], v142 offset:34816
	ds_read_b128 v[14:17], v142 offset:35840
	ds_read_b128 v[144:147], v142 offset:49152
	ds_read_b128 v[148:151], v142 offset:50176
	ds_read_b128 v[152:155], v142 offset:51200
	ds_read_b128 v[156:159], v142 offset:52224
	ds_read_b128 v[18:21], v141 offset:32768
	ds_read_b128 v[22:25], v141 offset:33792
	ds_read_b128 v[26:29], v141 offset:34816
	ds_read_b128 v[30:33], v141 offset:35840
	ds_read_b128 v[34:37], v141 offset:36864
	ds_read_b128 v[38:41], v141 offset:37888
	ds_read_b128 v[42:45], v141 offset:38912
	ds_read_b128 v[46:49], v141 offset:39936
	s_waitcnt vmcnt(8)
	s_waitcnt lgkmcnt(0)
	s_barrier
	s_waitcnt lgkmcnt(0)
	v_mfma_f32_16x16x128_f8f6f4 v[126:129], v[2:9], v[18:25], v[126:129]
	v_mfma_f32_16x16x128_f8f6f4 v[122:125], v[10:17], v[18:25], v[122:125]
	v_mfma_f32_16x16x128_f8f6f4 v[114:117], v[2:9], v[26:33], v[114:117]
	v_mfma_f32_16x16x128_f8f6f4 v[106:109], v[10:17], v[26:33], v[106:109]
	v_mfma_f32_16x16x128_f8f6f4 v[98:101], v[2:9], v[34:41], v[98:101]
	v_mfma_f32_16x16x128_f8f6f4 v[90:93], v[10:17], v[34:41], v[208:211]
	v_mfma_f32_16x16x128_f8f6f4 v[82:85], v[2:9], v[42:49], v[212:215]
	v_mfma_f32_16x16x128_f8f6f4 v[74:77], v[10:17], v[42:49], v[216:219]
	v_mfma_f32_16x16x128_f8f6f4 v[118:121], v[144:151], v[18:25], v[118:121]
	v_mfma_f32_16x16x128_f8f6f4 v[110:113], v[152:159], v[18:25], v[110:113]
	v_mfma_f32_16x16x128_f8f6f4 v[102:105], v[144:151], v[26:33], v[102:105]
	v_mfma_f32_16x16x128_f8f6f4 v[94:97], v[152:159], v[26:33], v[176:179]
	v_mfma_f32_16x16x128_f8f6f4 v[86:89], v[144:151], v[34:41], v[180:183]
	v_mfma_f32_16x16x128_f8f6f4 v[78:81], v[152:159], v[34:41], v[184:187]
	v_mfma_f32_16x16x128_f8f6f4 v[70:73], v[144:151], v[42:49], v[188:191]
	v_mfma_f32_16x16x128_f8f6f4 v[66:69], v[152:159], v[42:49], v[192:195]
	s_barrier
	s_add_u32 s24, s4, s24
	s_addc_u32 s25, s5, 0
	s_mov_b32 m0, s46
	v_lshl_add_u64 v[18:19], s[24:25], 0, v[134:135]
	s_add_i32 s22, s22, 0x20080
	global_load_lds_dwordx4 v[18:19], off
	v_lshl_add_u64 v[18:19], s[24:25], 0, v[252:253]
	s_add_u32 s24, s4, s22
	s_mov_b32 m0, s47
	s_addc_u32 s25, s5, 0
	s_addk_i32 s23, 0x80
	global_load_lds_dwordx4 v[18:19], off
	v_lshl_add_u64 v[18:19], s[24:25], 0, v[134:135]
	s_mov_b32 m0, s50
	s_add_u32 s22, s4, s23
	global_load_lds_dwordx4 v[18:19], off
	v_lshl_add_u64 v[18:19], s[24:25], 0, v[252:253]
	s_mov_b32 m0, s51
	s_addc_u32 s23, s5, 0
	global_load_lds_dwordx4 v[18:19], off
	v_lshl_add_u64 v[18:19], s[22:23], 0, v[136:137]
	s_mov_b32 m0, s48
	s_nop 0
	global_load_lds_dwordx4 v[18:19], off
	v_lshl_add_u64 v[18:19], s[22:23], 0, v[138:139]
	s_mov_b32 m0, s49
	s_nop 0
	global_load_lds_dwordx4 v[18:19], off
	ds_read_b128 v[160:163], v141 offset:49152
	ds_read_b128 v[164:167], v141 offset:50176
	ds_read_b128 v[168:171], v141 offset:51200
	ds_read_b128 v[172:175], v141 offset:52224
	ds_read_b128 v[176:179], v141 offset:53248
	ds_read_b128 v[180:183], v141 offset:54272
	ds_read_b128 v[184:187], v141 offset:55296
	ds_read_b128 v[188:191], v141 offset:56320
	s_waitcnt vmcnt(8)
	s_waitcnt lgkmcnt(0)
	s_barrier
	s_waitcnt lgkmcnt(0)
	v_mfma_f32_16x16x128_f8f6f4 v[62:65], v[2:9], v[160:167], v[62:65]
	v_mfma_f32_16x16x128_f8f6f4 v[58:61], v[10:17], v[160:167], v[58:61]
	v_mfma_f32_16x16x128_f8f6f4 v[50:53], v[2:9], v[168:175], v[50:53]
	v_mfma_f32_16x16x128_f8f6f4 v[42:45], v[10:17], v[168:175], v[196:199]
	v_mfma_f32_16x16x128_f8f6f4 v[34:37], v[2:9], v[176:183], v[200:203]
	v_mfma_f32_16x16x128_f8f6f4 v[26:29], v[10:17], v[176:183], v[204:207]
	v_mfma_f32_16x16x128_f8f6f4 v[18:21], v[2:9], v[184:191], v[220:223]
	v_mfma_f32_16x16x128_f8f6f4 v[10:13], v[10:17], v[184:191], v[224:227]
	v_mfma_f32_16x16x128_f8f6f4 v[54:57], v[144:151], v[160:167], v[54:57]
	v_mfma_f32_16x16x128_f8f6f4 v[46:49], v[152:159], v[160:167], v[228:231]
	v_mfma_f32_16x16x128_f8f6f4 v[38:41], v[144:151], v[168:175], v[232:235]
	v_mfma_f32_16x16x128_f8f6f4 v[30:33], v[152:159], v[168:175], v[236:239]
	v_mfma_f32_16x16x128_f8f6f4 v[22:25], v[144:151], v[176:183], v[240:243]
	v_mfma_f32_16x16x128_f8f6f4 v[14:17], v[152:159], v[176:183], v[244:247]
	v_mfma_f32_16x16x128_f8f6f4 v[6:9], v[144:151], v[184:191], v[248:251]
	v_mfma_f32_16x16x128_f8f6f4 v[2:5], v[152:159], v[184:191], v[130:133]
	s_barrier
	s_add_i32 s20, s20, 2
	s_addk_i32 s19, 0x100
	s_addk_i32 s18, 0x100
	s_cmp_gt_u32 s20, 5
	s_cbranch_scc0 .LBB0_573
	s_and_b64 vcc, exec, s[12:13]
	s_cbranch_vccz .LBB0_576
	s_barrier

; #define PG8_STAGE(bufoff, gbase, voff) do { _Pragma("unroll") for (int _i = 0; _i < 2; ++_i) \
;         __builtin_amdgcn_global_load_lds((const unsigned*)(wsb + (size_t)(gbase) + (voff)[_i]), (LAS unsigned*)(lds + (bufoff) + ldsw + _i * 8192), 16, 0, 0); } while (0)
; #define PG8_LDA(dst, b, h) do { _Pragma("unroll") for (int m = 0; m < 4; ++m) { if constexpr (FP8) dst##8[m] = PG8_LD8(pa, PG8_SA(b, h) + m * 2048); \
;         else { _Pragma("unroll") for (int k = 0; k < 2; ++k) dst[m][k] = *(const LAS bf16x8*)(pa + PG8_SA(b, h) + m * 2048 + k * 1024); } } } while (0)
; #define PG8_LDB(dst, b, h) do { _Pragma("unroll") for (int n = 0; n < 2; ++n) { if constexpr (FP8) dst##8[n] = PG8_LD8(pb, PG8_SA(b, h) + n * 2048); \
;         else { _Pragma("unroll") for (int k = 0; k < 2; ++k) dst[n][k] = *(const LAS bf16x8*)(pb + PG8_SA(b, h) + n * 2048 + k * 1024); } } } while (0)
; #define PG8_WAIT_V(n) asm volatile("s_waitcnt vmcnt(" #n ")" ::: "memory")
; #define PG8_WAIT_L(n) asm volatile("s_waitcnt lgkmcnt(" #n ")" ::: "memory")
; #define PG8_BAR __builtin_amdgcn_s_barrier()
; #define PG8_SCHED __builtin_amdgcn_sched_barrier(0)
; template <class Epi, class Sched, bool PERM, bool FP8 = false, bool GATHER = false>
; DI void gemm_phase(LAS unsigned char* lds, const unsigned char* wsb, const unsigned lda, const unsigned ldb, const int nt, const Sched& S, const Epi& E) {
;     ...
;             PG8_LDB(B0, 0, 0); PG8_LDB(B1, 0, 1); PG8_SCHED; PG8_LDA(At, 0, 0); PG8_STAGEA(PG8_SA(1, 1), t + 1, 1, false);
;             if constexpr (GATHER) { if (last) {
;                 int tz = tid; asm volatile("" : "+v"(tz));
; #pragma unroll
;                 for (int i = 0; i < 2; ++i) { int R, C; stage_rc(tz * 16 + i * 8192, R, C);
; #pragma unroll
;                     for (int h = 0; h < 2; ++h) { const unsigned tk = (unsigned)tokt[h * HALF + R]; offC[h][i] = (tk < (unsigned)NTOK ? tk : (unsigned)(NTOK - 1)) * lda + (unsigned)C * 2u; } } } }
;             PG8_WAIT_V(8); PG8_WAIT_L(0); PG8_BAR; PG8_MMA(0, 0, At, B0); PG8_MMA(0, 1, At, B1); PG8_BAR; PG8_SCHED;
;             PG8_LDA(At, 0, 1); PG8_STAGE(PG8_SB(0, 0), b2, voffB); PG8_STAGE(PG8_SB(0, 1), b2 + hstepB, voffB); PG8_STAGEA(PG8_SA(0, 0), k2, 0, last);
.LBB0_725:
	s_add_i32 s85, s83, s42
	s_add_u32 s54, s42, 0x100
	s_addc_u32 s55, s43, 0
	s_cmp_eq_u32 s84, 4
	s_cselect_b32 s85, s82, s85
	s_mov_b32 m0, s68
	v_lshl_add_u64 v[142:143], v[140:141], 0, s[42:43]
	global_load_lds_dwordx4 v[142:143], off
	v_lshl_add_u64 v[142:143], v[138:139], 0, s[42:43]
	s_mov_b32 m0, s69
	s_cselect_b32 s43, 0, s54
	global_load_lds_dwordx4 v[142:143], off
	ds_read_b128 v[150:153], v147
	ds_read_b128 v[154:157], v147 offset:1024
	ds_read_b128 v[158:161], v147 offset:2048
	ds_read_b128 v[162:165], v147 offset:3072
	ds_read_b128 v[166:169], v147 offset:16384
	ds_read_b128 v[170:173], v147 offset:17408
	ds_read_b128 v[174:177], v147 offset:18432
	ds_read_b128 v[178:181], v147 offset:19456
	ds_read_b128 v[182:185], v146
	ds_read_b128 v[186:189], v146 offset:1024
	ds_read_b128 v[190:193], v146 offset:2048
	ds_read_b128 v[194:197], v146 offset:3072
	ds_read_b128 v[198:201], v146 offset:4096
	ds_read_b128 v[202:205], v146 offset:5120
	ds_read_b128 v[212:215], v146 offset:6144
	ds_read_b128 v[216:219], v146 offset:7168
	s_waitcnt vmcnt(8)
	s_waitcnt lgkmcnt(0)
	s_add_i32 s42, s85, 0x80
	s_barrier
	s_waitcnt lgkmcnt(0)
	v_mfma_f32_16x16x32_bf16 v[126:129], v[150:153], v[182:185], v[126:129]
	v_mfma_f32_16x16x32_bf16 v[122:125], v[158:161], v[182:185], v[122:125]
	v_mfma_f32_16x16x32_bf16 v[110:113], v[150:153], v[190:193], v[110:113]
	v_mfma_f32_16x16x32_bf16 v[106:109], v[158:161], v[190:193], v[106:109]
	v_mfma_f32_16x16x32_bf16 v[94:97], v[150:153], v[198:201], v[94:97]
	v_mfma_f32_16x16x32_bf16 v[90:93], v[158:161], v[198:201], v[90:93]
	v_mfma_f32_16x16x32_bf16 v[78:81], v[150:153], v[212:215], v[78:81]
	v_mfma_f32_16x16x32_bf16 v[74:77], v[158:161], v[212:215], v[74:77]
	v_mfma_f32_16x16x32_bf16 v[126:129], v[154:157], v[186:189], v[126:129]
	v_mfma_f32_16x16x32_bf16 v[122:125], v[162:165], v[186:189], v[122:125]
	v_mfma_f32_16x16x32_bf16 v[110:113], v[154:157], v[194:197], v[110:113]
	v_mfma_f32_16x16x32_bf16 v[106:109], v[162:165], v[194:197], v[106:109]
	v_mfma_f32_16x16x32_bf16 v[94:97], v[154:157], v[202:205], v[94:97]
	v_mfma_f32_16x16x32_bf16 v[90:93], v[162:165], v[202:205], v[90:93]
	v_mfma_f32_16x16x32_bf16 v[78:81], v[154:157], v[216:219], v[78:81]
	v_mfma_f32_16x16x32_bf16 v[74:77], v[162:165], v[216:219], v[74:77]
	v_mfma_f32_16x16x32_bf16 v[118:121], v[166:169], v[182:185], v[118:121]
	v_mfma_f32_16x16x32_bf16 v[114:117], v[174:177], v[182:185], v[114:117]
	v_mfma_f32_16x16x32_bf16 v[102:105], v[166:169], v[190:193], v[102:105]
	v_mfma_f32_16x16x32_bf16 v[98:101], v[174:177], v[190:193], v[98:101]
	v_mfma_f32_16x16x32_bf16 v[86:89], v[166:169], v[198:201], v[86:89]
	v_mfma_f32_16x16x32_bf16 v[82:85], v[174:177], v[198:201], v[82:85]
	v_mfma_f32_16x16x32_bf16 v[70:73], v[166:169], v[212:215], v[70:73]
	v_mfma_f32_16x16x32_bf16 v[66:69], v[174:177], v[212:215], v[66:69]
	v_mfma_f32_16x16x32_bf16 v[118:121], v[170:173], v[186:189], v[118:121]
	v_mfma_f32_16x16x32_bf16 v[114:117], v[178:181], v[186:189], v[114:117]
	v_mfma_f32_16x16x32_bf16 v[102:105], v[170:173], v[194:197], v[102:105]
	v_mfma_f32_16x16x32_bf16 v[98:101], v[178:181], v[194:197], v[98:101]
	v_mfma_f32_16x16x32_bf16 v[86:89], v[170:173], v[202:205], v[86:89]
	v_mfma_f32_16x16x32_bf16 v[82:85], v[178:181], v[202:205], v[82:85]
	v_mfma_f32_16x16x32_bf16 v[70:73], v[170:173], v[216:219], v[70:73]
	v_mfma_f32_16x16x32_bf16 v[66:69], v[178:181], v[216:219], v[66:69]
	s_barrier
	s_add_u32 s86, s6, s85
	s_addc_u32 s87, s7, 0
	s_mov_b32 m0, s47
	v_lshl_add_u64 v[142:143], s[86:87], 0, v[134:135]
	global_load_lds_dwordx4 v[142:143], off
	v_lshl_add_u64 v[142:143], s[86:87], 0, v[130:131]
	s_add_i32 s86, s85, 0x20000
	s_add_u32 s86, s6, s86
	s_addc_u32 s87, s7, 0
	s_mov_b32 m0, s48
	s_add_u32 s88, s6, s43
	global_load_lds_dwordx4 v[142:143], off
	v_lshl_add_u64 v[142:143], s[86:87], 0, v[134:135]
	s_mov_b32 m0, s49
	s_addc_u32 s89, s7, 0
	global_load_lds_dwordx4 v[142:143], off
	v_lshl_add_u64 v[142:143], s[86:87], 0, v[130:131]
	s_add_u32 s86, s88, 0x1d094000
	s_mov_b32 m0, s56
	s_addc_u32 s87, s89, 0
	global_load_lds_dwordx4 v[142:143], off
	v_lshl_add_u64 v[142:143], s[86:87], 0, v[136:137]
	s_mov_b32 m0, s46
	s_nop 0
	global_load_lds_dwordx4 v[142:143], off
	v_lshl_add_u64 v[142:143], s[86:87], 0, v[132:133]
	s_mov_b32 m0, s57
	s_nop 0
	global_load_lds_dwordx4 v[142:143], off
	ds_read_b128 v[182:185], v146 offset:16384
	ds_read_b128 v[186:189], v146 offset:17408
	ds_read_b128 v[190:193], v146 offset:18432
	ds_read_b128 v[194:197], v146 offset:19456
	ds_read_b128 v[198:201], v146 offset:20480
	ds_read_b128 v[202:205], v146 offset:21504
	ds_read_b128 v[212:215], v146 offset:22528
	ds_read_b128 v[216:219], v146 offset:23552
	s_waitcnt vmcnt(8)
	s_waitcnt lgkmcnt(0)
	s_barrier
; #define PG8_LDA(dst, b, h) do { _Pragma("unroll") for (int m = 0; m < 4; ++m) { if constexpr (FP8) dst##8[m] = PG8_LD8(pa, PG8_SA(b, h) + m * 2048); \
;         else { _Pragma("unroll") for (int k = 0; k < 2; ++k) dst[m][k] = *(const LAS bf16x8*)(pa + PG8_SA(b, h) + m * 2048 + k * 1024); } } } while (0)
; #define PG8_LDB(dst, b, h) do { _Pragma("unroll") for (int n = 0; n < 2; ++n) { if constexpr (FP8) dst##8[n] = PG8_LD8(pb, PG8_SA(b, h) + n * 2048); \
;         else { _Pragma("unroll") for (int k = 0; k < 2; ++k) dst[n][k] = *(const LAS bf16x8*)(pb + PG8_SA(b, h) + n * 2048 + k * 1024); } } } while (0)
; #define PG8_WAIT_V(n) asm volatile("s_waitcnt vmcnt(" #n ")" ::: "memory")
; #define PG8_WAIT_L(n) asm volatile("s_waitcnt lgkmcnt(" #n ")" ::: "memory")
; #define PG8_BAR __builtin_amdgcn_s_barrier()
; #define PG8_SCHED __builtin_amdgcn_sched_barrier(0)
; template <class Epi, class Sched, bool PERM, bool FP8 = false, bool GATHER = false>
; DI void gemm_phase(LAS unsigned char* lds, const unsigned char* wsb, const unsigned lda, const unsigned ldb, const int nt, const Sched& S, const Epi& E) {
;     ...
;             PG8_WAIT_V(8); PG8_WAIT_L(0); PG8_BAR; PG8_MMA(1, 0, At, B0); PG8_MMA(1, 1, At, B1); PG8_BAR; PG8_SCHED;
;             PG8_LDB(B0, 1, 0); PG8_LDB(B1, 1, 1); PG8_SCHED; PG8_LDA(At, 1, 0); PG8_STAGEA(PG8_SA(0, 1), k2, 1, last);
;             PG8_WAIT_V(8); PG8_WAIT_L(0); PG8_BAR; PG8_MMA(0, 0, At, B0); PG8_MMA(0, 1, At, B1); PG8_BAR; PG8_SCHED;
	s_waitcnt lgkmcnt(0)
	v_mfma_f32_16x16x32_bf16 v[62:65], v[150:153], v[182:185], v[62:65]
	v_mfma_f32_16x16x32_bf16 v[58:61], v[158:161], v[182:185], v[58:61]
	v_mfma_f32_16x16x32_bf16 v[46:49], v[150:153], v[190:193], v[46:49]
	v_mfma_f32_16x16x32_bf16 v[42:45], v[158:161], v[190:193], v[42:45]
	v_mfma_f32_16x16x32_bf16 v[30:33], v[150:153], v[198:201], v[30:33]
	v_mfma_f32_16x16x32_bf16 v[26:29], v[158:161], v[198:201], v[26:29]
	v_mfma_f32_16x16x32_bf16 v[14:17], v[150:153], v[212:215], v[14:17]
	v_mfma_f32_16x16x32_bf16 v[10:13], v[158:161], v[212:215], v[10:13]
	v_mfma_f32_16x16x32_bf16 v[62:65], v[154:157], v[186:189], v[62:65]
	v_mfma_f32_16x16x32_bf16 v[58:61], v[162:165], v[186:189], v[58:61]
	v_mfma_f32_16x16x32_bf16 v[46:49], v[154:157], v[194:197], v[46:49]
	v_mfma_f32_16x16x32_bf16 v[42:45], v[162:165], v[194:197], v[42:45]
	v_mfma_f32_16x16x32_bf16 v[30:33], v[154:157], v[202:205], v[30:33]
	v_mfma_f32_16x16x32_bf16 v[26:29], v[162:165], v[202:205], v[26:29]
	v_mfma_f32_16x16x32_bf16 v[14:17], v[154:157], v[216:219], v[14:17]
	v_mfma_f32_16x16x32_bf16 v[10:13], v[162:165], v[216:219], v[10:13]
	v_mfma_f32_16x16x32_bf16 v[54:57], v[166:169], v[182:185], v[54:57]
	v_mfma_f32_16x16x32_bf16 v[50:53], v[174:177], v[182:185], v[50:53]
	v_mfma_f32_16x16x32_bf16 v[38:41], v[166:169], v[190:193], v[38:41]
	v_mfma_f32_16x16x32_bf16 v[34:37], v[174:177], v[190:193], v[34:37]
	v_mfma_f32_16x16x32_bf16 v[22:25], v[166:169], v[198:201], v[22:25]
	v_mfma_f32_16x16x32_bf16 v[18:21], v[174:177], v[198:201], v[18:21]
	v_mfma_f32_16x16x32_bf16 v[6:9], v[166:169], v[212:215], v[6:9]
	v_mfma_f32_16x16x32_bf16 v[2:5], v[174:177], v[212:215], v[2:5]
	v_mfma_f32_16x16x32_bf16 v[54:57], v[170:173], v[186:189], v[54:57]
	v_mfma_f32_16x16x32_bf16 v[50:53], v[178:181], v[186:189], v[50:53]
	v_mfma_f32_16x16x32_bf16 v[38:41], v[170:173], v[194:197], v[38:41]
	v_mfma_f32_16x16x32_bf16 v[34:37], v[178:181], v[194:197], v[34:37]
	v_mfma_f32_16x16x32_bf16 v[22:25], v[170:173], v[202:205], v[22:25]
	v_mfma_f32_16x16x32_bf16 v[18:21], v[178:181], v[202:205], v[18:21]
	v_mfma_f32_16x16x32_bf16 v[6:9], v[170:173], v[216:219], v[6:9]
	v_mfma_f32_16x16x32_bf16 v[2:5], v[178:181], v[216:219], v[2:5]
	s_barrier
	s_add_u32 s86, s88, 0x1d0b4000
	s_addc_u32 s87, s89, 0
	s_mov_b32 m0, s58
	v_lshl_add_u64 v[142:143], s[86:87], 0, v[136:137]
	global_load_lds_dwordx4 v[142:143], off
	v_lshl_add_u64 v[142:143], s[86:87], 0, v[132:133]
	s_mov_b32 m0, s59
	s_nop 0
	global_load_lds_dwordx4 v[142:143], off
	ds_read_b128 v[150:153], v147 offset:32768
	ds_read_b128 v[154:157], v147 offset:33792
	ds_read_b128 v[158:161], v147 offset:34816
	ds_read_b128 v[162:165], v147 offset:35840
	ds_read_b128 v[166:169], v147 offset:49152
	ds_read_b128 v[170:173], v147 offset:50176
	ds_read_b128 v[174:177], v147 offset:51200
	ds_read_b128 v[178:181], v147 offset:52224
	ds_read_b128 v[182:185], v146 offset:32768
	ds_read_b128 v[186:189], v146 offset:33792
	ds_read_b128 v[190:193], v146 offset:34816
	ds_read_b128 v[194:197], v146 offset:35840
	ds_read_b128 v[198:201], v146 offset:36864
	ds_read_b128 v[202:205], v146 offset:37888
	ds_read_b128 v[212:215], v146 offset:38912
	ds_read_b128 v[216:219], v146 offset:39936
	s_waitcnt vmcnt(8)
	s_waitcnt lgkmcnt(0)
	s_barrier
	s_waitcnt lgkmcnt(0)
	v_mfma_f32_16x16x32_bf16 v[126:129], v[150:153], v[182:185], v[126:129]
	v_mfma_f32_16x16x32_bf16 v[122:125], v[158:161], v[182:185], v[122:125]
	v_mfma_f32_16x16x32_bf16 v[110:113], v[150:153], v[190:193], v[110:113]
	v_mfma_f32_16x16x32_bf16 v[106:109], v[158:161], v[190:193], v[106:109]
	v_mfma_f32_16x16x32_bf16 v[94:97], v[150:153], v[198:201], v[94:97]
	v_mfma_f32_16x16x32_bf16 v[90:93], v[158:161], v[198:201], v[90:93]
	v_mfma_f32_16x16x32_bf16 v[78:81], v[150:153], v[212:215], v[78:81]
	v_mfma_f32_16x16x32_bf16 v[74:77], v[158:161], v[212:215], v[74:77]
	v_mfma_f32_16x16x32_bf16 v[126:129], v[154:157], v[186:189], v[126:129]
	v_mfma_f32_16x16x32_bf16 v[122:125], v[162:165], v[186:189], v[122:125]
	v_mfma_f32_16x16x32_bf16 v[110:113], v[154:157], v[194:197], v[110:113]
	v_mfma_f32_16x16x32_bf16 v[106:109], v[162:165], v[194:197], v[106:109]
	v_mfma_f32_16x16x32_bf16 v[94:97], v[154:157], v[202:205], v[94:97]
	v_mfma_f32_16x16x32_bf16 v[90:93], v[162:165], v[202:205], v[90:93]
	v_mfma_f32_16x16x32_bf16 v[78:81], v[154:157], v[216:219], v[78:81]
	v_mfma_f32_16x16x32_bf16 v[74:77], v[162:165], v[216:219], v[74:77]
	v_mfma_f32_16x16x32_bf16 v[118:121], v[166:169], v[182:185], v[118:121]
	v_mfma_f32_16x16x32_bf16 v[114:117], v[174:177], v[182:185], v[114:117]
	v_mfma_f32_16x16x32_bf16 v[102:105], v[166:169], v[190:193], v[102:105]
	v_mfma_f32_16x16x32_bf16 v[98:101], v[174:177], v[190:193], v[98:101]
	v_mfma_f32_16x16x32_bf16 v[86:89], v[166:169], v[198:201], v[86:89]
	v_mfma_f32_16x16x32_bf16 v[82:85], v[174:177], v[198:201], v[82:85]
	v_mfma_f32_16x16x32_bf16 v[70:73], v[166:169], v[212:215], v[70:73]
	v_mfma_f32_16x16x32_bf16 v[66:69], v[174:177], v[212:215], v[66:69]
	v_mfma_f32_16x16x32_bf16 v[118:121], v[170:173], v[186:189], v[118:121]
	v_mfma_f32_16x16x32_bf16 v[114:117], v[178:181], v[186:189], v[114:117]
	v_mfma_f32_16x16x32_bf16 v[102:105], v[170:173], v[194:197], v[102:105]
	v_mfma_f32_16x16x32_bf16 v[98:101], v[178:181], v[194:197], v[98:101]
	v_mfma_f32_16x16x32_bf16 v[86:89], v[170:173], v[202:205], v[86:89]
	v_mfma_f32_16x16x32_bf16 v[82:85], v[178:181], v[202:205], v[82:85]
	v_mfma_f32_16x16x32_bf16 v[70:73], v[170:173], v[216:219], v[70:73]
	v_mfma_f32_16x16x32_bf16 v[66:69], v[178:181], v[216:219], v[66:69]
	s_barrier
; #define PG8_STAGE(bufoff, gbase, voff) do { _Pragma("unroll") for (int _i = 0; _i < 2; ++_i) \
;         __builtin_amdgcn_global_load_lds((const unsigned*)(wsb + (size_t)(gbase) + (voff)[_i]), (LAS unsigned*)(lds + (bufoff) + ldsw + _i * 8192), 16, 0, 0); } while (0)
; #define PG8_LDA(dst, b, h) do { _Pragma("unroll") for (int m = 0; m < 4; ++m) { if constexpr (FP8) dst##8[m] = PG8_LD8(pa, PG8_SA(b, h) + m * 2048); \
;         else { _Pragma("unroll") for (int k = 0; k < 2; ++k) dst[m][k] = *(const LAS bf16x8*)(pa + PG8_SA(b, h) + m * 2048 + k * 1024); } } } while (0)
; #define PG8_WAIT_V(n) asm volatile("s_waitcnt vmcnt(" #n ")" ::: "memory")
; #define PG8_WAIT_L(n) asm volatile("s_waitcnt lgkmcnt(" #n ")" ::: "memory")
; #define PG8_BAR __builtin_amdgcn_s_barrier()
; #define PG8_SCHED __builtin_amdgcn_sched_barrier(0)
; template <class Epi, class Sched, bool PERM, bool FP8 = false, bool GATHER = false>
; DI void gemm_phase(LAS unsigned char* lds, const unsigned char* wsb, const unsigned lda, const unsigned ldb, const int nt, const Sched& S, const Epi& E) {
;     ...
;             PG8_LDA(At, 1, 1); PG8_STAGE(PG8_SB(1, 0), b3, voffB); PG8_STAGE(PG8_SB(1, 1), b3 + hstepB, voffB); PG8_STAGEA(PG8_SA(1, 0), k3, 0, last);
;             PG8_WAIT_V(8); PG8_WAIT_L(0); PG8_BAR; PG8_MMA(1, 0, At, B0); PG8_MMA(1, 1, At, B1); PG8_BAR; PG8_SCHED;
;         }
;         if (wr == 0) PG8_BAR;
	s_add_u32 s42, s6, s42
	s_addc_u32 s43, s7, 0
	s_mov_b32 m0, s60
	v_lshl_add_u64 v[142:143], s[42:43], 0, v[134:135]
	s_add_i32 s85, s85, 0x20080
	global_load_lds_dwordx4 v[142:143], off
	v_lshl_add_u64 v[142:143], s[42:43], 0, v[130:131]
	s_add_u32 s42, s6, s85
	s_mov_b32 m0, s61
	s_addc_u32 s43, s7, 0
	global_load_lds_dwordx4 v[142:143], off
	v_lshl_add_u64 v[142:143], s[42:43], 0, v[134:135]
	s_mov_b32 m0, s65
	s_nop 0
	global_load_lds_dwordx4 v[142:143], off
	v_lshl_add_u64 v[142:143], s[42:43], 0, v[130:131]
	s_add_u32 s42, s88, 0x1d094080
	s_mov_b32 m0, s66
	s_addc_u32 s43, s89, 0
	global_load_lds_dwordx4 v[142:143], off
	v_lshl_add_u64 v[142:143], s[42:43], 0, v[136:137]
	s_mov_b32 m0, s62
	s_nop 0
	global_load_lds_dwordx4 v[142:143], off
	v_lshl_add_u64 v[142:143], s[42:43], 0, v[132:133]
	s_mov_b32 m0, s63
	s_nop 0
	global_load_lds_dwordx4 v[142:143], off
	ds_read_b128 v[182:185], v146 offset:49152
	ds_read_b128 v[186:189], v146 offset:50176
	ds_read_b128 v[190:193], v146 offset:51200
	ds_read_b128 v[194:197], v146 offset:52224
	ds_read_b128 v[198:201], v146 offset:53248
	ds_read_b128 v[202:205], v146 offset:54272
	ds_read_b128 v[212:215], v146 offset:55296
	ds_read_b128 v[216:219], v146 offset:56320
	s_waitcnt vmcnt(8)
	s_waitcnt lgkmcnt(0)
	s_barrier
	s_waitcnt lgkmcnt(0)
	v_mfma_f32_16x16x32_bf16 v[62:65], v[150:153], v[182:185], v[62:65]
	v_mfma_f32_16x16x32_bf16 v[58:61], v[158:161], v[182:185], v[58:61]
	v_mfma_f32_16x16x32_bf16 v[46:49], v[150:153], v[190:193], v[46:49]
	v_mfma_f32_16x16x32_bf16 v[42:45], v[158:161], v[190:193], v[42:45]
	v_mfma_f32_16x16x32_bf16 v[30:33], v[150:153], v[198:201], v[30:33]
	v_mfma_f32_16x16x32_bf16 v[26:29], v[158:161], v[198:201], v[26:29]
	v_mfma_f32_16x16x32_bf16 v[14:17], v[150:153], v[212:215], v[14:17]
	v_mfma_f32_16x16x32_bf16 v[10:13], v[158:161], v[212:215], v[10:13]
	v_mfma_f32_16x16x32_bf16 v[62:65], v[154:157], v[186:189], v[62:65]
	v_mfma_f32_16x16x32_bf16 v[58:61], v[162:165], v[186:189], v[58:61]
	v_mfma_f32_16x16x32_bf16 v[46:49], v[154:157], v[194:197], v[46:49]
	v_mfma_f32_16x16x32_bf16 v[42:45], v[162:165], v[194:197], v[42:45]
	v_mfma_f32_16x16x32_bf16 v[30:33], v[154:157], v[202:205], v[30:33]
	v_mfma_f32_16x16x32_bf16 v[26:29], v[162:165], v[202:205], v[26:29]
	v_mfma_f32_16x16x32_bf16 v[14:17], v[154:157], v[216:219], v[14:17]
	v_mfma_f32_16x16x32_bf16 v[10:13], v[162:165], v[216:219], v[10:13]
	v_mfma_f32_16x16x32_bf16 v[54:57], v[166:169], v[182:185], v[54:57]
	v_mfma_f32_16x16x32_bf16 v[50:53], v[174:177], v[182:185], v[50:53]
	v_mfma_f32_16x16x32_bf16 v[38:41], v[166:169], v[190:193], v[38:41]
	v_mfma_f32_16x16x32_bf16 v[34:37], v[174:177], v[190:193], v[34:37]
	v_mfma_f32_16x16x32_bf16 v[22:25], v[166:169], v[198:201], v[22:25]
	v_mfma_f32_16x16x32_bf16 v[18:21], v[174:177], v[198:201], v[18:21]
	v_mfma_f32_16x16x32_bf16 v[6:9], v[166:169], v[212:215], v[6:9]
	v_mfma_f32_16x16x32_bf16 v[2:5], v[174:177], v[212:215], v[2:5]
	v_mfma_f32_16x16x32_bf16 v[54:57], v[170:173], v[186:189], v[54:57]
	v_mfma_f32_16x16x32_bf16 v[50:53], v[178:181], v[186:189], v[50:53]
	v_mfma_f32_16x16x32_bf16 v[38:41], v[170:173], v[194:197], v[38:41]
	v_mfma_f32_16x16x32_bf16 v[34:37], v[178:181], v[194:197], v[34:37]
	v_mfma_f32_16x16x32_bf16 v[22:25], v[170:173], v[202:205], v[22:25]
	v_mfma_f32_16x16x32_bf16 v[18:21], v[178:181], v[202:205], v[18:21]
	v_mfma_f32_16x16x32_bf16 v[6:9], v[170:173], v[216:219], v[6:9]
	v_mfma_f32_16x16x32_bf16 v[2:5], v[178:181], v[216:219], v[2:5]
	s_barrier
	s_add_i32 s84, s84, 2
	s_cmp_gt_u32 s84, 5
	s_mov_b64 s[42:43], s[54:55]
	s_cbranch_scc0 .LBB0_725
	s_and_b64 vcc, exec, s[10:11]
	s_cbranch_vccz .LBB0_728
	s_barrier

; #define PG8_STAGE(bufoff, gbase, voff) do { _Pragma("unroll") for (int _i = 0; _i < 2; ++_i) \
;         __builtin_amdgcn_global_load_lds((const unsigned*)(wsb + (size_t)(gbase) + (voff)[_i]), (LAS unsigned*)(lds + (bufoff) + ldsw + _i * 8192), 16, 0, 0); } while (0)
; #define PG8_LDA(dst, b, h) do { _Pragma("unroll") for (int m = 0; m < 4; ++m) { if constexpr (FP8) dst##8[m] = PG8_LD8(pa, PG8_SA(b, h) + m * 2048); \
;         else { _Pragma("unroll") for (int k = 0; k < 2; ++k) dst[m][k] = *(const LAS bf16x8*)(pa + PG8_SA(b, h) + m * 2048 + k * 1024); } } } while (0)
; #define PG8_LDB(dst, b, h) do { _Pragma("unroll") for (int n = 0; n < 2; ++n) { if constexpr (FP8) dst##8[n] = PG8_LD8(pb, PG8_SA(b, h) + n * 2048); \
;         else { _Pragma("unroll") for (int k = 0; k < 2; ++k) dst[n][k] = *(const LAS bf16x8*)(pb + PG8_SA(b, h) + n * 2048 + k * 1024); } } } while (0)
; #define PG8_WAIT_V(n) asm volatile("s_waitcnt vmcnt(" #n ")" ::: "memory")
; #define PG8_WAIT_L(n) asm volatile("s_waitcnt lgkmcnt(" #n ")" ::: "memory")
; #define PG8_BAR __builtin_amdgcn_s_barrier()
; #define PG8_SCHED __builtin_amdgcn_sched_barrier(0)
; template <class Epi, class Sched, bool PERM, bool FP8 = false, bool GATHER = false>
; DI void gemm_phase(LAS unsigned char* lds, const unsigned char* wsb, const unsigned lda, const unsigned ldb, const int nt, const Sched& S, const Epi& E) {
;     ...
;             PG8_LDB(B0, 0, 0); PG8_LDB(B1, 0, 1); PG8_SCHED; PG8_LDA(At, 0, 0); PG8_STAGEA(PG8_SA(1, 1), t + 1, 1, false);
;             if constexpr (GATHER) { if (last) {
;                 int tz = tid; asm volatile("" : "+v"(tz));
; #pragma unroll
;                 for (int i = 0; i < 2; ++i) { int R, C; stage_rc(tz * 16 + i * 8192, R, C);
; #pragma unroll
;                     for (int h = 0; h < 2; ++h) { const unsigned tk = (unsigned)tokt[h * HALF + R]; offC[h][i] = (tk < (unsigned)NTOK ? tk : (unsigned)(NTOK - 1)) * lda + (unsigned)C * 2u; } } } }
;             PG8_WAIT_V(8); PG8_WAIT_L(0); PG8_BAR; PG8_MMA(0, 0, At, B0); PG8_MMA(0, 1, At, B1); PG8_BAR; PG8_SCHED;
;             PG8_LDA(At, 0, 1); PG8_STAGE(PG8_SB(0, 0), b2, voffB); PG8_STAGE(PG8_SB(0, 1), b2 + hstepB, voffB); PG8_STAGEA(PG8_SA(0, 0), k2, 0, last);
;             PG8_WAIT_V(8); PG8_WAIT_L(0); PG8_BAR; PG8_MMA(1, 0, At, B0); PG8_MMA(1, 1, At, B1); PG8_BAR; PG8_SCHED;
.LBB0_910:
	s_add_i32 s25, s21, 0xfffe0080
	s_cmp_eq_u32 s23, 4
	s_cselect_b32 s24, s59, s22
	s_cselect_b32 s25, s58, s25
	s_add_i32 s61, s24, 0x80
	s_add_u32 s62, s6, s21
	s_addc_u32 s63, s7, 0
	s_mov_b32 m0, s54
	v_lshl_add_u64 v[158:159], s[62:63], 0, v[148:149]
	global_load_lds_dwordx4 v[158:159], off
	v_lshl_add_u64 v[158:159], s[62:63], 0, v[146:147]
	s_mov_b32 m0, s55
	s_nop 0
	global_load_lds_dwordx4 v[158:159], off
	ds_read_b128 v[130:133], v162
	ds_read_b128 v[134:137], v162 offset:1024
	ds_read_b128 v[138:141], v162 offset:2048
	ds_read_b128 v[142:145], v162 offset:3072
	ds_read_b128 v[150:153], v162 offset:16384
	ds_read_b128 v[154:157], v162 offset:17408
	ds_read_b128 v[164:167], v162 offset:18432
	ds_read_b128 v[168:171], v162 offset:19456
	ds_read_b128 v[172:175], v161
	ds_read_b128 v[176:179], v161 offset:1024
	ds_read_b128 v[180:183], v161 offset:2048
	ds_read_b128 v[184:187], v161 offset:3072
	ds_read_b128 v[188:191], v161 offset:4096
	ds_read_b128 v[192:195], v161 offset:5120
	ds_read_b128 v[196:199], v161 offset:6144
	ds_read_b128 v[200:203], v161 offset:7168
	s_waitcnt vmcnt(8)
	s_waitcnt lgkmcnt(0)
	s_barrier
	s_waitcnt lgkmcnt(0)
	v_mfma_f32_16x16x128_f8f6f4 v[126:129], v[130:137], v[172:179], v[126:129]
	v_mfma_f32_16x16x128_f8f6f4 v[122:125], v[138:145], v[172:179], v[122:125]
	v_mfma_f32_16x16x128_f8f6f4 v[118:121], v[130:137], v[180:187], v[118:121]
	v_mfma_f32_16x16x128_f8f6f4 v[114:117], v[138:145], v[180:187], v[114:117]
	v_mfma_f32_16x16x128_f8f6f4 v[102:105], v[130:137], v[188:195], v[102:105]
	v_mfma_f32_16x16x128_f8f6f4 v[98:101], v[138:145], v[188:195], v[98:101]
	v_mfma_f32_16x16x128_f8f6f4 v[204:207], v[130:137], v[196:203], v[86:89]
	v_mfma_f32_16x16x128_f8f6f4 v[208:211], v[138:145], v[196:203], v[78:81]
	v_mfma_f32_16x16x128_f8f6f4 v[110:113], v[150:157], v[172:179], v[110:113]
	v_mfma_f32_16x16x128_f8f6f4 v[106:109], v[164:171], v[172:179], v[106:109]
	v_mfma_f32_16x16x128_f8f6f4 v[172:175], v[150:157], v[180:187], v[94:97]
	v_mfma_f32_16x16x128_f8f6f4 v[176:179], v[164:171], v[180:187], v[90:93]
	v_mfma_f32_16x16x128_f8f6f4 v[180:183], v[150:157], v[188:195], v[82:85]
	v_mfma_f32_16x16x128_f8f6f4 v[184:187], v[164:171], v[188:195], v[74:77]
	v_mfma_f32_16x16x128_f8f6f4 v[188:191], v[150:157], v[196:203], v[70:73]
	v_mfma_f32_16x16x128_f8f6f4 v[192:195], v[164:171], v[196:203], v[66:69]
	s_barrier
	s_add_u32 s62, s6, s24
	s_addc_u32 s63, s7, 0
	s_mov_b32 m0, s36
	v_lshl_add_u64 v[158:159], s[62:63], 0, v[148:149]
	s_nop 0
	global_load_lds_dwordx4 v[158:159], off
	v_lshl_add_u64 v[158:159], s[62:63], 0, v[146:147]
	s_add_i32 s62, s24, 0x20000
	s_add_u32 s62, s6, s62
	s_mov_b32 m0, s37
	s_addc_u32 s63, s7, 0
	global_load_lds_dwordx4 v[158:159], off
	v_lshl_add_u64 v[158:159], s[62:63], 0, v[148:149]
	s_mov_b32 m0, s38
	s_nop 0
	global_load_lds_dwordx4 v[158:159], off
	v_lshl_add_u64 v[158:159], s[62:63], 0, v[146:147]
	s_add_u32 s62, s6, s25
	s_mov_b32 m0, s39
	s_addc_u32 s63, s7, 0
	global_load_lds_dwordx4 v[158:159], off
	v_lshl_add_u64 v[158:159], s[62:63], 0, v[148:149]
	s_mov_b32 m0, s29
	s_nop 0
	global_load_lds_dwordx4 v[158:159], off
	v_lshl_add_u64 v[158:159], s[62:63], 0, v[146:147]
	s_mov_b32 m0, s40
	s_nop 0
	global_load_lds_dwordx4 v[158:159], off
	ds_read_b128 v[66:69], v161 offset:16384
	ds_read_b128 v[70:73], v161 offset:17408
	ds_read_b128 v[74:77], v161 offset:18432
	ds_read_b128 v[78:81], v161 offset:19456
	ds_read_b128 v[82:85], v161 offset:20480
	ds_read_b128 v[86:89], v161 offset:21504
	ds_read_b128 v[90:93], v161 offset:22528
	ds_read_b128 v[94:97], v161 offset:23552
	s_waitcnt vmcnt(8)
	s_waitcnt lgkmcnt(0)
	s_barrier
	s_waitcnt lgkmcnt(0)
	v_mfma_f32_16x16x128_f8f6f4 v[62:65], v[130:137], v[66:73], v[62:65]
	v_mfma_f32_16x16x128_f8f6f4 v[58:61], v[138:145], v[66:73], v[58:61]
	v_mfma_f32_16x16x128_f8f6f4 v[50:53], v[130:137], v[74:81], v[50:53]
	v_mfma_f32_16x16x128_f8f6f4 v[196:199], v[138:145], v[74:81], v[42:45]
	v_mfma_f32_16x16x128_f8f6f4 v[200:203], v[130:137], v[82:89], v[38:41]
	v_mfma_f32_16x16x128_f8f6f4 v[212:215], v[138:145], v[82:89], v[30:33]
	v_mfma_f32_16x16x128_f8f6f4 v[216:219], v[130:137], v[90:97], v[22:25]
	v_mfma_f32_16x16x128_f8f6f4 v[220:223], v[138:145], v[90:97], v[14:17]
	v_mfma_f32_16x16x128_f8f6f4 v[54:57], v[150:157], v[66:73], v[54:57]
	v_mfma_f32_16x16x128_f8f6f4 v[224:227], v[164:171], v[66:73], v[46:49]
	v_mfma_f32_16x16x128_f8f6f4 v[228:231], v[150:157], v[74:81], v[34:37]
	v_mfma_f32_16x16x128_f8f6f4 v[232:235], v[164:171], v[74:81], v[26:29]
	v_mfma_f32_16x16x128_f8f6f4 v[236:239], v[150:157], v[82:89], v[18:21]
	v_mfma_f32_16x16x128_f8f6f4 v[240:243], v[164:171], v[82:89], v[10:13]
	v_mfma_f32_16x16x128_f8f6f4 v[244:247], v[150:157], v[90:97], v[6:9]
	v_mfma_f32_16x16x128_f8f6f4 v[248:251], v[164:171], v[90:97], v[2:5]
	s_barrier
; #define PG8_STAGE(bufoff, gbase, voff) do { _Pragma("unroll") for (int _i = 0; _i < 2; ++_i) \
;         __builtin_amdgcn_global_load_lds((const unsigned*)(wsb + (size_t)(gbase) + (voff)[_i]), (LAS unsigned*)(lds + (bufoff) + ldsw + _i * 8192), 16, 0, 0); } while (0)
; #define PG8_LDA(dst, b, h) do { _Pragma("unroll") for (int m = 0; m < 4; ++m) { if constexpr (FP8) dst##8[m] = PG8_LD8(pa, PG8_SA(b, h) + m * 2048); \
;         else { _Pragma("unroll") for (int k = 0; k < 2; ++k) dst[m][k] = *(const LAS bf16x8*)(pa + PG8_SA(b, h) + m * 2048 + k * 1024); } } } while (0)
; #define PG8_LDB(dst, b, h) do { _Pragma("unroll") for (int n = 0; n < 2; ++n) { if constexpr (FP8) dst##8[n] = PG8_LD8(pb, PG8_SA(b, h) + n * 2048); \
;         else { _Pragma("unroll") for (int k = 0; k < 2; ++k) dst[n][k] = *(const LAS bf16x8*)(pb + PG8_SA(b, h) + n * 2048 + k * 1024); } } } while (0)
; #define PG8_WAIT_V(n) asm volatile("s_waitcnt vmcnt(" #n ")" ::: "memory")
; #define PG8_WAIT_L(n) asm volatile("s_waitcnt lgkmcnt(" #n ")" ::: "memory")
; #define PG8_BAR __builtin_amdgcn_s_barrier()
; #define PG8_SCHED __builtin_amdgcn_sched_barrier(0)
; template <class Epi, class Sched, bool PERM, bool FP8 = false, bool GATHER = false>
; DI void gemm_phase(LAS unsigned char* lds, const unsigned char* wsb, const unsigned lda, const unsigned ldb, const int nt, const Sched& S, const Epi& E) {
;     ...
;             PG8_LDB(B0, 1, 0); PG8_LDB(B1, 1, 1); PG8_SCHED; PG8_LDA(At, 1, 0); PG8_STAGEA(PG8_SA(0, 1), k2, 1, last);
;             PG8_WAIT_V(8); PG8_WAIT_L(0); PG8_BAR; PG8_MMA(0, 0, At, B0); PG8_MMA(0, 1, At, B1); PG8_BAR; PG8_SCHED;
;             PG8_LDA(At, 1, 1); PG8_STAGE(PG8_SB(1, 0), b3, voffB); PG8_STAGE(PG8_SB(1, 1), b3 + hstepB, voffB); PG8_STAGEA(PG8_SA(1, 0), k3, 0, last);
;             PG8_WAIT_V(8); PG8_WAIT_L(0); PG8_BAR; PG8_MMA(1, 0, At, B0); PG8_MMA(1, 1, At, B1); PG8_BAR; PG8_SCHED;
;         }
;         if (wr == 0) PG8_BAR;
	s_nop 4
	s_add_i32 s62, s25, 0x20000
	s_add_u32 s62, s6, s62
	s_addc_u32 s63, s7, 0
	s_mov_b32 m0, s41
	v_lshl_add_u64 v[66:67], s[62:63], 0, v[148:149]
	global_load_lds_dwordx4 v[66:67], off
	v_lshl_add_u64 v[66:67], s[62:63], 0, v[146:147]
	s_mov_b32 m0, s42
	s_nop 0
	global_load_lds_dwordx4 v[66:67], off
	ds_read_b128 v[2:5], v162 offset:32768
	ds_read_b128 v[6:9], v162 offset:33792
	ds_read_b128 v[10:13], v162 offset:34816
	ds_read_b128 v[14:17], v162 offset:35840
	ds_read_b128 v[130:133], v162 offset:49152
	ds_read_b128 v[134:137], v162 offset:50176
	ds_read_b128 v[138:141], v162 offset:51200
	ds_read_b128 v[142:145], v162 offset:52224
	ds_read_b128 v[18:21], v161 offset:32768
	ds_read_b128 v[22:25], v161 offset:33792
	ds_read_b128 v[26:29], v161 offset:34816
	ds_read_b128 v[30:33], v161 offset:35840
	ds_read_b128 v[34:37], v161 offset:36864
	ds_read_b128 v[38:41], v161 offset:37888
	ds_read_b128 v[42:45], v161 offset:38912
	ds_read_b128 v[46:49], v161 offset:39936
	s_waitcnt vmcnt(8)
	s_waitcnt lgkmcnt(0)
	s_barrier
	s_waitcnt lgkmcnt(0)
	v_mfma_f32_16x16x128_f8f6f4 v[126:129], v[2:9], v[18:25], v[126:129]
	v_mfma_f32_16x16x128_f8f6f4 v[122:125], v[10:17], v[18:25], v[122:125]
	v_mfma_f32_16x16x128_f8f6f4 v[118:121], v[2:9], v[26:33], v[118:121]
	v_mfma_f32_16x16x128_f8f6f4 v[114:117], v[10:17], v[26:33], v[114:117]
	v_mfma_f32_16x16x128_f8f6f4 v[102:105], v[2:9], v[34:41], v[102:105]
	v_mfma_f32_16x16x128_f8f6f4 v[98:101], v[10:17], v[34:41], v[98:101]
	v_mfma_f32_16x16x128_f8f6f4 v[86:89], v[2:9], v[42:49], v[204:207]
	v_mfma_f32_16x16x128_f8f6f4 v[78:81], v[10:17], v[42:49], v[208:211]
	v_mfma_f32_16x16x128_f8f6f4 v[110:113], v[130:137], v[18:25], v[110:113]
	v_mfma_f32_16x16x128_f8f6f4 v[106:109], v[138:145], v[18:25], v[106:109]
	v_mfma_f32_16x16x128_f8f6f4 v[94:97], v[130:137], v[26:33], v[172:175]
	v_mfma_f32_16x16x128_f8f6f4 v[90:93], v[138:145], v[26:33], v[176:179]
	v_mfma_f32_16x16x128_f8f6f4 v[82:85], v[130:137], v[34:41], v[180:183]
	v_mfma_f32_16x16x128_f8f6f4 v[74:77], v[138:145], v[34:41], v[184:187]
	v_mfma_f32_16x16x128_f8f6f4 v[70:73], v[130:137], v[42:49], v[188:191]
	v_mfma_f32_16x16x128_f8f6f4 v[66:69], v[138:145], v[42:49], v[192:195]
	s_barrier
	s_add_u32 s62, s6, s61
	s_addc_u32 s63, s7, 0
	s_mov_b32 m0, s46
	v_lshl_add_u64 v[18:19], s[62:63], 0, v[148:149]
	s_add_i32 s24, s24, 0x20080
	global_load_lds_dwordx4 v[18:19], off
	v_lshl_add_u64 v[18:19], s[62:63], 0, v[146:147]
	s_add_u32 s62, s6, s24
	s_mov_b32 m0, s47
	s_addc_u32 s63, s7, 0
	s_addk_i32 s25, 0x80
	global_load_lds_dwordx4 v[18:19], off
	v_lshl_add_u64 v[18:19], s[62:63], 0, v[148:149]
	s_mov_b32 m0, s50
	s_add_u32 s24, s6, s25
	global_load_lds_dwordx4 v[18:19], off
	v_lshl_add_u64 v[18:19], s[62:63], 0, v[146:147]
	s_mov_b32 m0, s51
	s_addc_u32 s25, s7, 0
	global_load_lds_dwordx4 v[18:19], off
	v_lshl_add_u64 v[18:19], s[24:25], 0, v[148:149]
	s_mov_b32 m0, s48
	s_nop 0
	global_load_lds_dwordx4 v[18:19], off
	v_lshl_add_u64 v[18:19], s[24:25], 0, v[146:147]
	s_mov_b32 m0, s49
	s_nop 0
	global_load_lds_dwordx4 v[18:19], off
	ds_read_b128 v[150:153], v161 offset:49152
	ds_read_b128 v[154:157], v161 offset:50176
	ds_read_b128 v[164:167], v161 offset:51200
	ds_read_b128 v[168:171], v161 offset:52224
	ds_read_b128 v[172:175], v161 offset:53248
	ds_read_b128 v[176:179], v161 offset:54272
	ds_read_b128 v[180:183], v161 offset:55296
	ds_read_b128 v[184:187], v161 offset:56320
	s_waitcnt vmcnt(8)
	s_waitcnt lgkmcnt(0)
	s_barrier
	s_waitcnt lgkmcnt(0)
	v_mfma_f32_16x16x128_f8f6f4 v[62:65], v[2:9], v[150:157], v[62:65]
	v_mfma_f32_16x16x128_f8f6f4 v[58:61], v[10:17], v[150:157], v[58:61]
	v_mfma_f32_16x16x128_f8f6f4 v[50:53], v[2:9], v[164:171], v[50:53]
	v_mfma_f32_16x16x128_f8f6f4 v[42:45], v[10:17], v[164:171], v[196:199]
	v_mfma_f32_16x16x128_f8f6f4 v[38:41], v[2:9], v[172:179], v[200:203]
	v_mfma_f32_16x16x128_f8f6f4 v[30:33], v[10:17], v[172:179], v[212:215]
	v_mfma_f32_16x16x128_f8f6f4 v[22:25], v[2:9], v[180:187], v[216:219]
	v_mfma_f32_16x16x128_f8f6f4 v[14:17], v[10:17], v[180:187], v[220:223]
	v_mfma_f32_16x16x128_f8f6f4 v[54:57], v[130:137], v[150:157], v[54:57]
	v_mfma_f32_16x16x128_f8f6f4 v[46:49], v[138:145], v[150:157], v[224:227]
	v_mfma_f32_16x16x128_f8f6f4 v[34:37], v[130:137], v[164:171], v[228:231]
	v_mfma_f32_16x16x128_f8f6f4 v[26:29], v[138:145], v[164:171], v[232:235]
	v_mfma_f32_16x16x128_f8f6f4 v[18:21], v[130:137], v[172:179], v[236:239]
	v_mfma_f32_16x16x128_f8f6f4 v[10:13], v[138:145], v[172:179], v[240:243]
	v_mfma_f32_16x16x128_f8f6f4 v[6:9], v[130:137], v[180:187], v[244:247]
	v_mfma_f32_16x16x128_f8f6f4 v[2:5], v[138:145], v[180:187], v[248:251]
	s_barrier
	s_add_i32 s23, s23, 2
	s_addk_i32 s21, 0x100
	s_addk_i32 s22, 0x100
	s_cmp_gt_u32 s23, 5
	s_cbranch_scc0 .LBB0_910
	s_and_b64 vcc, exec, s[10:11]
	s_cbranch_vccz .LBB0_913
	s_barrier

; #define PG8_STAGE(bufoff, gbase, voff) do { _Pragma("unroll") for (int _i = 0; _i < 2; ++_i) \
;         __builtin_amdgcn_global_load_lds((const unsigned*)(wsb + (size_t)(gbase) + (voff)[_i]), (LAS unsigned*)(lds + (bufoff) + ldsw + _i * 8192), 16, 0, 0); } while (0)
; #define PG8_LDA(dst, b, h) do { _Pragma("unroll") for (int m = 0; m < 4; ++m) { if constexpr (FP8) dst##8[m] = PG8_LD8(pa, PG8_SA(b, h) + m * 2048); \
;         else { _Pragma("unroll") for (int k = 0; k < 2; ++k) dst[m][k] = *(const LAS bf16x8*)(pa + PG8_SA(b, h) + m * 2048 + k * 1024); } } } while (0)
; #define PG8_WAIT_V(n) asm volatile("s_waitcnt vmcnt(" #n ")" ::: "memory")
; #define PG8_WAIT_L(n) asm volatile("s_waitcnt lgkmcnt(" #n ")" ::: "memory")
; #define PG8_BAR __builtin_amdgcn_s_barrier()
; #define PG8_SCHED __builtin_amdgcn_sched_barrier(0)
; template <class Epi, class Sched, bool PERM, bool FP8 = false, bool GATHER = false>
; DI void gemm_phase(LAS unsigned char* lds, const unsigned char* wsb, const unsigned lda, const unsigned ldb, const int nt, const Sched& S, const Epi& E) {
;     ...
;             PG8_WAIT_V(8); PG8_WAIT_L(0); PG8_BAR; PG8_MMA(0, 0, At, B0); PG8_MMA(0, 1, At, B1); PG8_BAR; PG8_SCHED;
;             PG8_LDA(At, 0, 1); PG8_STAGE(PG8_SB(0, 0), b2, voffB); PG8_STAGE(PG8_SB(0, 1), b2 + hstepB, voffB); PG8_STAGEA(PG8_SA(0, 0), k2, 0, last);
;             PG8_WAIT_V(8); PG8_WAIT_L(0); PG8_BAR; PG8_MMA(1, 0, At, B0); PG8_MMA(1, 1, At, B1); PG8_BAR; PG8_SCHED;
.LBB0_1342:
	s_waitcnt vmcnt(8)
	s_add_i32 s85, s83, s50
	s_waitcnt lgkmcnt(0)
	s_and_b64 s[86:87], s[52:53], exec
	s_cselect_b32 s85, s14, s85
	v_mov_b32_e32 v205, v197
	s_add_i32 s86, s85, 0x80
	s_barrier
	s_waitcnt lgkmcnt(0)
	v_mfma_f32_16x16x128_f8f6f4 v[190:193], v[18:25], v[58:65], v[190:193]
	v_mfma_f32_16x16x128_f8f6f4 v[186:189], v[26:33], v[58:65], v[186:189]
	v_mfma_f32_16x16x128_f8f6f4 v[174:177], v[18:25], v[50:57], v[174:177]
	v_mfma_f32_16x16x128_f8f6f4 v[166:169], v[26:33], v[50:57], v[166:169]
	v_mfma_f32_16x16x128_f8f6f4 v[158:161], v[18:25], v[42:49], v[158:161]
	v_mfma_f32_16x16x128_f8f6f4 v[150:153], v[26:33], v[42:49], v[150:153]
	v_mfma_f32_16x16x128_f8f6f4 v[142:145], v[18:25], v[34:41], v[142:145]
	v_mfma_f32_16x16x128_f8f6f4 v[134:137], v[26:33], v[34:41], v[134:137]
	v_mfma_f32_16x16x128_f8f6f4 v[182:185], v[2:9], v[58:65], v[182:185]
	v_mfma_f32_16x16x128_f8f6f4 v[178:181], v[10:17], v[58:65], v[178:181]
	v_mfma_f32_16x16x128_f8f6f4 v[170:173], v[2:9], v[50:57], v[170:173]
	v_mfma_f32_16x16x128_f8f6f4 v[162:165], v[10:17], v[50:57], v[162:165]
	v_mfma_f32_16x16x128_f8f6f4 v[154:157], v[2:9], v[42:49], v[154:157]
	v_mfma_f32_16x16x128_f8f6f4 v[146:149], v[10:17], v[42:49], v[146:149]
	v_mfma_f32_16x16x128_f8f6f4 v[138:141], v[2:9], v[34:41], v[138:141]
	v_mfma_f32_16x16x128_f8f6f4 v[130:133], v[10:17], v[34:41], v[130:133]
	s_barrier
	s_add_u32 s88, s10, s85
	s_addc_u32 s89, s11, 0
	s_mov_b32 m0, s41
	v_lshl_add_u64 v[214:215], s[88:89], 0, v[198:199]
	s_add_i32 s87, s85, 0x20000
	global_load_lds_dwordx4 v[214:215], off
	v_lshl_add_u64 v[214:215], s[88:89], 0, v[200:201]
	s_add_u32 s88, s10, s87
	s_addc_u32 s89, s11, 0
	s_add_u32 s50, s50, 0x100
	s_addc_u32 s51, s51, 0
	s_mov_b32 m0, s46
	s_and_b64 s[52:53], s[52:53], exec
	global_load_lds_dwordx4 v[214:215], off
	v_lshl_add_u64 v[214:215], s[88:89], 0, v[198:199]
	s_mov_b32 m0, s47
	s_cselect_b32 s87, 0, s50
	global_load_lds_dwordx4 v[214:215], off
	v_lshl_add_u64 v[214:215], s[88:89], 0, v[200:201]
	s_mov_b32 m0, s54
	s_add_u32 s52, s12, s87
	global_load_lds_dwordx4 v[214:215], off
	s_addc_u32 s53, s13, 0
	s_mov_b32 m0, s39
	s_nop 0
	global_load_lds_dwordx4 v212, s[52:53]
	s_mov_b32 m0, s55
	s_nop 0
	global_load_lds_dwordx4 v202, s[52:53]
	ds_read_b128 v[34:37], v209 offset:16384
	ds_read_b128 v[38:41], v209 offset:17408
	ds_read_b128 v[42:45], v209 offset:18432
	ds_read_b128 v[46:49], v209 offset:19456
	ds_read_b128 v[50:53], v209 offset:20480
	ds_read_b128 v[54:57], v209 offset:21504
	ds_read_b128 v[58:61], v209 offset:22528
	ds_read_b128 v[62:65], v209 offset:23552
	s_waitcnt vmcnt(8)
	s_waitcnt lgkmcnt(0)
	s_barrier
	s_waitcnt lgkmcnt(0)
	v_mfma_f32_16x16x128_f8f6f4 v[126:129], v[18:25], v[34:41], v[126:129]
	v_mfma_f32_16x16x128_f8f6f4 v[118:121], v[26:33], v[34:41], v[118:121]
	v_mfma_f32_16x16x128_f8f6f4 v[110:113], v[18:25], v[42:49], v[110:113]
	v_mfma_f32_16x16x128_f8f6f4 v[102:105], v[26:33], v[42:49], v[102:105]
	v_mfma_f32_16x16x128_f8f6f4 v[94:97], v[18:25], v[50:57], v[94:97]
	v_mfma_f32_16x16x128_f8f6f4 v[86:89], v[26:33], v[50:57], v[86:89]
	v_mfma_f32_16x16x128_f8f6f4 v[78:81], v[18:25], v[58:65], v[78:81]
	v_mfma_f32_16x16x128_f8f6f4 v[70:73], v[26:33], v[58:65], v[70:73]
	v_mfma_f32_16x16x128_f8f6f4 v[122:125], v[2:9], v[34:41], v[122:125]
	v_mfma_f32_16x16x128_f8f6f4 v[114:117], v[10:17], v[34:41], v[114:117]
	v_mfma_f32_16x16x128_f8f6f4 v[106:109], v[2:9], v[42:49], v[106:109]
	v_mfma_f32_16x16x128_f8f6f4 v[98:101], v[10:17], v[42:49], v[98:101]
	v_mfma_f32_16x16x128_f8f6f4 v[90:93], v[2:9], v[50:57], v[90:93]
	v_mfma_f32_16x16x128_f8f6f4 v[82:85], v[10:17], v[50:57], v[82:85]
	v_mfma_f32_16x16x128_f8f6f4 v[74:77], v[2:9], v[58:65], v[74:77]
	v_mfma_f32_16x16x128_f8f6f4 v[66:69], v[10:17], v[58:65], v[66:69]
	s_barrier
; #define PG8_STAGE(bufoff, gbase, voff) do { _Pragma("unroll") for (int _i = 0; _i < 2; ++_i) \
;         __builtin_amdgcn_global_load_lds((const unsigned*)(wsb + (size_t)(gbase) + (voff)[_i]), (LAS unsigned*)(lds + (bufoff) + ldsw + _i * 8192), 16, 0, 0); } while (0)
; #define PG8_LDA(dst, b, h) do { _Pragma("unroll") for (int m = 0; m < 4; ++m) { if constexpr (FP8) dst##8[m] = PG8_LD8(pa, PG8_SA(b, h) + m * 2048); \
;         else { _Pragma("unroll") for (int k = 0; k < 2; ++k) dst[m][k] = *(const LAS bf16x8*)(pa + PG8_SA(b, h) + m * 2048 + k * 1024); } } } while (0)
; #define PG8_LDB(dst, b, h) do { _Pragma("unroll") for (int n = 0; n < 2; ++n) { if constexpr (FP8) dst##8[n] = PG8_LD8(pb, PG8_SA(b, h) + n * 2048); \
;         else { _Pragma("unroll") for (int k = 0; k < 2; ++k) dst[n][k] = *(const LAS bf16x8*)(pb + PG8_SA(b, h) + n * 2048 + k * 1024); } } } while (0)
; #define PG8_WAIT_V(n) asm volatile("s_waitcnt vmcnt(" #n ")" ::: "memory")
; #define PG8_WAIT_L(n) asm volatile("s_waitcnt lgkmcnt(" #n ")" ::: "memory")
; #define PG8_BAR __builtin_amdgcn_s_barrier()
; #define PG8_SCHED __builtin_amdgcn_sched_barrier(0)
; template <class Epi, class Sched, bool PERM, bool FP8 = false, bool GATHER = false>
; DI void gemm_phase(LAS unsigned char* lds, const unsigned char* wsb, const unsigned lda, const unsigned ldb, const int nt, const Sched& S, const Epi& E) {
;     ...
;             PG8_LDB(B0, 1, 0); PG8_LDB(B1, 1, 1); PG8_SCHED; PG8_LDA(At, 1, 0); PG8_STAGEA(PG8_SA(0, 1), k2, 1, last);
;             PG8_WAIT_V(8); PG8_WAIT_L(0); PG8_BAR; PG8_MMA(0, 0, At, B0); PG8_MMA(0, 1, At, B1); PG8_BAR; PG8_SCHED;
;             PG8_LDA(At, 1, 1); PG8_STAGE(PG8_SB(1, 0), b3, voffB); PG8_STAGE(PG8_SB(1, 1), b3 + hstepB, voffB); PG8_STAGEA(PG8_SA(1, 0), k3, 0, last);
;             PG8_WAIT_V(8); PG8_WAIT_L(0); PG8_BAR; PG8_MMA(1, 0, At, B0); PG8_MMA(1, 1, At, B1); PG8_BAR; PG8_SCHED;
;         }
;         if (wr == 0) PG8_BAR;
	s_mov_b32 m0, s56
	v_lshl_add_u64 v[214:215], s[52:53], 0, v[196:197]
	global_load_lds_dwordx4 v[214:215], off
	v_lshl_add_u64 v[214:215], s[52:53], 0, v[204:205]
	s_mov_b32 m0, s57
	s_nop 0
	global_load_lds_dwordx4 v[214:215], off
	ds_read_b128 v[2:5], v210 offset:32768
	ds_read_b128 v[6:9], v210 offset:33792
	ds_read_b128 v[10:13], v210 offset:34816
	ds_read_b128 v[14:17], v210 offset:35840
	ds_read_b128 v[18:21], v210 offset:49152
	ds_read_b128 v[22:25], v210 offset:50176
	ds_read_b128 v[26:29], v210 offset:51200
	ds_read_b128 v[30:33], v210 offset:52224
	ds_read_b128 v[34:37], v209 offset:32768
	ds_read_b128 v[38:41], v209 offset:33792
	ds_read_b128 v[42:45], v209 offset:34816
	ds_read_b128 v[46:49], v209 offset:35840
	ds_read_b128 v[50:53], v209 offset:36864
	ds_read_b128 v[54:57], v209 offset:37888
	ds_read_b128 v[58:61], v209 offset:38912
	ds_read_b128 v[62:65], v209 offset:39936
	s_waitcnt vmcnt(8)
	s_waitcnt lgkmcnt(0)
	s_barrier
	s_waitcnt lgkmcnt(0)
	v_mfma_f32_16x16x128_f8f6f4 v[190:193], v[2:9], v[34:41], v[190:193]
	v_mfma_f32_16x16x128_f8f6f4 v[186:189], v[10:17], v[34:41], v[186:189]
	v_mfma_f32_16x16x128_f8f6f4 v[174:177], v[2:9], v[42:49], v[174:177]
	v_mfma_f32_16x16x128_f8f6f4 v[166:169], v[10:17], v[42:49], v[166:169]
	v_mfma_f32_16x16x128_f8f6f4 v[158:161], v[2:9], v[50:57], v[158:161]
	v_mfma_f32_16x16x128_f8f6f4 v[150:153], v[10:17], v[50:57], v[150:153]
	v_mfma_f32_16x16x128_f8f6f4 v[142:145], v[2:9], v[58:65], v[142:145]
	v_mfma_f32_16x16x128_f8f6f4 v[134:137], v[10:17], v[58:65], v[134:137]
	v_mfma_f32_16x16x128_f8f6f4 v[182:185], v[18:25], v[34:41], v[182:185]
	v_mfma_f32_16x16x128_f8f6f4 v[178:181], v[26:33], v[34:41], v[178:181]
	v_mfma_f32_16x16x128_f8f6f4 v[170:173], v[18:25], v[42:49], v[170:173]
	v_mfma_f32_16x16x128_f8f6f4 v[162:165], v[26:33], v[42:49], v[162:165]
	v_mfma_f32_16x16x128_f8f6f4 v[154:157], v[18:25], v[50:57], v[154:157]
	v_mfma_f32_16x16x128_f8f6f4 v[146:149], v[26:33], v[50:57], v[146:149]
	v_mfma_f32_16x16x128_f8f6f4 v[138:141], v[18:25], v[58:65], v[138:141]
	v_mfma_f32_16x16x128_f8f6f4 v[130:133], v[26:33], v[58:65], v[130:133]
	s_barrier
	s_add_u32 s52, s10, s86
	s_addc_u32 s53, s11, 0
	s_mov_b32 m0, s61
	v_lshl_add_u64 v[214:215], s[52:53], 0, v[198:199]
	s_add_i32 s85, s85, 0x20080
	global_load_lds_dwordx4 v[214:215], off
	v_lshl_add_u64 v[214:215], s[52:53], 0, v[200:201]
	s_add_u32 s52, s10, s85
	s_mov_b32 m0, s63
	s_addc_u32 s53, s11, 0
	global_load_lds_dwordx4 v[214:215], off
	v_lshl_add_u64 v[214:215], s[52:53], 0, v[198:199]
	s_mov_b32 m0, s66
	s_nop 0
	global_load_lds_dwordx4 v[214:215], off
	v_lshl_add_u64 v[214:215], s[52:53], 0, v[200:201]
	s_add_u32 s52, s10, s87
	s_addc_u32 s53, s11, 0
	s_mov_b32 m0, s67
	s_add_u32 s52, s52, 0x5b9d4080
	global_load_lds_dwordx4 v[214:215], off
	s_addc_u32 s53, s53, 0
	s_mov_b32 m0, s64
	s_nop 0
	global_load_lds_dwordx4 v212, s[52:53]
	s_mov_b32 m0, s65
	s_nop 0
	global_load_lds_dwordx4 v202, s[52:53]
	ds_read_b128 v[34:37], v209 offset:49152
	ds_read_b128 v[38:41], v209 offset:50176
	ds_read_b128 v[42:45], v209 offset:51200
	ds_read_b128 v[46:49], v209 offset:52224
	ds_read_b128 v[50:53], v209 offset:53248
	ds_read_b128 v[54:57], v209 offset:54272
	ds_read_b128 v[58:61], v209 offset:55296
	ds_read_b128 v[62:65], v209 offset:56320
	s_waitcnt vmcnt(8)
	s_waitcnt lgkmcnt(0)
	s_barrier
	s_waitcnt lgkmcnt(0)
	v_mfma_f32_16x16x128_f8f6f4 v[126:129], v[2:9], v[34:41], v[126:129]
	v_mfma_f32_16x16x128_f8f6f4 v[118:121], v[10:17], v[34:41], v[118:121]
	v_mfma_f32_16x16x128_f8f6f4 v[110:113], v[2:9], v[42:49], v[110:113]
	v_mfma_f32_16x16x128_f8f6f4 v[102:105], v[10:17], v[42:49], v[102:105]
	v_mfma_f32_16x16x128_f8f6f4 v[94:97], v[2:9], v[50:57], v[94:97]
	v_mfma_f32_16x16x128_f8f6f4 v[86:89], v[10:17], v[50:57], v[86:89]
	v_mfma_f32_16x16x128_f8f6f4 v[78:81], v[2:9], v[58:65], v[78:81]
	v_mfma_f32_16x16x128_f8f6f4 v[70:73], v[10:17], v[58:65], v[70:73]
	v_mfma_f32_16x16x128_f8f6f4 v[122:125], v[18:25], v[34:41], v[122:125]
	v_mfma_f32_16x16x128_f8f6f4 v[114:117], v[26:33], v[34:41], v[114:117]
	v_mfma_f32_16x16x128_f8f6f4 v[106:109], v[18:25], v[42:49], v[106:109]
	v_mfma_f32_16x16x128_f8f6f4 v[98:101], v[26:33], v[42:49], v[98:101]
	v_mfma_f32_16x16x128_f8f6f4 v[90:93], v[18:25], v[50:57], v[90:93]
	v_mfma_f32_16x16x128_f8f6f4 v[82:85], v[26:33], v[50:57], v[82:85]
	v_mfma_f32_16x16x128_f8f6f4 v[74:77], v[18:25], v[58:65], v[74:77]
	v_mfma_f32_16x16x128_f8f6f4 v[66:69], v[26:33], v[58:65], v[66:69]
	s_barrier
	s_add_i32 s84, s84, 2
	s_cmp_gt_u32 s84, 5
	s_cbranch_scc1 .LBB0_1345

; #define PG8_STAGE(bufoff, gbase, voff) do { _Pragma("unroll") for (int _i = 0; _i < 2; ++_i) \
;         __builtin_amdgcn_global_load_lds((const unsigned*)(wsb + (size_t)(gbase) + (voff)[_i]), (LAS unsigned*)(lds + (bufoff) + ldsw + _i * 8192), 16, 0, 0); } while (0)
; #define PG8_LDA(dst, b, h) do { _Pragma("unroll") for (int m = 0; m < 4; ++m) { if constexpr (FP8) dst##8[m] = PG8_LD8(pa, PG8_SA(b, h) + m * 2048); \
;         else { _Pragma("unroll") for (int k = 0; k < 2; ++k) dst[m][k] = *(const LAS bf16x8*)(pa + PG8_SA(b, h) + m * 2048 + k * 1024); } } } while (0)
; #define PG8_LDB(dst, b, h) do { _Pragma("unroll") for (int n = 0; n < 2; ++n) { if constexpr (FP8) dst##8[n] = PG8_LD8(pb, PG8_SA(b, h) + n * 2048); \
;         else { _Pragma("unroll") for (int k = 0; k < 2; ++k) dst[n][k] = *(const LAS bf16x8*)(pb + PG8_SA(b, h) + n * 2048 + k * 1024); } } } while (0)
; #define PG8_WAIT_V(n) asm volatile("s_waitcnt vmcnt(" #n ")" ::: "memory")
; #define PG8_WAIT_L(n) asm volatile("s_waitcnt lgkmcnt(" #n ")" ::: "memory")
; #define PG8_BAR __builtin_amdgcn_s_barrier()
; #define PG8_SCHED __builtin_amdgcn_sched_barrier(0)
; template <class Epi, class Sched, bool PERM, bool FP8 = false, bool GATHER = false>
; DI void gemm_phase(LAS unsigned char* lds, const unsigned char* wsb, const unsigned lda, const unsigned ldb, const int nt, const Sched& S, const Epi& E) {
;     ...
;             PG8_LDB(B0, 0, 0); PG8_LDB(B1, 0, 1); PG8_SCHED; PG8_LDA(At, 0, 0); PG8_STAGEA(PG8_SA(1, 1), t + 1, 1, false);
;             if constexpr (GATHER) { if (last) {
;                 int tz = tid; asm volatile("" : "+v"(tz));
; #pragma unroll
;                 for (int i = 0; i < 2; ++i) { int R, C; stage_rc(tz * 16 + i * 8192, R, C);
; #pragma unroll
;                     for (int h = 0; h < 2; ++h) { const unsigned tk = (unsigned)tokt[h * HALF + R]; offC[h][i] = (tk < (unsigned)NTOK ? tk : (unsigned)(NTOK - 1)) * lda + (unsigned)C * 2u; } } } }
;             PG8_WAIT_V(8); PG8_WAIT_L(0); PG8_BAR; PG8_MMA(0, 0, At, B0); PG8_MMA(0, 1, At, B1); PG8_BAR; PG8_SCHED;
;             PG8_LDA(At, 0, 1); PG8_STAGE(PG8_SB(0, 0), b2, voffB); PG8_STAGE(PG8_SB(0, 1), b2 + hstepB, voffB); PG8_STAGEA(PG8_SA(0, 0), k2, 0, last);
;             PG8_WAIT_V(8); PG8_WAIT_L(0); PG8_BAR; PG8_MMA(1, 0, At, B0); PG8_MMA(1, 1, At, B1); PG8_BAR; PG8_SCHED;
.LBB0_1450:
	ds_read_b128 v[130:133], v154
	ds_read_b128 v[134:137], v154 offset:1024
	ds_read_b128 v[138:141], v154 offset:2048
	ds_read_b128 v[142:145], v154 offset:3072
	ds_read_b128 v[158:161], v154 offset:16384
	ds_read_b128 v[162:165], v154 offset:17408
	ds_read_b128 v[166:169], v154 offset:18432
	ds_read_b128 v[170:173], v154 offset:19456
	s_add_i32 s74, s71, 0xfffe0080
	s_add_i32 s75, s74, s68
	s_cmp_eq_u32 s70, 4
	s_cselect_b64 s[24:25], -1, 0
	s_and_b64 s[72:73], s[24:25], exec
	s_cselect_b32 s72, s69, s75
	s_cselect_b32 s76, 0, s74
	s_add_i32 s73, s72, 0x80
	s_add_i32 s74, s67, s71
	s_add_u32 s74, s10, s74
	s_addc_u32 s75, s11, 0
	v_lshl_add_u64 v[150:151], s[74:75], 0, v[146:147]
	s_add_i32 m0, s5, 0xc000
	ds_read_b128 v[174:177], v153
	ds_read_b128 v[178:181], v153 offset:1024
	ds_read_b128 v[182:185], v153 offset:2048
	ds_read_b128 v[186:189], v153 offset:3072
	ds_read_b128 v[190:193], v153 offset:4096
	ds_read_b128 v[194:197], v153 offset:5120
	ds_read_b128 v[198:201], v153 offset:6144
	ds_read_b128 v[202:205], v153 offset:7168
	global_load_lds_dwordx4 v[150:151], off
	v_lshl_add_u64 v[150:151], s[74:75], 0, v[148:149]
	s_add_i32 m0, s5, 0xe000
	s_nop 0
	global_load_lds_dwordx4 v[150:151], off
	s_waitcnt vmcnt(8)
	s_waitcnt lgkmcnt(0)
	s_barrier
	s_waitcnt lgkmcnt(0)
	v_mfma_f32_16x16x128_f8f6f4 v[126:129], v[130:137], v[174:181], v[126:129]
	v_mfma_f32_16x16x128_f8f6f4 v[122:125], v[138:145], v[174:181], v[122:125]
	v_mfma_f32_16x16x128_f8f6f4 v[118:121], v[130:137], v[182:189], v[118:121]
	v_mfma_f32_16x16x128_f8f6f4 v[114:117], v[138:145], v[182:189], v[114:117]
	v_mfma_f32_16x16x128_f8f6f4 v[206:209], v[130:137], v[190:197], v[94:97]
	v_mfma_f32_16x16x128_f8f6f4 v[210:213], v[138:145], v[190:197], v[90:93]
	v_mfma_f32_16x16x128_f8f6f4 v[214:217], v[130:137], v[198:205], v[82:85]
	v_mfma_f32_16x16x128_f8f6f4 v[218:221], v[138:145], v[198:205], v[74:77]
	v_mfma_f32_16x16x128_f8f6f4 v[110:113], v[158:165], v[174:181], v[110:113]
	v_mfma_f32_16x16x128_f8f6f4 v[106:109], v[166:173], v[174:181], v[106:109]
	v_mfma_f32_16x16x128_f8f6f4 v[102:105], v[158:165], v[182:189], v[102:105]
	v_mfma_f32_16x16x128_f8f6f4 v[98:101], v[166:173], v[182:189], v[98:101]
	v_mfma_f32_16x16x128_f8f6f4 v[174:177], v[158:165], v[190:197], v[86:89]
	v_mfma_f32_16x16x128_f8f6f4 v[178:181], v[166:173], v[190:197], v[78:81]
	v_mfma_f32_16x16x128_f8f6f4 v[182:185], v[158:165], v[198:205], v[70:73]
	v_mfma_f32_16x16x128_f8f6f4 v[186:189], v[166:173], v[198:205], v[66:69]
	s_barrier
	s_add_u32 s74, s10, s72
	s_addc_u32 s75, s11, 0
	s_mov_b32 m0, s19
	v_lshl_add_u64 v[150:151], s[74:75], 0, v[146:147]
	s_nop 0
	global_load_lds_dwordx4 v[150:151], off
	v_lshl_add_u64 v[150:151], s[74:75], 0, v[148:149]
	s_add_i32 s74, s72, 0x20000
	s_add_u32 s74, s10, s74
	s_addc_u32 s75, s11, 0
	s_and_b64 s[24:25], s[20:21], s[24:25]
	s_and_b64 s[24:25], s[24:25], exec
	s_mov_b32 m0, s28
	s_cselect_b32 s24, s60, s67
	global_load_lds_dwordx4 v[150:151], off
	v_lshl_add_u64 v[150:151], s[74:75], 0, v[146:147]
	s_mov_b32 m0, s29
	s_add_i32 s24, s76, s24
	global_load_lds_dwordx4 v[150:151], off
	v_lshl_add_u64 v[150:151], s[74:75], 0, v[148:149]
	s_add_u32 s74, s10, s24
	s_mov_b32 m0, s36
	s_addc_u32 s75, s11, 0
	global_load_lds_dwordx4 v[150:151], off
	v_lshl_add_u64 v[150:151], s[74:75], 0, v[146:147]
	s_mov_b32 m0, s5
	s_nop 0
	global_load_lds_dwordx4 v[150:151], off
	v_lshl_add_u64 v[150:151], s[74:75], 0, v[148:149]
	s_mov_b32 m0, s37
	s_nop 0
	global_load_lds_dwordx4 v[150:151], off
	ds_read_b128 v[66:69], v153 offset:16384
	ds_read_b128 v[70:73], v153 offset:17408
	ds_read_b128 v[74:77], v153 offset:18432
	ds_read_b128 v[78:81], v153 offset:19456
	ds_read_b128 v[82:85], v153 offset:20480
	ds_read_b128 v[86:89], v153 offset:21504
	ds_read_b128 v[90:93], v153 offset:22528
	ds_read_b128 v[94:97], v153 offset:23552
	s_waitcnt vmcnt(8)
	s_waitcnt lgkmcnt(0)
	s_barrier
	s_waitcnt lgkmcnt(0)
	v_mfma_f32_16x16x128_f8f6f4 v[62:65], v[130:137], v[66:73], v[62:65]
	v_mfma_f32_16x16x128_f8f6f4 v[58:61], v[138:145], v[66:73], v[58:61]
	v_mfma_f32_16x16x128_f8f6f4 v[50:53], v[130:137], v[74:81], v[50:53]
	v_mfma_f32_16x16x128_f8f6f4 v[190:193], v[138:145], v[74:81], v[42:45]
	v_mfma_f32_16x16x128_f8f6f4 v[194:197], v[130:137], v[82:89], v[34:37]
	v_mfma_f32_16x16x128_f8f6f4 v[198:201], v[138:145], v[82:89], v[26:29]
	v_mfma_f32_16x16x128_f8f6f4 v[202:205], v[130:137], v[90:97], v[18:21]
	v_mfma_f32_16x16x128_f8f6f4 v[222:225], v[138:145], v[90:97], v[10:13]
	v_mfma_f32_16x16x128_f8f6f4 v[54:57], v[158:165], v[66:73], v[54:57]
	v_mfma_f32_16x16x128_f8f6f4 v[226:229], v[166:173], v[66:73], v[46:49]
	v_mfma_f32_16x16x128_f8f6f4 v[230:233], v[158:165], v[74:81], v[38:41]
	v_mfma_f32_16x16x128_f8f6f4 v[234:237], v[166:173], v[74:81], v[30:33]
	v_mfma_f32_16x16x128_f8f6f4 v[238:241], v[158:165], v[82:89], v[22:25]
	v_mfma_f32_16x16x128_f8f6f4 v[242:245], v[166:173], v[82:89], v[14:17]
	v_mfma_f32_16x16x128_f8f6f4 v[246:249], v[158:165], v[90:97], v[6:9]
	v_mfma_f32_16x16x128_f8f6f4 v[250:253], v[166:173], v[90:97], v[2:5]
	s_barrier
; #define PG8_STAGE(bufoff, gbase, voff) do { _Pragma("unroll") for (int _i = 0; _i < 2; ++_i) \
;         __builtin_amdgcn_global_load_lds((const unsigned*)(wsb + (size_t)(gbase) + (voff)[_i]), (LAS unsigned*)(lds + (bufoff) + ldsw + _i * 8192), 16, 0, 0); } while (0)
; #define PG8_LDA(dst, b, h) do { _Pragma("unroll") for (int m = 0; m < 4; ++m) { if constexpr (FP8) dst##8[m] = PG8_LD8(pa, PG8_SA(b, h) + m * 2048); \
;         else { _Pragma("unroll") for (int k = 0; k < 2; ++k) dst[m][k] = *(const LAS bf16x8*)(pa + PG8_SA(b, h) + m * 2048 + k * 1024); } } } while (0)
; #define PG8_LDB(dst, b, h) do { _Pragma("unroll") for (int n = 0; n < 2; ++n) { if constexpr (FP8) dst##8[n] = PG8_LD8(pb, PG8_SA(b, h) + n * 2048); \
;         else { _Pragma("unroll") for (int k = 0; k < 2; ++k) dst[n][k] = *(const LAS bf16x8*)(pb + PG8_SA(b, h) + n * 2048 + k * 1024); } } } while (0)
; #define PG8_WAIT_V(n) asm volatile("s_waitcnt vmcnt(" #n ")" ::: "memory")
; #define PG8_WAIT_L(n) asm volatile("s_waitcnt lgkmcnt(" #n ")" ::: "memory")
; #define PG8_BAR __builtin_amdgcn_s_barrier()
; #define PG8_SCHED __builtin_amdgcn_sched_barrier(0)
; template <class Epi, class Sched, bool PERM, bool FP8 = false, bool GATHER = false>
; DI void gemm_phase(LAS unsigned char* lds, const unsigned char* wsb, const unsigned lda, const unsigned ldb, const int nt, const Sched& S, const Epi& E) {
;     ...
;             PG8_LDB(B0, 1, 0); PG8_LDB(B1, 1, 1); PG8_SCHED; PG8_LDA(At, 1, 0); PG8_STAGEA(PG8_SA(0, 1), k2, 1, last);
;             PG8_WAIT_V(8); PG8_WAIT_L(0); PG8_BAR; PG8_MMA(0, 0, At, B0); PG8_MMA(0, 1, At, B1); PG8_BAR; PG8_SCHED;
;             PG8_LDA(At, 1, 1); PG8_STAGE(PG8_SB(1, 0), b3, voffB); PG8_STAGE(PG8_SB(1, 1), b3 + hstepB, voffB); PG8_STAGEA(PG8_SA(1, 0), k3, 0, last);
;             PG8_WAIT_V(8); PG8_WAIT_L(0); PG8_BAR; PG8_MMA(1, 0, At, B0); PG8_MMA(1, 1, At, B1); PG8_BAR; PG8_SCHED;
;         }
;         if (wr == 0) PG8_BAR;
	s_nop 4
	s_add_i32 s25, s24, 0x20000
	s_add_u32 s74, s10, s25
	s_addc_u32 s75, s11, 0
	s_mov_b32 m0, s38
	v_lshl_add_u64 v[66:67], s[74:75], 0, v[146:147]
	global_load_lds_dwordx4 v[66:67], off
	v_lshl_add_u64 v[66:67], s[74:75], 0, v[148:149]
	s_mov_b32 m0, s39
	s_nop 0
	global_load_lds_dwordx4 v[66:67], off
	ds_read_b128 v[2:5], v154 offset:32768
	ds_read_b128 v[6:9], v154 offset:33792
	ds_read_b128 v[10:13], v154 offset:34816
	ds_read_b128 v[14:17], v154 offset:35840
	ds_read_b128 v[130:133], v154 offset:49152
	ds_read_b128 v[134:137], v154 offset:50176
	ds_read_b128 v[138:141], v154 offset:51200
	ds_read_b128 v[142:145], v154 offset:52224
	ds_read_b128 v[18:21], v153 offset:32768
	ds_read_b128 v[22:25], v153 offset:33792
	ds_read_b128 v[26:29], v153 offset:34816
	ds_read_b128 v[30:33], v153 offset:35840
	ds_read_b128 v[34:37], v153 offset:36864
	ds_read_b128 v[38:41], v153 offset:37888
	ds_read_b128 v[42:45], v153 offset:38912
	ds_read_b128 v[46:49], v153 offset:39936
	s_waitcnt vmcnt(8)
	s_waitcnt lgkmcnt(0)
	s_barrier
	s_waitcnt lgkmcnt(0)
	v_mfma_f32_16x16x128_f8f6f4 v[126:129], v[2:9], v[18:25], v[126:129]
	v_mfma_f32_16x16x128_f8f6f4 v[122:125], v[10:17], v[18:25], v[122:125]
	v_mfma_f32_16x16x128_f8f6f4 v[118:121], v[2:9], v[26:33], v[118:121]
	v_mfma_f32_16x16x128_f8f6f4 v[114:117], v[10:17], v[26:33], v[114:117]
	v_mfma_f32_16x16x128_f8f6f4 v[94:97], v[2:9], v[34:41], v[206:209]
	v_mfma_f32_16x16x128_f8f6f4 v[90:93], v[10:17], v[34:41], v[210:213]
	v_mfma_f32_16x16x128_f8f6f4 v[82:85], v[2:9], v[42:49], v[214:217]
	v_mfma_f32_16x16x128_f8f6f4 v[74:77], v[10:17], v[42:49], v[218:221]
	v_mfma_f32_16x16x128_f8f6f4 v[110:113], v[130:137], v[18:25], v[110:113]
	v_mfma_f32_16x16x128_f8f6f4 v[106:109], v[138:145], v[18:25], v[106:109]
	v_mfma_f32_16x16x128_f8f6f4 v[102:105], v[130:137], v[26:33], v[102:105]
	v_mfma_f32_16x16x128_f8f6f4 v[98:101], v[138:145], v[26:33], v[98:101]
	v_mfma_f32_16x16x128_f8f6f4 v[86:89], v[130:137], v[34:41], v[174:177]
	v_mfma_f32_16x16x128_f8f6f4 v[78:81], v[138:145], v[34:41], v[178:181]
	v_mfma_f32_16x16x128_f8f6f4 v[70:73], v[130:137], v[42:49], v[182:185]
	v_mfma_f32_16x16x128_f8f6f4 v[66:69], v[138:145], v[42:49], v[186:189]
	s_barrier
	s_add_u32 s74, s10, s73
	s_addc_u32 s75, s11, 0
	s_add_i32 s72, s72, 0x20080
	s_mov_b32 m0, s43
	v_lshl_add_u64 v[18:19], s[74:75], 0, v[146:147]
	s_add_u32 s72, s10, s72
	global_load_lds_dwordx4 v[18:19], off
	v_lshl_add_u64 v[18:19], s[74:75], 0, v[148:149]
	s_mov_b32 m0, s46
	s_addc_u32 s73, s11, 0
	s_addk_i32 s24, 0x80
	global_load_lds_dwordx4 v[18:19], off
	v_lshl_add_u64 v[18:19], s[72:73], 0, v[146:147]
	s_mov_b32 m0, s49
	s_add_u32 s24, s10, s24
	global_load_lds_dwordx4 v[18:19], off
	v_lshl_add_u64 v[18:19], s[72:73], 0, v[148:149]
	s_mov_b32 m0, s50
	s_addc_u32 s25, s11, 0
	global_load_lds_dwordx4 v[18:19], off
	v_lshl_add_u64 v[18:19], s[24:25], 0, v[146:147]
	s_mov_b32 m0, s47
	s_nop 0
	global_load_lds_dwordx4 v[18:19], off
	v_lshl_add_u64 v[18:19], s[24:25], 0, v[148:149]
	s_mov_b32 m0, s48
	s_nop 0
	global_load_lds_dwordx4 v[18:19], off
	ds_read_b128 v[158:161], v153 offset:49152
	ds_read_b128 v[162:165], v153 offset:50176
	ds_read_b128 v[166:169], v153 offset:51200
	ds_read_b128 v[170:173], v153 offset:52224
	ds_read_b128 v[174:177], v153 offset:53248
	ds_read_b128 v[178:181], v153 offset:54272
	ds_read_b128 v[182:185], v153 offset:55296
	ds_read_b128 v[186:189], v153 offset:56320
	s_waitcnt vmcnt(8)
	s_waitcnt lgkmcnt(0)
	s_barrier
	s_waitcnt lgkmcnt(0)
	v_mfma_f32_16x16x128_f8f6f4 v[62:65], v[2:9], v[158:165], v[62:65]
	v_mfma_f32_16x16x128_f8f6f4 v[58:61], v[10:17], v[158:165], v[58:61]
	v_mfma_f32_16x16x128_f8f6f4 v[50:53], v[2:9], v[166:173], v[50:53]
	v_mfma_f32_16x16x128_f8f6f4 v[42:45], v[10:17], v[166:173], v[190:193]
	v_mfma_f32_16x16x128_f8f6f4 v[34:37], v[2:9], v[174:181], v[194:197]
	v_mfma_f32_16x16x128_f8f6f4 v[26:29], v[10:17], v[174:181], v[198:201]
	v_mfma_f32_16x16x128_f8f6f4 v[18:21], v[2:9], v[182:189], v[202:205]
	v_mfma_f32_16x16x128_f8f6f4 v[10:13], v[10:17], v[182:189], v[222:225]
	v_mfma_f32_16x16x128_f8f6f4 v[54:57], v[130:137], v[158:165], v[54:57]
	v_mfma_f32_16x16x128_f8f6f4 v[46:49], v[138:145], v[158:165], v[226:229]
	v_mfma_f32_16x16x128_f8f6f4 v[38:41], v[130:137], v[166:173], v[230:233]
	v_mfma_f32_16x16x128_f8f6f4 v[30:33], v[138:145], v[166:173], v[234:237]
	v_mfma_f32_16x16x128_f8f6f4 v[22:25], v[130:137], v[174:181], v[238:241]
	v_mfma_f32_16x16x128_f8f6f4 v[14:17], v[138:145], v[174:181], v[242:245]
	v_mfma_f32_16x16x128_f8f6f4 v[6:9], v[130:137], v[182:189], v[246:249]
	v_mfma_f32_16x16x128_f8f6f4 v[2:5], v[138:145], v[182:189], v[250:253]
	s_barrier
	s_add_i32 s70, s70, 2
	s_addk_i32 s71, 0x100
	s_cmp_gt_u32 s70, 5
	s_cbranch_scc0 .LBB0_1450
	s_and_b64 vcc, exec, s[14:15]
	s_cbranch_vccz .LBB0_1453
	s_barrier

; #define PG8_STAGE(bufoff, gbase, voff) do { _Pragma("unroll") for (int _i = 0; _i < 2; ++_i) \
;         __builtin_amdgcn_global_load_lds((const unsigned*)(wsb + (size_t)(gbase) + (voff)[_i]), (LAS unsigned*)(lds + (bufoff) + ldsw + _i * 8192), 16, 0, 0); } while (0)
; #define PG8_LDA(dst, b, h) do { _Pragma("unroll") for (int m = 0; m < 4; ++m) { if constexpr (FP8) dst##8[m] = PG8_LD8(pa, PG8_SA(b, h) + m * 2048); \
;         else { _Pragma("unroll") for (int k = 0; k < 2; ++k) dst[m][k] = *(const LAS bf16x8*)(pa + PG8_SA(b, h) + m * 2048 + k * 1024); } } } while (0)
; #define PG8_LDB(dst, b, h) do { _Pragma("unroll") for (int n = 0; n < 2; ++n) { if constexpr (FP8) dst##8[n] = PG8_LD8(pb, PG8_SA(b, h) + n * 2048); \
;         else { _Pragma("unroll") for (int k = 0; k < 2; ++k) dst[n][k] = *(const LAS bf16x8*)(pb + PG8_SA(b, h) + n * 2048 + k * 1024); } } } while (0)
; #define PG8_WAIT_V(n) asm volatile("s_waitcnt vmcnt(" #n ")" ::: "memory")
; #define PG8_WAIT_L(n) asm volatile("s_waitcnt lgkmcnt(" #n ")" ::: "memory")
; #define PG8_BAR __builtin_amdgcn_s_barrier()
; #define PG8_SCHED __builtin_amdgcn_sched_barrier(0)
; template <class Epi, class Sched, bool PERM, bool FP8 = false, bool GATHER = false>
; DI void gemm_phase(LAS unsigned char* lds, const unsigned char* wsb, const unsigned lda, const unsigned ldb, const int nt, const Sched& S, const Epi& E) {
;     ...
;             PG8_LDB(B0, 0, 0); PG8_LDB(B1, 0, 1); PG8_SCHED; PG8_LDA(At, 0, 0); PG8_STAGEA(PG8_SA(1, 1), t + 1, 1, false);
;             if constexpr (GATHER) { if (last) {
;                 int tz = tid; asm volatile("" : "+v"(tz));
; #pragma unroll
;                 for (int i = 0; i < 2; ++i) { int R, C; stage_rc(tz * 16 + i * 8192, R, C);
; #pragma unroll
;                     for (int h = 0; h < 2; ++h) { const unsigned tk = (unsigned)tokt[h * HALF + R]; offC[h][i] = (tk < (unsigned)NTOK ? tk : (unsigned)(NTOK - 1)) * lda + (unsigned)C * 2u; } } } }
;             PG8_WAIT_V(8); PG8_WAIT_L(0); PG8_BAR; PG8_MMA(0, 0, At, B0); PG8_MMA(0, 1, At, B1); PG8_BAR; PG8_SCHED;
;             PG8_LDA(At, 0, 1); PG8_STAGE(PG8_SB(0, 0), b2, voffB); PG8_STAGE(PG8_SB(0, 1), b2 + hstepB, voffB); PG8_STAGEA(PG8_SA(0, 0), k2, 0, last);
;             PG8_WAIT_V(8); PG8_WAIT_L(0); PG8_BAR; PG8_MMA(1, 0, At, B0); PG8_MMA(1, 1, At, B1); PG8_BAR; PG8_SCHED;
.LBB0_1626:
	ds_read_b128 v[130:133], v186
	ds_read_b128 v[134:137], v186 offset:1024
	ds_read_b128 v[138:141], v186 offset:2048
	ds_read_b128 v[142:145], v186 offset:3072
	ds_read_b128 v[146:149], v186 offset:16384
	ds_read_b128 v[150:153], v186 offset:17408
	ds_read_b128 v[160:163], v186 offset:18432
	ds_read_b128 v[164:167], v186 offset:19456
	s_add_i32 s53, s7, 0xfffe0080
	s_cmp_eq_u32 s8, 4
	s_cselect_b32 s9, s50, s6
	s_cselect_b32 s53, s49, s53
	s_add_i32 s58, s9, 0x80
	s_add_u32 s60, s12, s7
	s_addc_u32 s61, s13, 0
	v_lshl_add_u64 v[206:207], s[60:61], 0, v[154:155]
	s_add_i32 m0, s69, 0xc000
	ds_read_b128 v[168:171], v185
	ds_read_b128 v[172:175], v185 offset:1024
	ds_read_b128 v[176:179], v185 offset:2048
	ds_read_b128 v[180:183], v185 offset:3072
	ds_read_b128 v[190:193], v185 offset:4096
	ds_read_b128 v[194:197], v185 offset:5120
	ds_read_b128 v[198:201], v185 offset:6144
	ds_read_b128 v[202:205], v185 offset:7168
	global_load_lds_dwordx4 v[206:207], off
	v_lshl_add_u64 v[206:207], s[60:61], 0, v[156:157]
	s_add_i32 m0, s69, 0xe000
	s_nop 0
	global_load_lds_dwordx4 v[206:207], off
	s_waitcnt vmcnt(8)
	s_waitcnt lgkmcnt(0)
	s_barrier
	s_waitcnt lgkmcnt(0)
	v_mfma_f32_16x16x128_f8f6f4 v[126:129], v[130:137], v[168:175], v[126:129]
	v_mfma_f32_16x16x128_f8f6f4 v[122:125], v[138:145], v[168:175], v[122:125]
	v_mfma_f32_16x16x128_f8f6f4 v[110:113], v[130:137], v[176:183], v[110:113]
	v_mfma_f32_16x16x128_f8f6f4 v[106:109], v[138:145], v[176:183], v[106:109]
	v_mfma_f32_16x16x128_f8f6f4 v[206:209], v[130:137], v[190:197], v[94:97]
	v_mfma_f32_16x16x128_f8f6f4 v[210:213], v[138:145], v[190:197], v[90:93]
	v_mfma_f32_16x16x128_f8f6f4 v[214:217], v[130:137], v[198:205], v[78:81]
	v_mfma_f32_16x16x128_f8f6f4 v[218:221], v[138:145], v[198:205], v[74:77]
	v_mfma_f32_16x16x128_f8f6f4 v[118:121], v[146:153], v[168:175], v[118:121]
	v_mfma_f32_16x16x128_f8f6f4 v[114:117], v[160:167], v[168:175], v[114:117]
	v_mfma_f32_16x16x128_f8f6f4 v[102:105], v[146:153], v[176:183], v[102:105]
	v_mfma_f32_16x16x128_f8f6f4 v[98:101], v[160:167], v[176:183], v[98:101]
	v_mfma_f32_16x16x128_f8f6f4 v[168:171], v[146:153], v[190:197], v[86:89]
	v_mfma_f32_16x16x128_f8f6f4 v[172:175], v[160:167], v[190:197], v[82:85]
	v_mfma_f32_16x16x128_f8f6f4 v[176:179], v[146:153], v[198:205], v[70:73]
	v_mfma_f32_16x16x128_f8f6f4 v[180:183], v[160:167], v[198:205], v[66:69]
	s_barrier
	s_add_u32 s60, s12, s9
	s_addc_u32 s61, s13, 0
	s_mov_b32 m0, s70
	v_lshl_add_u64 v[190:191], s[60:61], 0, v[154:155]
	s_add_i32 s59, s9, 0x20000
	global_load_lds_dwordx4 v[190:191], off
	v_lshl_add_u64 v[190:191], s[60:61], 0, v[156:157]
	s_add_u32 s60, s12, s59
	s_mov_b32 m0, s71
	s_addc_u32 s61, s13, 0
	global_load_lds_dwordx4 v[190:191], off
	v_lshl_add_u64 v[190:191], s[60:61], 0, v[154:155]
	s_mov_b32 m0, s72
	s_nop 0
	global_load_lds_dwordx4 v[190:191], off
	v_lshl_add_u64 v[190:191], s[60:61], 0, v[156:157]
	s_add_u32 s60, s12, s53
	s_mov_b32 m0, s73
	s_addc_u32 s61, s13, 0
	global_load_lds_dwordx4 v[190:191], off
	v_lshl_add_u64 v[190:191], s[60:61], 0, v[154:155]
	s_mov_b32 m0, s69
	s_nop 0
	global_load_lds_dwordx4 v[190:191], off
	v_lshl_add_u64 v[190:191], s[60:61], 0, v[156:157]
	s_mov_b32 m0, s74
	s_nop 0
	global_load_lds_dwordx4 v[190:191], off
	ds_read_b128 v[66:69], v185 offset:16384
	ds_read_b128 v[70:73], v185 offset:17408
	ds_read_b128 v[74:77], v185 offset:18432
	ds_read_b128 v[78:81], v185 offset:19456
	ds_read_b128 v[82:85], v185 offset:20480
	ds_read_b128 v[86:89], v185 offset:21504
	ds_read_b128 v[90:93], v185 offset:22528
	ds_read_b128 v[94:97], v185 offset:23552
	s_waitcnt vmcnt(8)
	s_waitcnt lgkmcnt(0)
	s_barrier
	s_waitcnt lgkmcnt(0)
	v_mfma_f32_16x16x128_f8f6f4 v[62:65], v[130:137], v[66:73], v[62:65]
	v_mfma_f32_16x16x128_f8f6f4 v[58:61], v[138:145], v[66:73], v[58:61]
	v_mfma_f32_16x16x128_f8f6f4 v[190:193], v[130:137], v[74:81], v[46:49]
	v_mfma_f32_16x16x128_f8f6f4 v[194:197], v[138:145], v[74:81], v[42:45]
	v_mfma_f32_16x16x128_f8f6f4 v[198:201], v[130:137], v[82:89], v[30:33]
	v_mfma_f32_16x16x128_f8f6f4 v[202:205], v[138:145], v[82:89], v[26:29]
	v_mfma_f32_16x16x128_f8f6f4 v[222:225], v[130:137], v[90:97], v[14:17]
	v_mfma_f32_16x16x128_f8f6f4 v[226:229], v[138:145], v[90:97], v[10:13]
	v_mfma_f32_16x16x128_f8f6f4 v[54:57], v[146:153], v[66:73], v[54:57]
	v_mfma_f32_16x16x128_f8f6f4 v[50:53], v[160:167], v[66:73], v[50:53]
	v_mfma_f32_16x16x128_f8f6f4 v[230:233], v[146:153], v[74:81], v[38:41]
	v_mfma_f32_16x16x128_f8f6f4 v[234:237], v[160:167], v[74:81], v[34:37]
	v_mfma_f32_16x16x128_f8f6f4 v[238:241], v[146:153], v[82:89], v[22:25]
	v_mfma_f32_16x16x128_f8f6f4 v[242:245], v[160:167], v[82:89], v[18:21]
	v_mfma_f32_16x16x128_f8f6f4 v[246:249], v[146:153], v[90:97], v[6:9]
	v_mfma_f32_16x16x128_f8f6f4 v[250:253], v[160:167], v[90:97], v[2:5]
	s_barrier
; #define PG8_STAGE(bufoff, gbase, voff) do { _Pragma("unroll") for (int _i = 0; _i < 2; ++_i) \
;         __builtin_amdgcn_global_load_lds((const unsigned*)(wsb + (size_t)(gbase) + (voff)[_i]), (LAS unsigned*)(lds + (bufoff) + ldsw + _i * 8192), 16, 0, 0); } while (0)
; #define PG8_LDA(dst, b, h) do { _Pragma("unroll") for (int m = 0; m < 4; ++m) { if constexpr (FP8) dst##8[m] = PG8_LD8(pa, PG8_SA(b, h) + m * 2048); \
;         else { _Pragma("unroll") for (int k = 0; k < 2; ++k) dst[m][k] = *(const LAS bf16x8*)(pa + PG8_SA(b, h) + m * 2048 + k * 1024); } } } while (0)
; #define PG8_LDB(dst, b, h) do { _Pragma("unroll") for (int n = 0; n < 2; ++n) { if constexpr (FP8) dst##8[n] = PG8_LD8(pb, PG8_SA(b, h) + n * 2048); \
;         else { _Pragma("unroll") for (int k = 0; k < 2; ++k) dst[n][k] = *(const LAS bf16x8*)(pb + PG8_SA(b, h) + n * 2048 + k * 1024); } } } while (0)
; #define PG8_WAIT_V(n) asm volatile("s_waitcnt vmcnt(" #n ")" ::: "memory")
; #define PG8_WAIT_L(n) asm volatile("s_waitcnt lgkmcnt(" #n ")" ::: "memory")
; #define PG8_BAR __builtin_amdgcn_s_barrier()
; #define PG8_SCHED __builtin_amdgcn_sched_barrier(0)
; template <class Epi, class Sched, bool PERM, bool FP8 = false, bool GATHER = false>
; DI void gemm_phase(LAS unsigned char* lds, const unsigned char* wsb, const unsigned lda, const unsigned ldb, const int nt, const Sched& S, const Epi& E) {
;     ...
;             PG8_LDB(B0, 1, 0); PG8_LDB(B1, 1, 1); PG8_SCHED; PG8_LDA(At, 1, 0); PG8_STAGEA(PG8_SA(0, 1), k2, 1, last);
;             PG8_WAIT_V(8); PG8_WAIT_L(0); PG8_BAR; PG8_MMA(0, 0, At, B0); PG8_MMA(0, 1, At, B1); PG8_BAR; PG8_SCHED;
;             PG8_LDA(At, 1, 1); PG8_STAGE(PG8_SB(1, 0), b3, voffB); PG8_STAGE(PG8_SB(1, 1), b3 + hstepB, voffB); PG8_STAGEA(PG8_SA(1, 0), k3, 0, last);
;             PG8_WAIT_V(8); PG8_WAIT_L(0); PG8_BAR; PG8_MMA(1, 0, At, B0); PG8_MMA(1, 1, At, B1); PG8_BAR; PG8_SCHED;
;         }
;         if (wr == 0) PG8_BAR;
	s_nop 4
	s_add_i32 s59, s53, 0x20000
	s_add_u32 s60, s12, s59
	s_addc_u32 s61, s13, 0
	s_mov_b32 m0, s75
	v_lshl_add_u64 v[66:67], s[60:61], 0, v[154:155]
	global_load_lds_dwordx4 v[66:67], off
	v_lshl_add_u64 v[66:67], s[60:61], 0, v[156:157]
	s_mov_b32 m0, s76
	s_nop 0
	global_load_lds_dwordx4 v[66:67], off
	ds_read_b128 v[2:5], v186 offset:32768
	ds_read_b128 v[6:9], v186 offset:33792
	ds_read_b128 v[18:21], v186 offset:34816
	ds_read_b128 v[22:25], v186 offset:35840
	ds_read_b128 v[130:133], v186 offset:49152
	ds_read_b128 v[134:137], v186 offset:50176
	ds_read_b128 v[138:141], v186 offset:51200
	ds_read_b128 v[142:145], v186 offset:52224
	ds_read_b128 v[10:13], v185 offset:32768
	ds_read_b128 v[14:17], v185 offset:33792
	ds_read_b128 v[26:29], v185 offset:34816
	ds_read_b128 v[30:33], v185 offset:35840
	ds_read_b128 v[34:37], v185 offset:36864
	ds_read_b128 v[38:41], v185 offset:37888
	ds_read_b128 v[42:45], v185 offset:38912
	ds_read_b128 v[46:49], v185 offset:39936
	s_waitcnt vmcnt(8)
	s_waitcnt lgkmcnt(0)
	s_barrier
	s_waitcnt lgkmcnt(0)
	v_mfma_f32_16x16x128_f8f6f4 v[126:129], v[2:9], v[10:17], v[126:129]
	v_mfma_f32_16x16x128_f8f6f4 v[122:125], v[18:25], v[10:17], v[122:125]
	v_mfma_f32_16x16x128_f8f6f4 v[110:113], v[2:9], v[26:33], v[110:113]
	v_mfma_f32_16x16x128_f8f6f4 v[106:109], v[18:25], v[26:33], v[106:109]
	v_mfma_f32_16x16x128_f8f6f4 v[94:97], v[2:9], v[34:41], v[206:209]
	v_mfma_f32_16x16x128_f8f6f4 v[90:93], v[18:25], v[34:41], v[210:213]
	v_mfma_f32_16x16x128_f8f6f4 v[78:81], v[2:9], v[42:49], v[214:217]
	v_mfma_f32_16x16x128_f8f6f4 v[74:77], v[18:25], v[42:49], v[218:221]
	v_mfma_f32_16x16x128_f8f6f4 v[118:121], v[130:137], v[10:17], v[118:121]
	v_mfma_f32_16x16x128_f8f6f4 v[114:117], v[138:145], v[10:17], v[114:117]
	v_mfma_f32_16x16x128_f8f6f4 v[102:105], v[130:137], v[26:33], v[102:105]
	v_mfma_f32_16x16x128_f8f6f4 v[98:101], v[138:145], v[26:33], v[98:101]
	v_mfma_f32_16x16x128_f8f6f4 v[86:89], v[130:137], v[34:41], v[168:171]
	v_mfma_f32_16x16x128_f8f6f4 v[82:85], v[138:145], v[34:41], v[172:175]
	v_mfma_f32_16x16x128_f8f6f4 v[70:73], v[130:137], v[42:49], v[176:179]
	v_mfma_f32_16x16x128_f8f6f4 v[66:69], v[138:145], v[42:49], v[180:183]
	s_barrier
	s_add_u32 s58, s12, s58
	s_addc_u32 s59, s13, 0
	s_mov_b32 m0, s85
	v_lshl_add_u64 v[10:11], s[58:59], 0, v[154:155]
	s_add_i32 s9, s9, 0x20080
	global_load_lds_dwordx4 v[10:11], off
	v_lshl_add_u64 v[10:11], s[58:59], 0, v[156:157]
	s_add_u32 s58, s12, s9
	s_mov_b32 m0, s86
	s_addc_u32 s59, s13, 0
	global_load_lds_dwordx4 v[10:11], off
	v_lshl_add_u64 v[10:11], s[58:59], 0, v[154:155]
	s_mov_b32 m0, s89
	s_addk_i32 s53, 0x80
	global_load_lds_dwordx4 v[10:11], off
	v_lshl_add_u64 v[10:11], s[58:59], 0, v[156:157]
	s_add_u32 s58, s12, s53
	s_mov_b32 m0, s90
	s_addc_u32 s59, s13, 0
	global_load_lds_dwordx4 v[10:11], off
	v_lshl_add_u64 v[10:11], s[58:59], 0, v[154:155]
	s_mov_b32 m0, s87
	s_nop 0
	global_load_lds_dwordx4 v[10:11], off
	v_lshl_add_u64 v[10:11], s[58:59], 0, v[156:157]
	s_mov_b32 m0, s88
	s_nop 0
	global_load_lds_dwordx4 v[10:11], off
	ds_read_b128 v[34:37], v185 offset:49152
	ds_read_b128 v[38:41], v185 offset:50176
	ds_read_b128 v[146:149], v185 offset:51200
	ds_read_b128 v[150:153], v185 offset:52224
	ds_read_b128 v[160:163], v185 offset:53248
	ds_read_b128 v[164:167], v185 offset:54272
	ds_read_b128 v[168:171], v185 offset:55296
	ds_read_b128 v[172:175], v185 offset:56320
	s_waitcnt vmcnt(8)
	s_waitcnt lgkmcnt(0)
	s_barrier
	s_waitcnt lgkmcnt(0)
	v_mfma_f32_16x16x128_f8f6f4 v[62:65], v[2:9], v[34:41], v[62:65]
	v_mfma_f32_16x16x128_f8f6f4 v[58:61], v[18:25], v[34:41], v[58:61]
	v_mfma_f32_16x16x128_f8f6f4 v[46:49], v[2:9], v[146:153], v[190:193]
	v_mfma_f32_16x16x128_f8f6f4 v[42:45], v[18:25], v[146:153], v[194:197]
	v_mfma_f32_16x16x128_f8f6f4 v[30:33], v[2:9], v[160:167], v[198:201]
	v_mfma_f32_16x16x128_f8f6f4 v[26:29], v[18:25], v[160:167], v[202:205]
	v_mfma_f32_16x16x128_f8f6f4 v[14:17], v[2:9], v[168:175], v[222:225]
	v_mfma_f32_16x16x128_f8f6f4 v[10:13], v[18:25], v[168:175], v[226:229]
	v_mfma_f32_16x16x128_f8f6f4 v[54:57], v[130:137], v[34:41], v[54:57]
	v_mfma_f32_16x16x128_f8f6f4 v[50:53], v[138:145], v[34:41], v[50:53]
	v_mfma_f32_16x16x128_f8f6f4 v[38:41], v[130:137], v[146:153], v[230:233]
	v_mfma_f32_16x16x128_f8f6f4 v[34:37], v[138:145], v[146:153], v[234:237]
	v_mfma_f32_16x16x128_f8f6f4 v[22:25], v[130:137], v[160:167], v[238:241]
	v_mfma_f32_16x16x128_f8f6f4 v[18:21], v[138:145], v[160:167], v[242:245]
	v_mfma_f32_16x16x128_f8f6f4 v[6:9], v[130:137], v[168:175], v[246:249]
	v_mfma_f32_16x16x128_f8f6f4 v[2:5], v[138:145], v[168:175], v[250:253]
	s_barrier
	s_add_i32 s8, s8, 2
	s_addk_i32 s7, 0x100
	s_addk_i32 s6, 0x100
	s_cmp_gt_u32 s8, 5
	s_cbranch_scc0 .LBB0_1626
	s_and_b64 vcc, exec, s[16:17]
	s_cbranch_vccz .LBB0_1629
	s_barrier

; #define PG8_STAGE(bufoff, gbase, voff) do { _Pragma("unroll") for (int _i = 0; _i < 2; ++_i) \
;         __builtin_amdgcn_global_load_lds((const unsigned*)(wsb + (size_t)(gbase) + (voff)[_i]), (LAS unsigned*)(lds + (bufoff) + ldsw + _i * 8192), 16, 0, 0); } while (0)
; #define PG8_LDA(dst, b, h) do { _Pragma("unroll") for (int m = 0; m < 4; ++m) { if constexpr (FP8) dst##8[m] = PG8_LD8(pa, PG8_SA(b, h) + m * 2048); \
;         else { _Pragma("unroll") for (int k = 0; k < 2; ++k) dst[m][k] = *(const LAS bf16x8*)(pa + PG8_SA(b, h) + m * 2048 + k * 1024); } } } while (0)
; #define PG8_LDB(dst, b, h) do { _Pragma("unroll") for (int n = 0; n < 2; ++n) { if constexpr (FP8) dst##8[n] = PG8_LD8(pb, PG8_SA(b, h) + n * 2048); \
;         else { _Pragma("unroll") for (int k = 0; k < 2; ++k) dst[n][k] = *(const LAS bf16x8*)(pb + PG8_SA(b, h) + n * 2048 + k * 1024); } } } while (0)
; #define PG8_WAIT_V(n) asm volatile("s_waitcnt vmcnt(" #n ")" ::: "memory")
; #define PG8_WAIT_L(n) asm volatile("s_waitcnt lgkmcnt(" #n ")" ::: "memory")
; #define PG8_BAR __builtin_amdgcn_s_barrier()
; #define PG8_SCHED __builtin_amdgcn_sched_barrier(0)
; template <class Epi, class Sched, bool PERM, bool FP8 = false, bool GATHER = false>
; DI void gemm_phase(LAS unsigned char* lds, const unsigned char* wsb, const unsigned lda, const unsigned ldb, const int nt, const Sched& S, const Epi& E) {
;     ...
;             PG8_LDB(B0, 0, 0); PG8_LDB(B1, 0, 1); PG8_SCHED; PG8_LDA(At, 0, 0); PG8_STAGEA(PG8_SA(1, 1), t + 1, 1, false);
;             if constexpr (GATHER) { if (last) {
;                 int tz = tid; asm volatile("" : "+v"(tz));
; #pragma unroll
;                 for (int i = 0; i < 2; ++i) { int R, C; stage_rc(tz * 16 + i * 8192, R, C);
; #pragma unroll
;                     for (int h = 0; h < 2; ++h) { const unsigned tk = (unsigned)tokt[h * HALF + R]; offC[h][i] = (tk < (unsigned)NTOK ? tk : (unsigned)(NTOK - 1)) * lda + (unsigned)C * 2u; } } } }
;             PG8_WAIT_V(8); PG8_WAIT_L(0); PG8_BAR; PG8_MMA(0, 0, At, B0); PG8_MMA(0, 1, At, B1); PG8_BAR; PG8_SCHED;
;             PG8_LDA(At, 0, 1); PG8_STAGE(PG8_SB(0, 0), b2, voffB); PG8_STAGE(PG8_SB(0, 1), b2 + hstepB, voffB); PG8_STAGEA(PG8_SA(0, 0), k2, 0, last);
;             PG8_WAIT_V(8); PG8_WAIT_L(0); PG8_BAR; PG8_MMA(1, 0, At, B0); PG8_MMA(1, 1, At, B1); PG8_BAR; PG8_SCHED;
.LBB0_1802:
	s_add_i32 s24, s20, 0xfffe0080
	s_cmp_eq_u32 s21, 4
	s_cselect_b32 s22, s72, s8
	s_cselect_b32 s24, s71, s24
	s_add_i32 s36, s22, 0x80
	s_add_u32 s38, s6, s20
	s_addc_u32 s39, s7, 0
	s_mov_b32 m0, s65
	v_lshl_add_u64 v[130:131], s[38:39], 0, v[138:139]
	global_load_lds_dwordx4 v[130:131], off
	v_lshl_add_u64 v[130:131], s[38:39], 0, v[134:135]
	s_mov_b32 m0, s66
	s_nop 0
	global_load_lds_dwordx4 v[130:131], off
	ds_read_b128 v[144:147], v142
	ds_read_b128 v[148:151], v142 offset:1024
	ds_read_b128 v[152:155], v142 offset:2048
	ds_read_b128 v[156:159], v142 offset:3072
	ds_read_b128 v[160:163], v142 offset:16384
	ds_read_b128 v[164:167], v142 offset:17408
	ds_read_b128 v[168:171], v142 offset:18432
	ds_read_b128 v[172:175], v142 offset:19456
	ds_read_b128 v[176:179], v141
	ds_read_b128 v[180:183], v141 offset:1024
	ds_read_b128 v[184:187], v141 offset:2048
	ds_read_b128 v[188:191], v141 offset:3072
	ds_read_b128 v[192:195], v141 offset:4096
	ds_read_b128 v[196:199], v141 offset:5120
	ds_read_b128 v[200:203], v141 offset:6144
	ds_read_b128 v[204:207], v141 offset:7168
	s_waitcnt vmcnt(8)
	s_waitcnt lgkmcnt(0)
	s_barrier
	s_waitcnt lgkmcnt(0)
	v_mfma_f32_16x16x128_f8f6f4 v[126:129], v[144:151], v[176:183], v[126:129]
	v_mfma_f32_16x16x128_f8f6f4 v[122:125], v[152:159], v[176:183], v[122:125]
	v_mfma_f32_16x16x128_f8f6f4 v[114:117], v[144:151], v[184:191], v[114:117]
	v_mfma_f32_16x16x128_f8f6f4 v[106:109], v[152:159], v[184:191], v[106:109]
	v_mfma_f32_16x16x128_f8f6f4 v[98:101], v[144:151], v[192:199], v[98:101]
	v_mfma_f32_16x16x128_f8f6f4 v[208:211], v[152:159], v[192:199], v[90:93]
	v_mfma_f32_16x16x128_f8f6f4 v[212:215], v[144:151], v[200:207], v[82:85]
	v_mfma_f32_16x16x128_f8f6f4 v[216:219], v[152:159], v[200:207], v[74:77]
	v_mfma_f32_16x16x128_f8f6f4 v[118:121], v[160:167], v[176:183], v[118:121]
	v_mfma_f32_16x16x128_f8f6f4 v[110:113], v[168:175], v[176:183], v[110:113]
	v_mfma_f32_16x16x128_f8f6f4 v[102:105], v[160:167], v[184:191], v[102:105]
	v_mfma_f32_16x16x128_f8f6f4 v[176:179], v[168:175], v[184:191], v[94:97]
	v_mfma_f32_16x16x128_f8f6f4 v[180:183], v[160:167], v[192:199], v[86:89]
	v_mfma_f32_16x16x128_f8f6f4 v[184:187], v[168:175], v[192:199], v[78:81]
	v_mfma_f32_16x16x128_f8f6f4 v[188:191], v[160:167], v[200:207], v[70:73]
	v_mfma_f32_16x16x128_f8f6f4 v[192:195], v[168:175], v[200:207], v[66:69]
	s_barrier
	s_add_u32 s38, s6, s22
	s_addc_u32 s39, s7, 0
	s_mov_b32 m0, s28
	v_lshl_add_u64 v[130:131], s[38:39], 0, v[252:253]
	s_add_i32 s37, s22, 0x20000
	global_load_lds_dwordx4 v[130:131], off
	v_lshl_add_u64 v[130:131], s[38:39], 0, v[136:137]
	s_add_u32 s38, s6, s37
	s_mov_b32 m0, s29
	s_addc_u32 s39, s7, 0
	global_load_lds_dwordx4 v[130:131], off
	v_lshl_add_u64 v[130:131], s[38:39], 0, v[252:253]
	s_mov_b32 m0, s42
	s_nop 0
	global_load_lds_dwordx4 v[130:131], off
	v_lshl_add_u64 v[130:131], s[38:39], 0, v[136:137]
	s_add_u32 s38, s6, s24
	s_mov_b32 m0, s43
	s_addc_u32 s39, s7, 0
	global_load_lds_dwordx4 v[130:131], off
	v_lshl_add_u64 v[130:131], s[38:39], 0, v[138:139]
	s_mov_b32 m0, s17
	s_nop 0
	global_load_lds_dwordx4 v[130:131], off
	v_lshl_add_u64 v[130:131], s[38:39], 0, v[134:135]
	s_mov_b32 m0, s46
	s_nop 0
	global_load_lds_dwordx4 v[130:131], off
	ds_read_b128 v[66:69], v141 offset:16384
	ds_read_b128 v[70:73], v141 offset:17408
	ds_read_b128 v[74:77], v141 offset:18432
	ds_read_b128 v[78:81], v141 offset:19456
	ds_read_b128 v[82:85], v141 offset:20480
	ds_read_b128 v[86:89], v141 offset:21504
	ds_read_b128 v[90:93], v141 offset:22528
	ds_read_b128 v[94:97], v141 offset:23552
	s_waitcnt vmcnt(8)
	s_waitcnt lgkmcnt(0)
	s_barrier
	s_waitcnt lgkmcnt(0)
	v_mfma_f32_16x16x128_f8f6f4 v[62:65], v[144:151], v[66:73], v[62:65]
	v_mfma_f32_16x16x128_f8f6f4 v[58:61], v[152:159], v[66:73], v[58:61]
	v_mfma_f32_16x16x128_f8f6f4 v[50:53], v[144:151], v[74:81], v[50:53]
	v_mfma_f32_16x16x128_f8f6f4 v[196:199], v[152:159], v[74:81], v[42:45]
	v_mfma_f32_16x16x128_f8f6f4 v[200:203], v[144:151], v[82:89], v[34:37]
	v_mfma_f32_16x16x128_f8f6f4 v[204:207], v[152:159], v[82:89], v[26:29]
	v_mfma_f32_16x16x128_f8f6f4 v[220:223], v[144:151], v[90:97], v[18:21]
	v_mfma_f32_16x16x128_f8f6f4 v[224:227], v[152:159], v[90:97], v[10:13]
	v_mfma_f32_16x16x128_f8f6f4 v[54:57], v[160:167], v[66:73], v[54:57]
	v_mfma_f32_16x16x128_f8f6f4 v[228:231], v[168:175], v[66:73], v[46:49]
	v_mfma_f32_16x16x128_f8f6f4 v[232:235], v[160:167], v[74:81], v[38:41]
	v_mfma_f32_16x16x128_f8f6f4 v[236:239], v[168:175], v[74:81], v[30:33]
	v_mfma_f32_16x16x128_f8f6f4 v[240:243], v[160:167], v[82:89], v[22:25]
	v_mfma_f32_16x16x128_f8f6f4 v[244:247], v[168:175], v[82:89], v[14:17]
	v_mfma_f32_16x16x128_f8f6f4 v[248:251], v[160:167], v[90:97], v[6:9]
	v_mfma_f32_16x16x128_f8f6f4 v[130:133], v[168:175], v[90:97], v[2:5]
	s_barrier
; #define PG8_STAGE(bufoff, gbase, voff) do { _Pragma("unroll") for (int _i = 0; _i < 2; ++_i) \
;         __builtin_amdgcn_global_load_lds((const unsigned*)(wsb + (size_t)(gbase) + (voff)[_i]), (LAS unsigned*)(lds + (bufoff) + ldsw + _i * 8192), 16, 0, 0); } while (0)
; #define PG8_LDA(dst, b, h) do { _Pragma("unroll") for (int m = 0; m < 4; ++m) { if constexpr (FP8) dst##8[m] = PG8_LD8(pa, PG8_SA(b, h) + m * 2048); \
;         else { _Pragma("unroll") for (int k = 0; k < 2; ++k) dst[m][k] = *(const LAS bf16x8*)(pa + PG8_SA(b, h) + m * 2048 + k * 1024); } } } while (0)
; #define PG8_LDB(dst, b, h) do { _Pragma("unroll") for (int n = 0; n < 2; ++n) { if constexpr (FP8) dst##8[n] = PG8_LD8(pb, PG8_SA(b, h) + n * 2048); \
;         else { _Pragma("unroll") for (int k = 0; k < 2; ++k) dst[n][k] = *(const LAS bf16x8*)(pb + PG8_SA(b, h) + n * 2048 + k * 1024); } } } while (0)
; #define PG8_WAIT_V(n) asm volatile("s_waitcnt vmcnt(" #n ")" ::: "memory")
; #define PG8_WAIT_L(n) asm volatile("s_waitcnt lgkmcnt(" #n ")" ::: "memory")
; #define PG8_BAR __builtin_amdgcn_s_barrier()
; #define PG8_SCHED __builtin_amdgcn_sched_barrier(0)
; template <class Epi, class Sched, bool PERM, bool FP8 = false, bool GATHER = false>
; DI void gemm_phase(LAS unsigned char* lds, const unsigned char* wsb, const unsigned lda, const unsigned ldb, const int nt, const Sched& S, const Epi& E) {
;     ...
;             PG8_LDB(B0, 1, 0); PG8_LDB(B1, 1, 1); PG8_SCHED; PG8_LDA(At, 1, 0); PG8_STAGEA(PG8_SA(0, 1), k2, 1, last);
;             PG8_WAIT_V(8); PG8_WAIT_L(0); PG8_BAR; PG8_MMA(0, 0, At, B0); PG8_MMA(0, 1, At, B1); PG8_BAR; PG8_SCHED;
;             PG8_LDA(At, 1, 1); PG8_STAGE(PG8_SB(1, 0), b3, voffB); PG8_STAGE(PG8_SB(1, 1), b3 + hstepB, voffB); PG8_STAGEA(PG8_SA(1, 0), k3, 0, last);
;             PG8_WAIT_V(8); PG8_WAIT_L(0); PG8_BAR; PG8_MMA(1, 0, At, B0); PG8_MMA(1, 1, At, B1); PG8_BAR; PG8_SCHED;
;         }
;         if (wr == 0) PG8_BAR;
	s_nop 4
	s_add_i32 s37, s24, 0x20000
	s_add_u32 s38, s6, s37
	s_addc_u32 s39, s7, 0
	s_mov_b32 m0, s47
	v_lshl_add_u64 v[66:67], s[38:39], 0, v[138:139]
	global_load_lds_dwordx4 v[66:67], off
	v_lshl_add_u64 v[66:67], s[38:39], 0, v[134:135]
	s_mov_b32 m0, s48
	s_nop 0
	global_load_lds_dwordx4 v[66:67], off
	ds_read_b128 v[2:5], v142 offset:32768
	ds_read_b128 v[6:9], v142 offset:33792
	ds_read_b128 v[10:13], v142 offset:34816
	ds_read_b128 v[14:17], v142 offset:35840
	ds_read_b128 v[144:147], v142 offset:49152
	ds_read_b128 v[148:151], v142 offset:50176
	ds_read_b128 v[152:155], v142 offset:51200
	ds_read_b128 v[156:159], v142 offset:52224
	ds_read_b128 v[18:21], v141 offset:32768
	ds_read_b128 v[22:25], v141 offset:33792
	ds_read_b128 v[26:29], v141 offset:34816
	ds_read_b128 v[30:33], v141 offset:35840
	ds_read_b128 v[34:37], v141 offset:36864
	ds_read_b128 v[38:41], v141 offset:37888
	ds_read_b128 v[42:45], v141 offset:38912
	ds_read_b128 v[46:49], v141 offset:39936
	s_waitcnt vmcnt(8)
	s_waitcnt lgkmcnt(0)
	s_barrier
	s_waitcnt lgkmcnt(0)
	v_mfma_f32_16x16x128_f8f6f4 v[126:129], v[2:9], v[18:25], v[126:129]
	v_mfma_f32_16x16x128_f8f6f4 v[122:125], v[10:17], v[18:25], v[122:125]
	v_mfma_f32_16x16x128_f8f6f4 v[114:117], v[2:9], v[26:33], v[114:117]
	v_mfma_f32_16x16x128_f8f6f4 v[106:109], v[10:17], v[26:33], v[106:109]
	v_mfma_f32_16x16x128_f8f6f4 v[98:101], v[2:9], v[34:41], v[98:101]
	v_mfma_f32_16x16x128_f8f6f4 v[90:93], v[10:17], v[34:41], v[208:211]
	v_mfma_f32_16x16x128_f8f6f4 v[82:85], v[2:9], v[42:49], v[212:215]
	v_mfma_f32_16x16x128_f8f6f4 v[74:77], v[10:17], v[42:49], v[216:219]
	v_mfma_f32_16x16x128_f8f6f4 v[118:121], v[144:151], v[18:25], v[118:121]
	v_mfma_f32_16x16x128_f8f6f4 v[110:113], v[152:159], v[18:25], v[110:113]
	v_mfma_f32_16x16x128_f8f6f4 v[102:105], v[144:151], v[26:33], v[102:105]
	v_mfma_f32_16x16x128_f8f6f4 v[94:97], v[152:159], v[26:33], v[176:179]
	v_mfma_f32_16x16x128_f8f6f4 v[86:89], v[144:151], v[34:41], v[180:183]
	v_mfma_f32_16x16x128_f8f6f4 v[78:81], v[152:159], v[34:41], v[184:187]
	v_mfma_f32_16x16x128_f8f6f4 v[70:73], v[144:151], v[42:49], v[188:191]
	v_mfma_f32_16x16x128_f8f6f4 v[66:69], v[152:159], v[42:49], v[192:195]
	s_barrier
	s_add_u32 s36, s6, s36
	s_addc_u32 s37, s7, 0
	s_mov_b32 m0, s50
	v_lshl_add_u64 v[18:19], s[36:37], 0, v[252:253]
	s_add_i32 s22, s22, 0x20080
	global_load_lds_dwordx4 v[18:19], off
	v_lshl_add_u64 v[18:19], s[36:37], 0, v[136:137]
	s_add_u32 s36, s6, s22
	s_mov_b32 m0, s51
	s_addc_u32 s37, s7, 0
	global_load_lds_dwordx4 v[18:19], off
	v_lshl_add_u64 v[18:19], s[36:37], 0, v[252:253]
	s_mov_b32 m0, s54
	s_addk_i32 s24, 0x80
	global_load_lds_dwordx4 v[18:19], off
	v_lshl_add_u64 v[18:19], s[36:37], 0, v[136:137]
	s_add_u32 s36, s6, s24
	s_mov_b32 m0, s55
	s_addc_u32 s37, s7, 0
	global_load_lds_dwordx4 v[18:19], off
	v_lshl_add_u64 v[18:19], s[36:37], 0, v[138:139]
	s_mov_b32 m0, s52
	s_nop 0
	global_load_lds_dwordx4 v[18:19], off
	v_lshl_add_u64 v[18:19], s[36:37], 0, v[134:135]
	s_mov_b32 m0, s53
	s_nop 0
	global_load_lds_dwordx4 v[18:19], off
	ds_read_b128 v[160:163], v141 offset:49152
	ds_read_b128 v[164:167], v141 offset:50176
	ds_read_b128 v[168:171], v141 offset:51200
	ds_read_b128 v[172:175], v141 offset:52224
	ds_read_b128 v[176:179], v141 offset:53248
	ds_read_b128 v[180:183], v141 offset:54272
	ds_read_b128 v[184:187], v141 offset:55296
	ds_read_b128 v[188:191], v141 offset:56320
	s_waitcnt vmcnt(8)
	s_waitcnt lgkmcnt(0)
	s_barrier
	s_waitcnt lgkmcnt(0)
	v_mfma_f32_16x16x128_f8f6f4 v[62:65], v[2:9], v[160:167], v[62:65]
	v_mfma_f32_16x16x128_f8f6f4 v[58:61], v[10:17], v[160:167], v[58:61]
	v_mfma_f32_16x16x128_f8f6f4 v[50:53], v[2:9], v[168:175], v[50:53]
	v_mfma_f32_16x16x128_f8f6f4 v[42:45], v[10:17], v[168:175], v[196:199]
	v_mfma_f32_16x16x128_f8f6f4 v[34:37], v[2:9], v[176:183], v[200:203]
	v_mfma_f32_16x16x128_f8f6f4 v[26:29], v[10:17], v[176:183], v[204:207]
	v_mfma_f32_16x16x128_f8f6f4 v[18:21], v[2:9], v[184:191], v[220:223]
	v_mfma_f32_16x16x128_f8f6f4 v[10:13], v[10:17], v[184:191], v[224:227]
	v_mfma_f32_16x16x128_f8f6f4 v[54:57], v[144:151], v[160:167], v[54:57]
	v_mfma_f32_16x16x128_f8f6f4 v[46:49], v[152:159], v[160:167], v[228:231]
	v_mfma_f32_16x16x128_f8f6f4 v[38:41], v[144:151], v[168:175], v[232:235]
	v_mfma_f32_16x16x128_f8f6f4 v[30:33], v[152:159], v[168:175], v[236:239]
	v_mfma_f32_16x16x128_f8f6f4 v[22:25], v[144:151], v[176:183], v[240:243]
	v_mfma_f32_16x16x128_f8f6f4 v[14:17], v[152:159], v[176:183], v[244:247]
	v_mfma_f32_16x16x128_f8f6f4 v[6:9], v[144:151], v[184:191], v[248:251]
	v_mfma_f32_16x16x128_f8f6f4 v[2:5], v[152:159], v[184:191], v[130:133]
	s_barrier
	s_add_i32 s21, s21, 2
	s_addk_i32 s20, 0x100
	s_addk_i32 s8, 0x100
	s_cmp_gt_u32 s21, 5
	s_cbranch_scc0 .LBB0_1802
	s_and_b64 vcc, exec, s[14:15]
	s_cbranch_vccz .LBB0_1805
	s_barrier

; #define PG8_STAGE(bufoff, gbase, voff) do { _Pragma("unroll") for (int _i = 0; _i < 2; ++_i) \
;         __builtin_amdgcn_global_load_lds((const unsigned*)(wsb + (size_t)(gbase) + (voff)[_i]), (LAS unsigned*)(lds + (bufoff) + ldsw + _i * 8192), 16, 0, 0); } while (0)
; #define PG8_LDA(dst, b, h) do { _Pragma("unroll") for (int m = 0; m < 4; ++m) { if constexpr (FP8) dst##8[m] = PG8_LD8(pa, PG8_SA(b, h) + m * 2048); \
;         else { _Pragma("unroll") for (int k = 0; k < 2; ++k) dst[m][k] = *(const LAS bf16x8*)(pa + PG8_SA(b, h) + m * 2048 + k * 1024); } } } while (0)
; #define PG8_LDB(dst, b, h) do { _Pragma("unroll") for (int n = 0; n < 2; ++n) { if constexpr (FP8) dst##8[n] = PG8_LD8(pb, PG8_SA(b, h) + n * 2048); \
;         else { _Pragma("unroll") for (int k = 0; k < 2; ++k) dst[n][k] = *(const LAS bf16x8*)(pb + PG8_SA(b, h) + n * 2048 + k * 1024); } } } while (0)
; #define PG8_WAIT_V(n) asm volatile("s_waitcnt vmcnt(" #n ")" ::: "memory")
; #define PG8_WAIT_L(n) asm volatile("s_waitcnt lgkmcnt(" #n ")" ::: "memory")
; #define PG8_BAR __builtin_amdgcn_s_barrier()
; #define PG8_SCHED __builtin_amdgcn_sched_barrier(0)
; template <class Epi, class Sched, bool PERM, bool FP8 = false, bool GATHER = false>
; DI void gemm_phase(LAS unsigned char* lds, const unsigned char* wsb, const unsigned lda, const unsigned ldb, const int nt, const Sched& S, const Epi& E) {
;     ...
;             PG8_LDB(B0, 0, 0); PG8_LDB(B1, 0, 1); PG8_SCHED; PG8_LDA(At, 0, 0); PG8_STAGEA(PG8_SA(1, 1), t + 1, 1, false);
;             if constexpr (GATHER) { if (last) {
;                 int tz = tid; asm volatile("" : "+v"(tz));
; #pragma unroll
;                 for (int i = 0; i < 2; ++i) { int R, C; stage_rc(tz * 16 + i * 8192, R, C);
; #pragma unroll
;                     for (int h = 0; h < 2; ++h) { const unsigned tk = (unsigned)tokt[h * HALF + R]; offC[h][i] = (tk < (unsigned)NTOK ? tk : (unsigned)(NTOK - 1)) * lda + (unsigned)C * 2u; } } } }
;             PG8_WAIT_V(8); PG8_WAIT_L(0); PG8_BAR; PG8_MMA(0, 0, At, B0); PG8_MMA(0, 1, At, B1); PG8_BAR; PG8_SCHED;
;             PG8_LDA(At, 0, 1); PG8_STAGE(PG8_SB(0, 0), b2, voffB); PG8_STAGE(PG8_SB(0, 1), b2 + hstepB, voffB); PG8_STAGEA(PG8_SA(0, 0), k2, 0, last);
;             PG8_WAIT_V(8); PG8_WAIT_L(0); PG8_BAR; PG8_MMA(1, 0, At, B0); PG8_MMA(1, 1, At, B1); PG8_BAR; PG8_SCHED;
.LBB0_2116:
	s_add_i32 s75, s71, 0xfffe0080
	s_cmp_eq_u32 s73, 4
	s_cselect_b32 s74, s68, s72
	s_cselect_b32 s75, s67, s75
	s_add_i32 s76, s74, 0x80
	s_add_u32 s78, s8, s71
	s_addc_u32 s79, s9, 0
	s_mov_b32 m0, s60
	v_lshl_add_u64 v[162:163], s[78:79], 0, v[168:169]
	global_load_lds_dwordx4 v[162:163], off
	v_lshl_add_u64 v[162:163], s[78:79], 0, v[166:167]
	s_mov_b32 m0, s61
	s_nop 0
	global_load_lds_dwordx4 v[162:163], off
	ds_read_b128 v[130:133], v200
	ds_read_b128 v[134:137], v200 offset:1024
	ds_read_b128 v[138:141], v200 offset:2048
	ds_read_b128 v[142:145], v200 offset:3072
	ds_read_b128 v[146:149], v200 offset:16384
	ds_read_b128 v[150:153], v200 offset:17408
	ds_read_b128 v[154:157], v200 offset:18432
	ds_read_b128 v[158:161], v200 offset:19456
	ds_read_b128 v[170:173], v199
	ds_read_b128 v[174:177], v199 offset:1024
	ds_read_b128 v[178:181], v199 offset:2048
	ds_read_b128 v[182:185], v199 offset:3072
	ds_read_b128 v[186:189], v199 offset:4096
	ds_read_b128 v[190:193], v199 offset:5120
	ds_read_b128 v[202:205], v199 offset:6144
	ds_read_b128 v[206:209], v199 offset:7168
	s_waitcnt vmcnt(8)
	s_waitcnt lgkmcnt(0)
	s_barrier
	s_waitcnt lgkmcnt(0)
	v_mfma_f32_16x16x128_f8f6f4 v[126:129], v[130:137], v[170:177], v[126:129]
	v_mfma_f32_16x16x128_f8f6f4 v[122:125], v[138:145], v[170:177], v[122:125]
	v_mfma_f32_16x16x128_f8f6f4 v[114:117], v[130:137], v[178:185], v[114:117]
	v_mfma_f32_16x16x128_f8f6f4 v[106:109], v[138:145], v[178:185], v[106:109]
	v_mfma_f32_16x16x128_f8f6f4 v[98:101], v[130:137], v[186:193], v[98:101]
	v_mfma_f32_16x16x128_f8f6f4 v[162:165], v[138:145], v[186:193], v[90:93]
	v_mfma_f32_16x16x128_f8f6f4 v[194:197], v[130:137], v[202:209], v[82:85]
	v_mfma_f32_16x16x128_f8f6f4 v[210:213], v[138:145], v[202:209], v[74:77]
	v_mfma_f32_16x16x128_f8f6f4 v[118:121], v[146:153], v[170:177], v[118:121]
	v_mfma_f32_16x16x128_f8f6f4 v[110:113], v[154:161], v[170:177], v[110:113]
	v_mfma_f32_16x16x128_f8f6f4 v[102:105], v[146:153], v[178:185], v[102:105]
	v_mfma_f32_16x16x128_f8f6f4 v[170:173], v[154:161], v[178:185], v[94:97]
	v_mfma_f32_16x16x128_f8f6f4 v[174:177], v[146:153], v[186:193], v[86:89]
	v_mfma_f32_16x16x128_f8f6f4 v[178:181], v[154:161], v[186:193], v[78:81]
	v_mfma_f32_16x16x128_f8f6f4 v[182:185], v[146:153], v[202:209], v[70:73]
	v_mfma_f32_16x16x128_f8f6f4 v[186:189], v[154:161], v[202:209], v[66:69]
	s_barrier
	s_add_u32 s78, s8, s74
	s_addc_u32 s79, s9, 0
	s_mov_b32 m0, s28
	v_lshl_add_u64 v[190:191], s[78:79], 0, v[168:169]
	s_add_i32 s77, s74, 0x20000
	global_load_lds_dwordx4 v[190:191], off
	v_lshl_add_u64 v[190:191], s[78:79], 0, v[166:167]
	s_add_u32 s78, s8, s77
	s_mov_b32 m0, s29
	s_addc_u32 s79, s9, 0
	global_load_lds_dwordx4 v[190:191], off
	v_lshl_add_u64 v[190:191], s[78:79], 0, v[168:169]
	s_mov_b32 m0, s46
	s_nop 0
	global_load_lds_dwordx4 v[190:191], off
	v_lshl_add_u64 v[190:191], s[78:79], 0, v[166:167]
	s_add_u32 s78, s8, s75
	s_mov_b32 m0, s47
	s_addc_u32 s79, s9, 0
	global_load_lds_dwordx4 v[190:191], off
	v_lshl_add_u64 v[190:191], s[78:79], 0, v[168:169]
	s_mov_b32 m0, s21
	s_nop 0
	global_load_lds_dwordx4 v[190:191], off
	v_lshl_add_u64 v[190:191], s[78:79], 0, v[166:167]
	s_mov_b32 m0, s48
	s_nop 0
	global_load_lds_dwordx4 v[190:191], off
	ds_read_b128 v[66:69], v199 offset:16384
	ds_read_b128 v[70:73], v199 offset:17408
	ds_read_b128 v[74:77], v199 offset:18432
	ds_read_b128 v[78:81], v199 offset:19456
	ds_read_b128 v[82:85], v199 offset:20480
	ds_read_b128 v[86:89], v199 offset:21504
	ds_read_b128 v[90:93], v199 offset:22528
	ds_read_b128 v[94:97], v199 offset:23552
	s_waitcnt vmcnt(8)
	s_waitcnt lgkmcnt(0)
	s_barrier
	s_waitcnt lgkmcnt(0)
	v_mfma_f32_16x16x128_f8f6f4 v[62:65], v[130:137], v[66:73], v[62:65]
	v_mfma_f32_16x16x128_f8f6f4 v[58:61], v[138:145], v[66:73], v[58:61]
	v_mfma_f32_16x16x128_f8f6f4 v[50:53], v[130:137], v[74:81], v[50:53]
	v_mfma_f32_16x16x128_f8f6f4 v[190:193], v[138:145], v[74:81], v[42:45]
	v_mfma_f32_16x16x128_f8f6f4 v[202:205], v[130:137], v[82:89], v[34:37]
	v_mfma_f32_16x16x128_f8f6f4 v[206:209], v[138:145], v[82:89], v[26:29]
	v_mfma_f32_16x16x128_f8f6f4 v[214:217], v[130:137], v[90:97], v[18:21]
	v_mfma_f32_16x16x128_f8f6f4 v[218:221], v[138:145], v[90:97], v[10:13]
	v_mfma_f32_16x16x128_f8f6f4 v[54:57], v[146:153], v[66:73], v[54:57]
	v_mfma_f32_16x16x128_f8f6f4 v[222:225], v[154:161], v[66:73], v[46:49]
	v_mfma_f32_16x16x128_f8f6f4 v[226:229], v[146:153], v[74:81], v[38:41]
	v_mfma_f32_16x16x128_f8f6f4 v[230:233], v[154:161], v[74:81], v[30:33]
	v_mfma_f32_16x16x128_f8f6f4 v[234:237], v[146:153], v[82:89], v[22:25]
	v_mfma_f32_16x16x128_f8f6f4 v[238:241], v[154:161], v[82:89], v[14:17]
	v_mfma_f32_16x16x128_f8f6f4 v[242:245], v[146:153], v[90:97], v[6:9]
	v_mfma_f32_16x16x128_f8f6f4 v[246:249], v[154:161], v[90:97], v[2:5]
	s_barrier
; #define PG8_STAGE(bufoff, gbase, voff) do { _Pragma("unroll") for (int _i = 0; _i < 2; ++_i) \
;         __builtin_amdgcn_global_load_lds((const unsigned*)(wsb + (size_t)(gbase) + (voff)[_i]), (LAS unsigned*)(lds + (bufoff) + ldsw + _i * 8192), 16, 0, 0); } while (0)
; #define PG8_LDA(dst, b, h) do { _Pragma("unroll") for (int m = 0; m < 4; ++m) { if constexpr (FP8) dst##8[m] = PG8_LD8(pa, PG8_SA(b, h) + m * 2048); \
;         else { _Pragma("unroll") for (int k = 0; k < 2; ++k) dst[m][k] = *(const LAS bf16x8*)(pa + PG8_SA(b, h) + m * 2048 + k * 1024); } } } while (0)
; #define PG8_LDB(dst, b, h) do { _Pragma("unroll") for (int n = 0; n < 2; ++n) { if constexpr (FP8) dst##8[n] = PG8_LD8(pb, PG8_SA(b, h) + n * 2048); \
;         else { _Pragma("unroll") for (int k = 0; k < 2; ++k) dst[n][k] = *(const LAS bf16x8*)(pb + PG8_SA(b, h) + n * 2048 + k * 1024); } } } while (0)
; #define PG8_WAIT_V(n) asm volatile("s_waitcnt vmcnt(" #n ")" ::: "memory")
; #define PG8_WAIT_L(n) asm volatile("s_waitcnt lgkmcnt(" #n ")" ::: "memory")
; #define PG8_BAR __builtin_amdgcn_s_barrier()
; #define PG8_SCHED __builtin_amdgcn_sched_barrier(0)
; template <class Epi, class Sched, bool PERM, bool FP8 = false, bool GATHER = false>
; DI void gemm_phase(LAS unsigned char* lds, const unsigned char* wsb, const unsigned lda, const unsigned ldb, const int nt, const Sched& S, const Epi& E) {
;     ...
;             PG8_LDB(B0, 1, 0); PG8_LDB(B1, 1, 1); PG8_SCHED; PG8_LDA(At, 1, 0); PG8_STAGEA(PG8_SA(0, 1), k2, 1, last);
;             PG8_WAIT_V(8); PG8_WAIT_L(0); PG8_BAR; PG8_MMA(0, 0, At, B0); PG8_MMA(0, 1, At, B1); PG8_BAR; PG8_SCHED;
;             PG8_LDA(At, 1, 1); PG8_STAGE(PG8_SB(1, 0), b3, voffB); PG8_STAGE(PG8_SB(1, 1), b3 + hstepB, voffB); PG8_STAGEA(PG8_SA(1, 0), k3, 0, last);
;             PG8_WAIT_V(8); PG8_WAIT_L(0); PG8_BAR; PG8_MMA(1, 0, At, B0); PG8_MMA(1, 1, At, B1); PG8_BAR; PG8_SCHED;
;         }
;         if (wr == 0) PG8_BAR;
	s_nop 4
	s_add_i32 s77, s75, 0x20000
	s_add_u32 s78, s8, s77
	s_addc_u32 s79, s9, 0
	s_mov_b32 m0, s49
	v_lshl_add_u64 v[66:67], s[78:79], 0, v[168:169]
	global_load_lds_dwordx4 v[66:67], off
	v_lshl_add_u64 v[66:67], s[78:79], 0, v[166:167]
	s_mov_b32 m0, s50
	s_nop 0
	global_load_lds_dwordx4 v[66:67], off
	ds_read_b128 v[2:5], v200 offset:32768
	ds_read_b128 v[6:9], v200 offset:33792
	ds_read_b128 v[10:13], v200 offset:34816
	ds_read_b128 v[14:17], v200 offset:35840
	ds_read_b128 v[130:133], v200 offset:49152
	ds_read_b128 v[134:137], v200 offset:50176
	ds_read_b128 v[138:141], v200 offset:51200
	ds_read_b128 v[142:145], v200 offset:52224
	ds_read_b128 v[18:21], v199 offset:32768
	ds_read_b128 v[22:25], v199 offset:33792
	ds_read_b128 v[26:29], v199 offset:34816
	ds_read_b128 v[30:33], v199 offset:35840
	ds_read_b128 v[34:37], v199 offset:36864
	ds_read_b128 v[38:41], v199 offset:37888
	ds_read_b128 v[42:45], v199 offset:38912
	ds_read_b128 v[46:49], v199 offset:39936
	s_waitcnt vmcnt(8)
	s_waitcnt lgkmcnt(0)
	s_barrier
	s_waitcnt lgkmcnt(0)
	v_mfma_f32_16x16x128_f8f6f4 v[126:129], v[2:9], v[18:25], v[126:129]
	v_mfma_f32_16x16x128_f8f6f4 v[122:125], v[10:17], v[18:25], v[122:125]
	v_mfma_f32_16x16x128_f8f6f4 v[114:117], v[2:9], v[26:33], v[114:117]
	v_mfma_f32_16x16x128_f8f6f4 v[106:109], v[10:17], v[26:33], v[106:109]
	v_mfma_f32_16x16x128_f8f6f4 v[98:101], v[2:9], v[34:41], v[98:101]
	v_mfma_f32_16x16x128_f8f6f4 v[90:93], v[10:17], v[34:41], v[162:165]
	v_mfma_f32_16x16x128_f8f6f4 v[82:85], v[2:9], v[42:49], v[194:197]
	v_mfma_f32_16x16x128_f8f6f4 v[74:77], v[10:17], v[42:49], v[210:213]
	v_mfma_f32_16x16x128_f8f6f4 v[118:121], v[130:137], v[18:25], v[118:121]
	v_mfma_f32_16x16x128_f8f6f4 v[110:113], v[138:145], v[18:25], v[110:113]
	v_mfma_f32_16x16x128_f8f6f4 v[102:105], v[130:137], v[26:33], v[102:105]
	v_mfma_f32_16x16x128_f8f6f4 v[94:97], v[138:145], v[26:33], v[170:173]
	v_mfma_f32_16x16x128_f8f6f4 v[86:89], v[130:137], v[34:41], v[174:177]
	v_mfma_f32_16x16x128_f8f6f4 v[78:81], v[138:145], v[34:41], v[178:181]
	v_mfma_f32_16x16x128_f8f6f4 v[70:73], v[130:137], v[42:49], v[182:185]
	v_mfma_f32_16x16x128_f8f6f4 v[66:69], v[138:145], v[42:49], v[186:189]
	s_barrier
	s_add_u32 s76, s8, s76
	s_addc_u32 s77, s9, 0
	s_mov_b32 m0, s52
	v_lshl_add_u64 v[18:19], s[76:77], 0, v[168:169]
	s_add_i32 s74, s74, 0x20080
	global_load_lds_dwordx4 v[18:19], off
	v_lshl_add_u64 v[18:19], s[76:77], 0, v[166:167]
	s_add_u32 s76, s8, s74
	s_mov_b32 m0, s53
	s_addc_u32 s77, s9, 0
	s_addk_i32 s75, 0x80
	global_load_lds_dwordx4 v[18:19], off
	v_lshl_add_u64 v[18:19], s[76:77], 0, v[168:169]
	s_mov_b32 m0, s56
	s_add_u32 s74, s8, s75
	global_load_lds_dwordx4 v[18:19], off
	v_lshl_add_u64 v[18:19], s[76:77], 0, v[166:167]
	s_mov_b32 m0, s57
	s_addc_u32 s75, s9, 0
	global_load_lds_dwordx4 v[18:19], off
	v_lshl_add_u64 v[18:19], s[74:75], 0, v[168:169]
	s_mov_b32 m0, s54
	s_nop 0
	global_load_lds_dwordx4 v[18:19], off
	v_lshl_add_u64 v[18:19], s[74:75], 0, v[166:167]
	s_mov_b32 m0, s55
	s_nop 0
	global_load_lds_dwordx4 v[18:19], off
	ds_read_b128 v[146:149], v199 offset:49152
	ds_read_b128 v[150:153], v199 offset:50176
	ds_read_b128 v[154:157], v199 offset:51200
	ds_read_b128 v[158:161], v199 offset:52224
	ds_read_b128 v[170:173], v199 offset:53248
	ds_read_b128 v[174:177], v199 offset:54272
	ds_read_b128 v[178:181], v199 offset:55296
	ds_read_b128 v[182:185], v199 offset:56320
	s_waitcnt vmcnt(8)
	s_waitcnt lgkmcnt(0)
	s_barrier
	s_waitcnt lgkmcnt(0)
	v_mfma_f32_16x16x128_f8f6f4 v[62:65], v[2:9], v[146:153], v[62:65]
	v_mfma_f32_16x16x128_f8f6f4 v[58:61], v[10:17], v[146:153], v[58:61]
	v_mfma_f32_16x16x128_f8f6f4 v[50:53], v[2:9], v[154:161], v[50:53]
	v_mfma_f32_16x16x128_f8f6f4 v[42:45], v[10:17], v[154:161], v[190:193]
	v_mfma_f32_16x16x128_f8f6f4 v[34:37], v[2:9], v[170:177], v[202:205]
	v_mfma_f32_16x16x128_f8f6f4 v[26:29], v[10:17], v[170:177], v[206:209]
	v_mfma_f32_16x16x128_f8f6f4 v[18:21], v[2:9], v[178:185], v[214:217]
	v_mfma_f32_16x16x128_f8f6f4 v[10:13], v[10:17], v[178:185], v[218:221]
	v_mfma_f32_16x16x128_f8f6f4 v[54:57], v[130:137], v[146:153], v[54:57]
	v_mfma_f32_16x16x128_f8f6f4 v[46:49], v[138:145], v[146:153], v[222:225]
	v_mfma_f32_16x16x128_f8f6f4 v[38:41], v[130:137], v[154:161], v[226:229]
	v_mfma_f32_16x16x128_f8f6f4 v[30:33], v[138:145], v[154:161], v[230:233]
	v_mfma_f32_16x16x128_f8f6f4 v[22:25], v[130:137], v[170:177], v[234:237]
	v_mfma_f32_16x16x128_f8f6f4 v[14:17], v[138:145], v[170:177], v[238:241]
	v_mfma_f32_16x16x128_f8f6f4 v[6:9], v[130:137], v[178:185], v[242:245]
	v_mfma_f32_16x16x128_f8f6f4 v[2:5], v[138:145], v[178:185], v[246:249]
	s_barrier
	s_add_i32 s73, s73, 2
	s_addk_i32 s71, 0x100
	s_addk_i32 s72, 0x100
	s_cmp_gt_u32 s73, 5
	s_cbranch_scc0 .LBB0_2116
	s_and_b64 vcc, exec, s[12:13]
	s_cbranch_vccz .LBB0_2119
	s_barrier

; #define PG8_STAGE(bufoff, gbase, voff) do { _Pragma("unroll") for (int _i = 0; _i < 2; ++_i) \
;         __builtin_amdgcn_global_load_lds((const unsigned*)(wsb + (size_t)(gbase) + (voff)[_i]), (LAS unsigned*)(lds + (bufoff) + ldsw + _i * 8192), 16, 0, 0); } while (0)
; #define PG8_LDA(dst, b, h) do { _Pragma("unroll") for (int m = 0; m < 4; ++m) { if constexpr (FP8) dst##8[m] = PG8_LD8(pa, PG8_SA(b, h) + m * 2048); \
;         else { _Pragma("unroll") for (int k = 0; k < 2; ++k) dst[m][k] = *(const LAS bf16x8*)(pa + PG8_SA(b, h) + m * 2048 + k * 1024); } } } while (0)
; #define PG8_WAIT_V(n) asm volatile("s_waitcnt vmcnt(" #n ")" ::: "memory")
; #define PG8_WAIT_L(n) asm volatile("s_waitcnt lgkmcnt(" #n ")" ::: "memory")
; #define PG8_BAR __builtin_amdgcn_s_barrier()
; #define PG8_SCHED __builtin_amdgcn_sched_barrier(0)
; template <class Epi, class Sched, bool PERM, bool FP8 = false, bool GATHER = false>
; DI void gemm_phase(LAS unsigned char* lds, const unsigned char* wsb, const unsigned lda, const unsigned ldb, const int nt, const Sched& S, const Epi& E) {
;     ...
;             PG8_WAIT_V(8); PG8_WAIT_L(0); PG8_BAR; PG8_MMA(0, 0, At, B0); PG8_MMA(0, 1, At, B1); PG8_BAR; PG8_SCHED;
;             PG8_LDA(At, 0, 1); PG8_STAGE(PG8_SB(0, 0), b2, voffB); PG8_STAGE(PG8_SB(0, 1), b2 + hstepB, voffB); PG8_STAGEA(PG8_SA(0, 0), k2, 0, last);
;             PG8_WAIT_V(8); PG8_WAIT_L(0); PG8_BAR; PG8_MMA(1, 0, At, B0); PG8_MMA(1, 1, At, B1); PG8_BAR; PG8_SCHED;
.LBB0_2544:
	s_waitcnt vmcnt(8)
	s_add_i32 s84, s80, s44
	s_waitcnt lgkmcnt(0)
	s_and_b64 s[82:83], s[46:47], exec
	s_cselect_b32 s82, s12, s84
	v_mov_b32_e32 v205, v197
	s_add_i32 s83, s82, 0x80
	s_barrier
	s_waitcnt lgkmcnt(0)
	v_mfma_f32_16x16x128_f8f6f4 v[190:193], v[18:25], v[58:65], v[190:193]
	v_mfma_f32_16x16x128_f8f6f4 v[186:189], v[26:33], v[58:65], v[186:189]
	v_mfma_f32_16x16x128_f8f6f4 v[174:177], v[18:25], v[50:57], v[174:177]
	v_mfma_f32_16x16x128_f8f6f4 v[166:169], v[26:33], v[50:57], v[166:169]
	v_mfma_f32_16x16x128_f8f6f4 v[158:161], v[18:25], v[42:49], v[158:161]
	v_mfma_f32_16x16x128_f8f6f4 v[150:153], v[26:33], v[42:49], v[150:153]
	v_mfma_f32_16x16x128_f8f6f4 v[142:145], v[18:25], v[34:41], v[142:145]
	v_mfma_f32_16x16x128_f8f6f4 v[134:137], v[26:33], v[34:41], v[134:137]
	v_mfma_f32_16x16x128_f8f6f4 v[182:185], v[2:9], v[58:65], v[182:185]
	v_mfma_f32_16x16x128_f8f6f4 v[178:181], v[10:17], v[58:65], v[178:181]
	v_mfma_f32_16x16x128_f8f6f4 v[170:173], v[2:9], v[50:57], v[170:173]
	v_mfma_f32_16x16x128_f8f6f4 v[162:165], v[10:17], v[50:57], v[162:165]
	v_mfma_f32_16x16x128_f8f6f4 v[154:157], v[2:9], v[42:49], v[154:157]
	v_mfma_f32_16x16x128_f8f6f4 v[146:149], v[10:17], v[42:49], v[146:149]
	v_mfma_f32_16x16x128_f8f6f4 v[138:141], v[2:9], v[34:41], v[138:141]
	v_mfma_f32_16x16x128_f8f6f4 v[130:133], v[10:17], v[34:41], v[130:133]
	s_barrier
	s_add_u32 s84, s8, s82
	s_addc_u32 s85, s9, 0
	s_mov_b32 m0, s48
	v_lshl_add_u64 v[214:215], s[84:85], 0, v[198:199]
	global_load_lds_dwordx4 v[214:215], off
	v_lshl_add_u64 v[214:215], s[84:85], 0, v[200:201]
	s_add_i32 s84, s82, 0x20000
	s_add_u32 s84, s8, s84
	s_addc_u32 s85, s9, 0
	s_add_u32 s44, s44, 0x100
	s_mov_b32 m0, s49
	s_addc_u32 s45, s45, 0
	global_load_lds_dwordx4 v[214:215], off
	v_lshl_add_u64 v[214:215], s[84:85], 0, v[198:199]
	s_mov_b32 m0, s50
	s_and_b64 s[46:47], s[46:47], exec
	global_load_lds_dwordx4 v[214:215], off
	v_lshl_add_u64 v[214:215], s[84:85], 0, v[200:201]
	s_cselect_b32 s84, 0, s44
	s_mov_b32 m0, s51
	s_add_u32 s46, s10, s84
	global_load_lds_dwordx4 v[214:215], off
	s_addc_u32 s47, s11, 0
	s_mov_b32 m0, s39
	s_nop 0
	global_load_lds_dwordx4 v212, s[46:47]
	s_mov_b32 m0, s52
	s_nop 0
	global_load_lds_dwordx4 v202, s[46:47]
	ds_read_b128 v[34:37], v209 offset:16384
	ds_read_b128 v[38:41], v209 offset:17408
	ds_read_b128 v[42:45], v209 offset:18432
	ds_read_b128 v[46:49], v209 offset:19456
	ds_read_b128 v[50:53], v209 offset:20480
	ds_read_b128 v[54:57], v209 offset:21504
	ds_read_b128 v[58:61], v209 offset:22528
	ds_read_b128 v[62:65], v209 offset:23552
	s_waitcnt vmcnt(8)
	s_waitcnt lgkmcnt(0)
	s_barrier
	s_waitcnt lgkmcnt(0)
	v_mfma_f32_16x16x128_f8f6f4 v[126:129], v[18:25], v[34:41], v[126:129]
	v_mfma_f32_16x16x128_f8f6f4 v[118:121], v[26:33], v[34:41], v[118:121]
	v_mfma_f32_16x16x128_f8f6f4 v[110:113], v[18:25], v[42:49], v[110:113]
	v_mfma_f32_16x16x128_f8f6f4 v[102:105], v[26:33], v[42:49], v[102:105]
	v_mfma_f32_16x16x128_f8f6f4 v[94:97], v[18:25], v[50:57], v[94:97]
	v_mfma_f32_16x16x128_f8f6f4 v[86:89], v[26:33], v[50:57], v[86:89]
	v_mfma_f32_16x16x128_f8f6f4 v[78:81], v[18:25], v[58:65], v[78:81]
	v_mfma_f32_16x16x128_f8f6f4 v[70:73], v[26:33], v[58:65], v[70:73]
	v_mfma_f32_16x16x128_f8f6f4 v[122:125], v[2:9], v[34:41], v[122:125]
	v_mfma_f32_16x16x128_f8f6f4 v[114:117], v[10:17], v[34:41], v[114:117]
	v_mfma_f32_16x16x128_f8f6f4 v[106:109], v[2:9], v[42:49], v[106:109]
	v_mfma_f32_16x16x128_f8f6f4 v[98:101], v[10:17], v[42:49], v[98:101]
	v_mfma_f32_16x16x128_f8f6f4 v[90:93], v[2:9], v[50:57], v[90:93]
	v_mfma_f32_16x16x128_f8f6f4 v[82:85], v[10:17], v[50:57], v[82:85]
	v_mfma_f32_16x16x128_f8f6f4 v[74:77], v[2:9], v[58:65], v[74:77]
	v_mfma_f32_16x16x128_f8f6f4 v[66:69], v[10:17], v[58:65], v[66:69]
	s_barrier
; #define PG8_STAGE(bufoff, gbase, voff) do { _Pragma("unroll") for (int _i = 0; _i < 2; ++_i) \
;         __builtin_amdgcn_global_load_lds((const unsigned*)(wsb + (size_t)(gbase) + (voff)[_i]), (LAS unsigned*)(lds + (bufoff) + ldsw + _i * 8192), 16, 0, 0); } while (0)
; #define PG8_LDA(dst, b, h) do { _Pragma("unroll") for (int m = 0; m < 4; ++m) { if constexpr (FP8) dst##8[m] = PG8_LD8(pa, PG8_SA(b, h) + m * 2048); \
;         else { _Pragma("unroll") for (int k = 0; k < 2; ++k) dst[m][k] = *(const LAS bf16x8*)(pa + PG8_SA(b, h) + m * 2048 + k * 1024); } } } while (0)
; #define PG8_LDB(dst, b, h) do { _Pragma("unroll") for (int n = 0; n < 2; ++n) { if constexpr (FP8) dst##8[n] = PG8_LD8(pb, PG8_SA(b, h) + n * 2048); \
;         else { _Pragma("unroll") for (int k = 0; k < 2; ++k) dst[n][k] = *(const LAS bf16x8*)(pb + PG8_SA(b, h) + n * 2048 + k * 1024); } } } while (0)
; #define PG8_WAIT_V(n) asm volatile("s_waitcnt vmcnt(" #n ")" ::: "memory")
; #define PG8_WAIT_L(n) asm volatile("s_waitcnt lgkmcnt(" #n ")" ::: "memory")
; #define PG8_BAR __builtin_amdgcn_s_barrier()
; #define PG8_SCHED __builtin_amdgcn_sched_barrier(0)
; template <class Epi, class Sched, bool PERM, bool FP8 = false, bool GATHER = false>
; DI void gemm_phase(LAS unsigned char* lds, const unsigned char* wsb, const unsigned lda, const unsigned ldb, const int nt, const Sched& S, const Epi& E) {
;     ...
;             PG8_LDB(B0, 1, 0); PG8_LDB(B1, 1, 1); PG8_SCHED; PG8_LDA(At, 1, 0); PG8_STAGEA(PG8_SA(0, 1), k2, 1, last);
;             PG8_WAIT_V(8); PG8_WAIT_L(0); PG8_BAR; PG8_MMA(0, 0, At, B0); PG8_MMA(0, 1, At, B1); PG8_BAR; PG8_SCHED;
;             PG8_LDA(At, 1, 1); PG8_STAGE(PG8_SB(1, 0), b3, voffB); PG8_STAGE(PG8_SB(1, 1), b3 + hstepB, voffB); PG8_STAGEA(PG8_SA(1, 0), k3, 0, last);
;             PG8_WAIT_V(8); PG8_WAIT_L(0); PG8_BAR; PG8_MMA(1, 0, At, B0); PG8_MMA(1, 1, At, B1); PG8_BAR; PG8_SCHED;
;         }
	s_mov_b32 m0, s53
	v_lshl_add_u64 v[214:215], s[46:47], 0, v[196:197]
	global_load_lds_dwordx4 v[214:215], off
	v_lshl_add_u64 v[214:215], s[46:47], 0, v[204:205]
	s_mov_b32 m0, s54
	s_nop 0
	global_load_lds_dwordx4 v[214:215], off
	ds_read_b128 v[2:5], v210 offset:32768
	ds_read_b128 v[6:9], v210 offset:33792
	ds_read_b128 v[10:13], v210 offset:34816
	ds_read_b128 v[14:17], v210 offset:35840
	ds_read_b128 v[18:21], v210 offset:49152
	ds_read_b128 v[22:25], v210 offset:50176
	ds_read_b128 v[26:29], v210 offset:51200
	ds_read_b128 v[30:33], v210 offset:52224
	ds_read_b128 v[34:37], v209 offset:32768
	ds_read_b128 v[38:41], v209 offset:33792
	ds_read_b128 v[42:45], v209 offset:34816
	ds_read_b128 v[46:49], v209 offset:35840
	ds_read_b128 v[50:53], v209 offset:36864
	ds_read_b128 v[54:57], v209 offset:37888
	ds_read_b128 v[58:61], v209 offset:38912
	ds_read_b128 v[62:65], v209 offset:39936
	s_waitcnt vmcnt(8)
	s_waitcnt lgkmcnt(0)
	s_barrier
	s_waitcnt lgkmcnt(0)
	v_mfma_f32_16x16x128_f8f6f4 v[190:193], v[2:9], v[34:41], v[190:193]
	v_mfma_f32_16x16x128_f8f6f4 v[186:189], v[10:17], v[34:41], v[186:189]
	v_mfma_f32_16x16x128_f8f6f4 v[174:177], v[2:9], v[42:49], v[174:177]
	v_mfma_f32_16x16x128_f8f6f4 v[166:169], v[10:17], v[42:49], v[166:169]
	v_mfma_f32_16x16x128_f8f6f4 v[158:161], v[2:9], v[50:57], v[158:161]
	v_mfma_f32_16x16x128_f8f6f4 v[150:153], v[10:17], v[50:57], v[150:153]
	v_mfma_f32_16x16x128_f8f6f4 v[142:145], v[2:9], v[58:65], v[142:145]
	v_mfma_f32_16x16x128_f8f6f4 v[134:137], v[10:17], v[58:65], v[134:137]
	v_mfma_f32_16x16x128_f8f6f4 v[182:185], v[18:25], v[34:41], v[182:185]
	v_mfma_f32_16x16x128_f8f6f4 v[178:181], v[26:33], v[34:41], v[178:181]
	v_mfma_f32_16x16x128_f8f6f4 v[170:173], v[18:25], v[42:49], v[170:173]
	v_mfma_f32_16x16x128_f8f6f4 v[162:165], v[26:33], v[42:49], v[162:165]
	v_mfma_f32_16x16x128_f8f6f4 v[154:157], v[18:25], v[50:57], v[154:157]
	v_mfma_f32_16x16x128_f8f6f4 v[146:149], v[26:33], v[50:57], v[146:149]
	v_mfma_f32_16x16x128_f8f6f4 v[138:141], v[18:25], v[58:65], v[138:141]
	v_mfma_f32_16x16x128_f8f6f4 v[130:133], v[26:33], v[58:65], v[130:133]
	s_barrier
	s_add_u32 s46, s8, s83
	s_addc_u32 s47, s9, 0
	s_mov_b32 m0, s58
	v_lshl_add_u64 v[214:215], s[46:47], 0, v[198:199]
	s_add_i32 s82, s82, 0x20080
	global_load_lds_dwordx4 v[214:215], off
	v_lshl_add_u64 v[214:215], s[46:47], 0, v[200:201]
	s_add_u32 s46, s8, s82
	s_mov_b32 m0, s59
	s_addc_u32 s47, s9, 0
	global_load_lds_dwordx4 v[214:215], off
	v_lshl_add_u64 v[214:215], s[46:47], 0, v[198:199]
	s_mov_b32 m0, s64
	s_nop 0
	global_load_lds_dwordx4 v[214:215], off
	v_lshl_add_u64 v[214:215], s[46:47], 0, v[200:201]
	s_add_u32 s46, s8, s84
	s_addc_u32 s47, s9, 0
	s_mov_b32 m0, s65
	s_add_u32 s46, s46, 0x5b9d4080
	global_load_lds_dwordx4 v[214:215], off
	s_addc_u32 s47, s47, 0
	s_mov_b32 m0, s60
	s_nop 0
	global_load_lds_dwordx4 v212, s[46:47]
	s_mov_b32 m0, s61
	s_nop 0
	global_load_lds_dwordx4 v202, s[46:47]
	ds_read_b128 v[34:37], v209 offset:49152
	ds_read_b128 v[38:41], v209 offset:50176
	ds_read_b128 v[42:45], v209 offset:51200
	ds_read_b128 v[46:49], v209 offset:52224
	ds_read_b128 v[50:53], v209 offset:53248
	ds_read_b128 v[54:57], v209 offset:54272
	ds_read_b128 v[58:61], v209 offset:55296
	ds_read_b128 v[62:65], v209 offset:56320
	s_waitcnt vmcnt(8)
	s_waitcnt lgkmcnt(0)
	s_barrier
	s_waitcnt lgkmcnt(0)
	v_mfma_f32_16x16x128_f8f6f4 v[126:129], v[2:9], v[34:41], v[126:129]
	v_mfma_f32_16x16x128_f8f6f4 v[118:121], v[10:17], v[34:41], v[118:121]
	v_mfma_f32_16x16x128_f8f6f4 v[110:113], v[2:9], v[42:49], v[110:113]
	v_mfma_f32_16x16x128_f8f6f4 v[102:105], v[10:17], v[42:49], v[102:105]
	v_mfma_f32_16x16x128_f8f6f4 v[94:97], v[2:9], v[50:57], v[94:97]
	v_mfma_f32_16x16x128_f8f6f4 v[86:89], v[10:17], v[50:57], v[86:89]
	v_mfma_f32_16x16x128_f8f6f4 v[78:81], v[2:9], v[58:65], v[78:81]
	v_mfma_f32_16x16x128_f8f6f4 v[70:73], v[10:17], v[58:65], v[70:73]
	v_mfma_f32_16x16x128_f8f6f4 v[122:125], v[18:25], v[34:41], v[122:125]
	v_mfma_f32_16x16x128_f8f6f4 v[114:117], v[26:33], v[34:41], v[114:117]
	v_mfma_f32_16x16x128_f8f6f4 v[106:109], v[18:25], v[42:49], v[106:109]
	v_mfma_f32_16x16x128_f8f6f4 v[98:101], v[26:33], v[42:49], v[98:101]
	v_mfma_f32_16x16x128_f8f6f4 v[90:93], v[18:25], v[50:57], v[90:93]
	v_mfma_f32_16x16x128_f8f6f4 v[82:85], v[26:33], v[50:57], v[82:85]
	v_mfma_f32_16x16x128_f8f6f4 v[74:77], v[18:25], v[58:65], v[74:77]
	v_mfma_f32_16x16x128_f8f6f4 v[66:69], v[26:33], v[58:65], v[66:69]
	s_barrier
	s_add_i32 s81, s81, 2
	s_cmp_gt_u32 s81, 5
	s_cbranch_scc1 .LBB0_2547

; #define PG8_STAGE(bufoff, gbase, voff) do { _Pragma("unroll") for (int _i = 0; _i < 2; ++_i) \
;         __builtin_amdgcn_global_load_lds((const unsigned*)(wsb + (size_t)(gbase) + (voff)[_i]), (LAS unsigned*)(lds + (bufoff) + ldsw + _i * 8192), 16, 0, 0); } while (0)
; #define PG8_LDA(dst, b, h) do { _Pragma("unroll") for (int m = 0; m < 4; ++m) { if constexpr (FP8) dst##8[m] = PG8_LD8(pa, PG8_SA(b, h) + m * 2048); \
;         else { _Pragma("unroll") for (int k = 0; k < 2; ++k) dst[m][k] = *(const LAS bf16x8*)(pa + PG8_SA(b, h) + m * 2048 + k * 1024); } } } while (0)
; #define PG8_LDB(dst, b, h) do { _Pragma("unroll") for (int n = 0; n < 2; ++n) { if constexpr (FP8) dst##8[n] = PG8_LD8(pb, PG8_SA(b, h) + n * 2048); \
;         else { _Pragma("unroll") for (int k = 0; k < 2; ++k) dst[n][k] = *(const LAS bf16x8*)(pb + PG8_SA(b, h) + n * 2048 + k * 1024); } } } while (0)
; #define PG8_WAIT_V(n) asm volatile("s_waitcnt vmcnt(" #n ")" ::: "memory")
; #define PG8_WAIT_L(n) asm volatile("s_waitcnt lgkmcnt(" #n ")" ::: "memory")
; #define PG8_BAR __builtin_amdgcn_s_barrier()
; #define PG8_SCHED __builtin_amdgcn_sched_barrier(0)
; template <class Epi, class Sched, bool PERM, bool FP8 = false, bool GATHER = false>
; DI void gemm_phase(LAS unsigned char* lds, const unsigned char* wsb, const unsigned lda, const unsigned ldb, const int nt, const Sched& S, const Epi& E) {
;     ...
;             PG8_LDB(B0, 0, 0); PG8_LDB(B1, 0, 1); PG8_SCHED; PG8_LDA(At, 0, 0); PG8_STAGEA(PG8_SA(1, 1), t + 1, 1, false);
;             if constexpr (GATHER) { if (last) {
;                 int tz = tid; asm volatile("" : "+v"(tz));
; #pragma unroll
;                 for (int i = 0; i < 2; ++i) { int R, C; stage_rc(tz * 16 + i * 8192, R, C);
; #pragma unroll
;                     for (int h = 0; h < 2; ++h) { const unsigned tk = (unsigned)tokt[h * HALF + R]; offC[h][i] = (tk < (unsigned)NTOK ? tk : (unsigned)(NTOK - 1)) * lda + (unsigned)C * 2u; } } } }
;             PG8_WAIT_V(8); PG8_WAIT_L(0); PG8_BAR; PG8_MMA(0, 0, At, B0); PG8_MMA(0, 1, At, B1); PG8_BAR; PG8_SCHED;
;             PG8_LDA(At, 0, 1); PG8_STAGE(PG8_SB(0, 0), b2, voffB); PG8_STAGE(PG8_SB(0, 1), b2 + hstepB, voffB); PG8_STAGEA(PG8_SA(0, 0), k2, 0, last);
;             PG8_WAIT_V(8); PG8_WAIT_L(0); PG8_BAR; PG8_MMA(1, 0, At, B0); PG8_MMA(1, 1, At, B1); PG8_BAR; PG8_SCHED;
.LBB0_2652:
	ds_read_b128 v[130:133], v154
	ds_read_b128 v[134:137], v154 offset:1024
	ds_read_b128 v[138:141], v154 offset:2048
	ds_read_b128 v[142:145], v154 offset:3072
	ds_read_b128 v[158:161], v154 offset:16384
	ds_read_b128 v[162:165], v154 offset:17408
	ds_read_b128 v[166:169], v154 offset:18432
	ds_read_b128 v[170:173], v154 offset:19456
	s_add_i32 s70, s67, 0xfffe0080
	s_add_i32 s71, s70, s64
	s_cmp_eq_u32 s66, 4
	s_cselect_b64 s[24:25], -1, 0
	s_and_b64 s[68:69], s[24:25], exec
	s_cselect_b32 s68, s65, s71
	s_cselect_b32 s72, 0, s70
	s_add_i32 s69, s68, 0x80
	s_add_i32 s70, s62, s67
	s_add_u32 s70, s8, s70
	s_addc_u32 s71, s9, 0
	v_lshl_add_u64 v[150:151], s[70:71], 0, v[146:147]
	s_add_i32 m0, s26, 0xc000
	ds_read_b128 v[174:177], v153
	ds_read_b128 v[178:181], v153 offset:1024
	ds_read_b128 v[182:185], v153 offset:2048
	ds_read_b128 v[186:189], v153 offset:3072
	ds_read_b128 v[190:193], v153 offset:4096
	ds_read_b128 v[194:197], v153 offset:5120
	ds_read_b128 v[198:201], v153 offset:6144
	ds_read_b128 v[202:205], v153 offset:7168
	global_load_lds_dwordx4 v[150:151], off
	v_lshl_add_u64 v[150:151], s[70:71], 0, v[148:149]
	s_add_i32 m0, s26, 0xe000
	s_nop 0
	global_load_lds_dwordx4 v[150:151], off
	s_waitcnt vmcnt(8)
	s_waitcnt lgkmcnt(0)
	s_barrier
	s_waitcnt lgkmcnt(0)
	v_mfma_f32_16x16x128_f8f6f4 v[126:129], v[130:137], v[174:181], v[126:129]
	v_mfma_f32_16x16x128_f8f6f4 v[122:125], v[138:145], v[174:181], v[122:125]
	v_mfma_f32_16x16x128_f8f6f4 v[118:121], v[130:137], v[182:189], v[118:121]
	v_mfma_f32_16x16x128_f8f6f4 v[114:117], v[138:145], v[182:189], v[114:117]
	v_mfma_f32_16x16x128_f8f6f4 v[206:209], v[130:137], v[190:197], v[94:97]
	v_mfma_f32_16x16x128_f8f6f4 v[210:213], v[138:145], v[190:197], v[90:93]
	v_mfma_f32_16x16x128_f8f6f4 v[214:217], v[130:137], v[198:205], v[82:85]
	v_mfma_f32_16x16x128_f8f6f4 v[218:221], v[138:145], v[198:205], v[74:77]
	v_mfma_f32_16x16x128_f8f6f4 v[110:113], v[158:165], v[174:181], v[110:113]
	v_mfma_f32_16x16x128_f8f6f4 v[106:109], v[166:173], v[174:181], v[106:109]
	v_mfma_f32_16x16x128_f8f6f4 v[102:105], v[158:165], v[182:189], v[102:105]
	v_mfma_f32_16x16x128_f8f6f4 v[98:101], v[166:173], v[182:189], v[98:101]
	v_mfma_f32_16x16x128_f8f6f4 v[174:177], v[158:165], v[190:197], v[86:89]
	v_mfma_f32_16x16x128_f8f6f4 v[178:181], v[166:173], v[190:197], v[78:81]
	v_mfma_f32_16x16x128_f8f6f4 v[182:185], v[158:165], v[198:205], v[70:73]
	v_mfma_f32_16x16x128_f8f6f4 v[186:189], v[166:173], v[198:205], v[66:69]
	s_barrier
	s_add_u32 s70, s8, s68
	s_addc_u32 s71, s9, 0
	s_mov_b32 m0, s27
	v_lshl_add_u64 v[150:151], s[70:71], 0, v[146:147]
	s_nop 0
	global_load_lds_dwordx4 v[150:151], off
	v_lshl_add_u64 v[150:151], s[70:71], 0, v[148:149]
	s_add_i32 s70, s68, 0x20000
	s_add_u32 s70, s8, s70
	s_addc_u32 s71, s9, 0
	s_and_b64 s[24:25], s[20:21], s[24:25]
	s_and_b64 s[24:25], s[24:25], exec
	s_mov_b32 m0, s28
	s_cselect_b32 s24, s58, s62
	global_load_lds_dwordx4 v[150:151], off
	v_lshl_add_u64 v[150:151], s[70:71], 0, v[146:147]
	s_mov_b32 m0, s29
	s_add_i32 s24, s72, s24
	global_load_lds_dwordx4 v[150:151], off
	v_lshl_add_u64 v[150:151], s[70:71], 0, v[148:149]
	s_add_u32 s70, s8, s24
	s_mov_b32 m0, s36
	s_addc_u32 s71, s9, 0
	global_load_lds_dwordx4 v[150:151], off
	v_lshl_add_u64 v[150:151], s[70:71], 0, v[146:147]
	s_mov_b32 m0, s26
	s_nop 0
	global_load_lds_dwordx4 v[150:151], off
	v_lshl_add_u64 v[150:151], s[70:71], 0, v[148:149]
	s_mov_b32 m0, s37
	s_nop 0
	global_load_lds_dwordx4 v[150:151], off
	ds_read_b128 v[66:69], v153 offset:16384
	ds_read_b128 v[70:73], v153 offset:17408
	ds_read_b128 v[74:77], v153 offset:18432
	ds_read_b128 v[78:81], v153 offset:19456
	ds_read_b128 v[82:85], v153 offset:20480
	ds_read_b128 v[86:89], v153 offset:21504
	ds_read_b128 v[90:93], v153 offset:22528
	ds_read_b128 v[94:97], v153 offset:23552
	s_waitcnt vmcnt(8)
	s_waitcnt lgkmcnt(0)
	s_barrier
	s_waitcnt lgkmcnt(0)
	v_mfma_f32_16x16x128_f8f6f4 v[62:65], v[130:137], v[66:73], v[62:65]
	v_mfma_f32_16x16x128_f8f6f4 v[58:61], v[138:145], v[66:73], v[58:61]
	v_mfma_f32_16x16x128_f8f6f4 v[50:53], v[130:137], v[74:81], v[50:53]
	v_mfma_f32_16x16x128_f8f6f4 v[190:193], v[138:145], v[74:81], v[42:45]
	v_mfma_f32_16x16x128_f8f6f4 v[194:197], v[130:137], v[82:89], v[34:37]
	v_mfma_f32_16x16x128_f8f6f4 v[198:201], v[138:145], v[82:89], v[26:29]
	v_mfma_f32_16x16x128_f8f6f4 v[202:205], v[130:137], v[90:97], v[18:21]
	v_mfma_f32_16x16x128_f8f6f4 v[222:225], v[138:145], v[90:97], v[10:13]
	v_mfma_f32_16x16x128_f8f6f4 v[54:57], v[158:165], v[66:73], v[54:57]
	v_mfma_f32_16x16x128_f8f6f4 v[226:229], v[166:173], v[66:73], v[46:49]
	v_mfma_f32_16x16x128_f8f6f4 v[230:233], v[158:165], v[74:81], v[38:41]
	v_mfma_f32_16x16x128_f8f6f4 v[234:237], v[166:173], v[74:81], v[30:33]
	v_mfma_f32_16x16x128_f8f6f4 v[238:241], v[158:165], v[82:89], v[22:25]
	v_mfma_f32_16x16x128_f8f6f4 v[242:245], v[166:173], v[82:89], v[14:17]
	v_mfma_f32_16x16x128_f8f6f4 v[246:249], v[158:165], v[90:97], v[6:9]
	v_mfma_f32_16x16x128_f8f6f4 v[250:253], v[166:173], v[90:97], v[2:5]
	s_barrier
; #define PG8_STAGE(bufoff, gbase, voff) do { _Pragma("unroll") for (int _i = 0; _i < 2; ++_i) \
;         __builtin_amdgcn_global_load_lds((const unsigned*)(wsb + (size_t)(gbase) + (voff)[_i]), (LAS unsigned*)(lds + (bufoff) + ldsw + _i * 8192), 16, 0, 0); } while (0)
; #define PG8_LDA(dst, b, h) do { _Pragma("unroll") for (int m = 0; m < 4; ++m) { if constexpr (FP8) dst##8[m] = PG8_LD8(pa, PG8_SA(b, h) + m * 2048); \
;         else { _Pragma("unroll") for (int k = 0; k < 2; ++k) dst[m][k] = *(const LAS bf16x8*)(pa + PG8_SA(b, h) + m * 2048 + k * 1024); } } } while (0)
; #define PG8_LDB(dst, b, h) do { _Pragma("unroll") for (int n = 0; n < 2; ++n) { if constexpr (FP8) dst##8[n] = PG8_LD8(pb, PG8_SA(b, h) + n * 2048); \
;         else { _Pragma("unroll") for (int k = 0; k < 2; ++k) dst[n][k] = *(const LAS bf16x8*)(pb + PG8_SA(b, h) + n * 2048 + k * 1024); } } } while (0)
; #define PG8_WAIT_V(n) asm volatile("s_waitcnt vmcnt(" #n ")" ::: "memory")
; #define PG8_WAIT_L(n) asm volatile("s_waitcnt lgkmcnt(" #n ")" ::: "memory")
; #define PG8_BAR __builtin_amdgcn_s_barrier()
; #define PG8_SCHED __builtin_amdgcn_sched_barrier(0)
; template <class Epi, class Sched, bool PERM, bool FP8 = false, bool GATHER = false>
; DI void gemm_phase(LAS unsigned char* lds, const unsigned char* wsb, const unsigned lda, const unsigned ldb, const int nt, const Sched& S, const Epi& E) {
;     ...
;             PG8_LDB(B0, 1, 0); PG8_LDB(B1, 1, 1); PG8_SCHED; PG8_LDA(At, 1, 0); PG8_STAGEA(PG8_SA(0, 1), k2, 1, last);
;             PG8_WAIT_V(8); PG8_WAIT_L(0); PG8_BAR; PG8_MMA(0, 0, At, B0); PG8_MMA(0, 1, At, B1); PG8_BAR; PG8_SCHED;
;             PG8_LDA(At, 1, 1); PG8_STAGE(PG8_SB(1, 0), b3, voffB); PG8_STAGE(PG8_SB(1, 1), b3 + hstepB, voffB); PG8_STAGEA(PG8_SA(1, 0), k3, 0, last);
;             PG8_WAIT_V(8); PG8_WAIT_L(0); PG8_BAR; PG8_MMA(1, 0, At, B0); PG8_MMA(1, 1, At, B1); PG8_BAR; PG8_SCHED;
;         }
	s_nop 4
	s_add_i32 s25, s24, 0x20000
	s_add_u32 s70, s8, s25
	s_addc_u32 s71, s9, 0
	s_mov_b32 m0, s38
	v_lshl_add_u64 v[66:67], s[70:71], 0, v[146:147]
	global_load_lds_dwordx4 v[66:67], off
	v_lshl_add_u64 v[66:67], s[70:71], 0, v[148:149]
	s_mov_b32 m0, s39
	s_nop 0
	global_load_lds_dwordx4 v[66:67], off
	ds_read_b128 v[2:5], v154 offset:32768
	ds_read_b128 v[6:9], v154 offset:33792
	ds_read_b128 v[10:13], v154 offset:34816
	ds_read_b128 v[14:17], v154 offset:35840
	ds_read_b128 v[130:133], v154 offset:49152
	ds_read_b128 v[134:137], v154 offset:50176
	ds_read_b128 v[138:141], v154 offset:51200
	ds_read_b128 v[142:145], v154 offset:52224
	ds_read_b128 v[18:21], v153 offset:32768
	ds_read_b128 v[22:25], v153 offset:33792
	ds_read_b128 v[26:29], v153 offset:34816
	ds_read_b128 v[30:33], v153 offset:35840
	ds_read_b128 v[34:37], v153 offset:36864
	ds_read_b128 v[38:41], v153 offset:37888
	ds_read_b128 v[42:45], v153 offset:38912
	ds_read_b128 v[46:49], v153 offset:39936
	s_waitcnt vmcnt(8)
	s_waitcnt lgkmcnt(0)
	s_barrier
	s_waitcnt lgkmcnt(0)
	v_mfma_f32_16x16x128_f8f6f4 v[126:129], v[2:9], v[18:25], v[126:129]
	v_mfma_f32_16x16x128_f8f6f4 v[122:125], v[10:17], v[18:25], v[122:125]
	v_mfma_f32_16x16x128_f8f6f4 v[118:121], v[2:9], v[26:33], v[118:121]
	v_mfma_f32_16x16x128_f8f6f4 v[114:117], v[10:17], v[26:33], v[114:117]
	v_mfma_f32_16x16x128_f8f6f4 v[94:97], v[2:9], v[34:41], v[206:209]
	v_mfma_f32_16x16x128_f8f6f4 v[90:93], v[10:17], v[34:41], v[210:213]
	v_mfma_f32_16x16x128_f8f6f4 v[82:85], v[2:9], v[42:49], v[214:217]
	v_mfma_f32_16x16x128_f8f6f4 v[74:77], v[10:17], v[42:49], v[218:221]
	v_mfma_f32_16x16x128_f8f6f4 v[110:113], v[130:137], v[18:25], v[110:113]
	v_mfma_f32_16x16x128_f8f6f4 v[106:109], v[138:145], v[18:25], v[106:109]
	v_mfma_f32_16x16x128_f8f6f4 v[102:105], v[130:137], v[26:33], v[102:105]
	v_mfma_f32_16x16x128_f8f6f4 v[98:101], v[138:145], v[26:33], v[98:101]
	v_mfma_f32_16x16x128_f8f6f4 v[86:89], v[130:137], v[34:41], v[174:177]
	v_mfma_f32_16x16x128_f8f6f4 v[78:81], v[138:145], v[34:41], v[178:181]
	v_mfma_f32_16x16x128_f8f6f4 v[70:73], v[130:137], v[42:49], v[182:185]
	v_mfma_f32_16x16x128_f8f6f4 v[66:69], v[138:145], v[42:49], v[186:189]
	s_barrier
	s_add_u32 s70, s8, s69
	s_addc_u32 s71, s9, 0
	s_add_i32 s68, s68, 0x20080
	s_mov_b32 m0, s43
	v_lshl_add_u64 v[18:19], s[70:71], 0, v[146:147]
	s_add_u32 s68, s8, s68
	global_load_lds_dwordx4 v[18:19], off
	v_lshl_add_u64 v[18:19], s[70:71], 0, v[148:149]
	s_mov_b32 m0, s44
	s_addc_u32 s69, s9, 0
	s_addk_i32 s24, 0x80
	global_load_lds_dwordx4 v[18:19], off
	v_lshl_add_u64 v[18:19], s[68:69], 0, v[146:147]
	s_mov_b32 m0, s47
	s_add_u32 s24, s8, s24
	global_load_lds_dwordx4 v[18:19], off
	v_lshl_add_u64 v[18:19], s[68:69], 0, v[148:149]
	s_mov_b32 m0, s48
	s_addc_u32 s25, s9, 0
	global_load_lds_dwordx4 v[18:19], off
	v_lshl_add_u64 v[18:19], s[24:25], 0, v[146:147]
	s_mov_b32 m0, s45
	s_nop 0
	global_load_lds_dwordx4 v[18:19], off
	v_lshl_add_u64 v[18:19], s[24:25], 0, v[148:149]
	s_mov_b32 m0, s46
	s_nop 0
	global_load_lds_dwordx4 v[18:19], off
	ds_read_b128 v[158:161], v153 offset:49152
	ds_read_b128 v[162:165], v153 offset:50176
	ds_read_b128 v[166:169], v153 offset:51200
	ds_read_b128 v[170:173], v153 offset:52224
	ds_read_b128 v[174:177], v153 offset:53248
	ds_read_b128 v[178:181], v153 offset:54272
	ds_read_b128 v[182:185], v153 offset:55296
	ds_read_b128 v[186:189], v153 offset:56320
	s_waitcnt vmcnt(8)
	s_waitcnt lgkmcnt(0)
	s_barrier
	s_waitcnt lgkmcnt(0)
	v_mfma_f32_16x16x128_f8f6f4 v[62:65], v[2:9], v[158:165], v[62:65]
	v_mfma_f32_16x16x128_f8f6f4 v[58:61], v[10:17], v[158:165], v[58:61]
	v_mfma_f32_16x16x128_f8f6f4 v[50:53], v[2:9], v[166:173], v[50:53]
	v_mfma_f32_16x16x128_f8f6f4 v[42:45], v[10:17], v[166:173], v[190:193]
	v_mfma_f32_16x16x128_f8f6f4 v[34:37], v[2:9], v[174:181], v[194:197]
	v_mfma_f32_16x16x128_f8f6f4 v[26:29], v[10:17], v[174:181], v[198:201]
	v_mfma_f32_16x16x128_f8f6f4 v[18:21], v[2:9], v[182:189], v[202:205]
	v_mfma_f32_16x16x128_f8f6f4 v[10:13], v[10:17], v[182:189], v[222:225]
	v_mfma_f32_16x16x128_f8f6f4 v[54:57], v[130:137], v[158:165], v[54:57]
	v_mfma_f32_16x16x128_f8f6f4 v[46:49], v[138:145], v[158:165], v[226:229]
	v_mfma_f32_16x16x128_f8f6f4 v[38:41], v[130:137], v[166:173], v[230:233]
	v_mfma_f32_16x16x128_f8f6f4 v[30:33], v[138:145], v[166:173], v[234:237]
	v_mfma_f32_16x16x128_f8f6f4 v[22:25], v[130:137], v[174:181], v[238:241]
	v_mfma_f32_16x16x128_f8f6f4 v[14:17], v[138:145], v[174:181], v[242:245]
	v_mfma_f32_16x16x128_f8f6f4 v[6:9], v[130:137], v[182:189], v[246:249]
	v_mfma_f32_16x16x128_f8f6f4 v[2:5], v[138:145], v[182:189], v[250:253]
	s_barrier
	s_add_i32 s66, s66, 2
	s_addk_i32 s67, 0x100
	s_cmp_gt_u32 s66, 5
	s_cbranch_scc0 .LBB0_2652
	s_and_b64 vcc, exec, s[12:13]
	s_cbranch_vccz .LBB0_2655
	s_barrier
